# static s_setprio 1 for waves 4-7 at entry, all per-block s_setprio flips deleted, vacuous post-barrier lgkmcnt(0) deleted in all 11 K-loops
# speedup vs baseline: 1.0185x; 1.0167x over previous
_Z10fwd_kernel6Params:
	s_mov_b64 s[88:89], s[0:1]
	v_readfirstlane_b32 s3, v0
	s_nop 3
	s_lshr_b32 s3, s3, 6
	s_cmp_ge_u32 s3, 4
	s_cbranch_scc0 .Lprio_done
	s_setprio 1
.Lprio_done:
	s_load_dword s74, s[0:1], 0x98
	s_add_u32 s0, s88, 0x98
	s_addc_u32 s1, s89, 0
	v_lshl_add_u32 v1, v0, 2, 0
	v_writelane_b32 v253, s0, 0
	v_add_u32_e32 v1, 0x24000, v1
	v_mov_b32_e32 v2, 0
	s_mov_b32 s87, s2
	v_writelane_b32 v253, s1, 1
	ds_write2st64_b32 v1, v2, v2 offset1:8
	ds_write2st64_b32 v1, v2, v2 offset0:16 offset1:24
	v_or_b32_e32 v1, 0x800, v0
	s_mov_b64 s[0:1], -1
	s_and_saveexec_b64 s[2:3], s[0:1]
	v_lshl_add_u32 v3, v1, 2, 0
	v_add_u32_e32 v3, 0x24000, v3
	ds_write_b32 v3, v2
	s_or_b64 exec, exec, s[2:3]
	s_and_saveexec_b64 s[2:3], s[0:1]
	s_add_i32 s0, 0, 0x24000
	v_lshl_add_u32 v1, v1, 2, s0
	v_mov_b32_e32 v2, 0
	ds_write_b32 v1, v2 offset:2048
	s_or_b64 exec, exec, s[2:3]
	s_load_dwordx2 s[0:1], s[88:89], 0x88
	v_or_b32_e32 v1, 0xc00, v0
	v_cmp_gt_u32_e64 s[2:3], 7, 6
	v_cmp_gt_u32_e64 s[6:7], 7, 5
	s_and_saveexec_b64 s[4:5], s[6:7]
	v_lshl_add_u32 v2, v1, 2, 0
	v_add_u32_e32 v2, 0x24000, v2
	v_mov_b32_e32 v3, 0
	ds_write_b32 v2, v3
	s_or_b64 exec, exec, s[4:5]
	s_load_dwordx2 s[50:51], s[88:89], 0x90
	s_and_saveexec_b64 s[4:5], s[2:3]
	s_add_i32 s2, 0, 0x24000
	v_lshl_add_u32 v1, v1, 2, s2
	v_mov_b32_e32 v2, 0
	ds_write_b32 v1, v2 offset:2048
	s_or_b64 exec, exec, s[4:5]
	s_waitcnt lgkmcnt(0)
	s_barrier
	s_add_u32 s26, s0, 0x4000
	s_getreg_b32 s2, hwreg(HW_REG_XCC_ID, 0, 4)
	s_addc_u32 s27, s1, 0
	s_and_b32 s33, s2, 15
	v_cmp_eq_u32_e64 s[4:5], 0, v0
	s_mov_b64 s[2:3], exec
	s_nop 0
	v_writelane_b32 v253, s4, 2
	s_nop 1
	v_writelane_b32 v253, s5, 3
	s_and_b64 s[4:5], s[2:3], s[4:5]
	s_mov_b64 exec, s[4:5]
	s_cbranch_execz .LBB0_11
	s_mov_b64 s[4:5], exec
	v_mbcnt_lo_u32_b32 v1, s4, 0
	v_mbcnt_hi_u32_b32 v1, s5, v1
	v_cmp_eq_u32_e32 vcc, 0, v1
	s_and_b64 s[6:7], exec, vcc
	s_mov_b64 exec, s[6:7]
	s_cbranch_execz .LBB0_11
	s_lshl_b32 s6, s33, 8
	s_bcnt1_i32_b64 s4, s[4:5]
	v_mov_b32_e32 v1, s6
	v_mov_b32_e32 v2, s4
	global_atomic_add v1, v2, s[26:27] offset:1024

.LBB0_200:
	s_waitcnt lgkmcnt(0)
	s_barrier
	v_mfma_f32_16x16x32_bf16 v[72:75], v[156:159], v[196:199], v[72:75]
	v_mfma_f32_16x16x32_bf16 v[68:71], v[164:167], v[196:199], v[68:71]
	v_mfma_f32_16x16x32_bf16 v[54:57], v[156:159], v[188:191], v[54:57]
	v_mfma_f32_16x16x32_bf16 v[50:53], v[164:167], v[188:191], v[50:53]
	v_mfma_f32_16x16x32_bf16 v[38:41], v[156:159], v[180:183], v[38:41]
	v_mfma_f32_16x16x32_bf16 v[34:37], v[164:167], v[180:183], v[34:37]
	v_mfma_f32_16x16x32_bf16 v[22:25], v[156:159], v[172:175], v[22:25]
	v_mfma_f32_16x16x32_bf16 v[18:21], v[164:167], v[172:175], v[18:21]
	v_mfma_f32_16x16x32_bf16 v[72:75], v[160:163], v[200:203], v[72:75]
	v_mfma_f32_16x16x32_bf16 v[68:71], v[168:171], v[200:203], v[68:71]
	v_mfma_f32_16x16x32_bf16 v[54:57], v[160:163], v[192:195], v[54:57]
	v_mfma_f32_16x16x32_bf16 v[50:53], v[168:171], v[192:195], v[50:53]
	v_mfma_f32_16x16x32_bf16 v[38:41], v[160:163], v[184:187], v[38:41]
	v_mfma_f32_16x16x32_bf16 v[34:37], v[168:171], v[184:187], v[34:37]
	v_mfma_f32_16x16x32_bf16 v[22:25], v[160:163], v[176:179], v[22:25]
	v_mfma_f32_16x16x32_bf16 v[18:21], v[168:171], v[176:179], v[18:21]
	v_mfma_f32_16x16x32_bf16 v[62:65], v[140:143], v[196:199], v[62:65]
	v_mfma_f32_16x16x32_bf16 v[58:61], v[148:151], v[196:199], v[58:61]
	v_mfma_f32_16x16x32_bf16 v[46:49], v[140:143], v[188:191], v[46:49]
	v_mfma_f32_16x16x32_bf16 v[42:45], v[148:151], v[188:191], v[42:45]
	v_mfma_f32_16x16x32_bf16 v[30:33], v[140:143], v[180:183], v[30:33]
	v_mfma_f32_16x16x32_bf16 v[26:29], v[148:151], v[180:183], v[26:29]
	v_mfma_f32_16x16x32_bf16 v[14:17], v[140:143], v[172:175], v[14:17]
	v_mfma_f32_16x16x32_bf16 v[10:13], v[148:151], v[172:175], v[10:13]
	v_mfma_f32_16x16x32_bf16 v[62:65], v[144:147], v[200:203], v[62:65]
	v_mfma_f32_16x16x32_bf16 v[58:61], v[152:155], v[200:203], v[58:61]
	v_mfma_f32_16x16x32_bf16 v[46:49], v[144:147], v[192:195], v[46:49]
	v_mfma_f32_16x16x32_bf16 v[42:45], v[152:155], v[192:195], v[42:45]
	v_mfma_f32_16x16x32_bf16 v[30:33], v[144:147], v[184:187], v[30:33]
	v_mfma_f32_16x16x32_bf16 v[26:29], v[152:155], v[184:187], v[26:29]
	v_mfma_f32_16x16x32_bf16 v[14:17], v[144:147], v[176:179], v[14:17]
	v_mfma_f32_16x16x32_bf16 v[10:13], v[152:155], v[176:179], v[10:13]
	s_barrier
	s_add_i32 s10, 0, 0x18000
	v_add_u32_e32 v66, s10, v219
	s_add_i32 s11, 0, 0x1c000
	ds_read_b128 v[140:143], v66
	ds_read_b128 v[144:147], v66 offset:1024
	ds_read_b128 v[148:151], v66 offset:2048
	ds_read_b128 v[152:155], v66 offset:3072
	v_add_u32_e32 v66, s11, v219
	ds_read_b128 v[156:159], v66
	ds_read_b128 v[160:163], v66 offset:1024
	ds_read_b128 v[164:167], v66 offset:2048
	ds_read_b128 v[168:171], v66 offset:3072
	s_add_u32 s8, s58, 0x40000
	s_addc_u32 s9, s59, 0
	s_mov_b32 m0, s91
	v_lshl_add_u64 v[246:247], s[8:9], 0, v[208:209]
	ds_read_b128 v[172:175], v244 offset:32768
	ds_read_b128 v[176:179], v244 offset:33792
	ds_read_b128 v[180:183], v244 offset:34816
	ds_read_b128 v[184:187], v244 offset:35840
	ds_read_b128 v[188:191], v244 offset:36864
	ds_read_b128 v[192:195], v244 offset:37888
	ds_read_b128 v[196:199], v244 offset:38912
	ds_read_b128 v[200:203], v244 offset:39936
	global_load_lds_dwordx4 v[246:247], off
	v_lshl_add_u64 v[246:247], s[8:9], 0, v[212:213]
	s_mov_b32 m0, s92
	s_nop 0
	global_load_lds_dwordx4 v[246:247], off
	s_waitcnt vmcnt(8)
	s_waitcnt lgkmcnt(0)
	s_barrier
	v_mfma_f32_16x16x32_bf16 v[136:139], v[140:143], v[172:175], v[136:139]
	v_mfma_f32_16x16x32_bf16 v[132:135], v[148:151], v[172:175], v[132:135]
	v_mfma_f32_16x16x32_bf16 v[120:123], v[140:143], v[180:183], v[120:123]
	v_mfma_f32_16x16x32_bf16 v[116:119], v[148:151], v[180:183], v[116:119]
	v_mfma_f32_16x16x32_bf16 v[104:107], v[140:143], v[188:191], v[104:107]
	v_mfma_f32_16x16x32_bf16 v[100:103], v[148:151], v[188:191], v[100:103]
	v_mfma_f32_16x16x32_bf16 v[88:91], v[140:143], v[196:199], v[88:91]
	v_mfma_f32_16x16x32_bf16 v[84:87], v[148:151], v[196:199], v[84:87]
	v_mfma_f32_16x16x32_bf16 v[136:139], v[144:147], v[176:179], v[136:139]
	v_mfma_f32_16x16x32_bf16 v[132:135], v[152:155], v[176:179], v[132:135]
	v_mfma_f32_16x16x32_bf16 v[120:123], v[144:147], v[184:187], v[120:123]
	v_mfma_f32_16x16x32_bf16 v[116:119], v[152:155], v[184:187], v[116:119]
	v_mfma_f32_16x16x32_bf16 v[104:107], v[144:147], v[192:195], v[104:107]
	v_mfma_f32_16x16x32_bf16 v[100:103], v[152:155], v[192:195], v[100:103]
	v_mfma_f32_16x16x32_bf16 v[88:91], v[144:147], v[200:203], v[88:91]
	v_mfma_f32_16x16x32_bf16 v[84:87], v[152:155], v[200:203], v[84:87]
	v_mfma_f32_16x16x32_bf16 v[128:131], v[156:159], v[172:175], v[128:131]
	v_mfma_f32_16x16x32_bf16 v[124:127], v[164:167], v[172:175], v[124:127]
	v_mfma_f32_16x16x32_bf16 v[112:115], v[156:159], v[180:183], v[112:115]
	v_mfma_f32_16x16x32_bf16 v[108:111], v[164:167], v[180:183], v[108:111]
	v_mfma_f32_16x16x32_bf16 v[96:99], v[156:159], v[188:191], v[96:99]
	v_mfma_f32_16x16x32_bf16 v[92:95], v[164:167], v[188:191], v[92:95]
	v_mfma_f32_16x16x32_bf16 v[80:83], v[156:159], v[196:199], v[80:83]
	v_mfma_f32_16x16x32_bf16 v[76:79], v[164:167], v[196:199], v[76:79]
	v_mfma_f32_16x16x32_bf16 v[128:131], v[160:163], v[176:179], v[128:131]
	v_mfma_f32_16x16x32_bf16 v[124:127], v[168:171], v[176:179], v[124:127]
	v_mfma_f32_16x16x32_bf16 v[112:115], v[160:163], v[184:187], v[112:115]
	v_mfma_f32_16x16x32_bf16 v[108:111], v[168:171], v[184:187], v[108:111]
	v_mfma_f32_16x16x32_bf16 v[96:99], v[160:163], v[192:195], v[96:99]
	v_mfma_f32_16x16x32_bf16 v[92:95], v[168:171], v[192:195], v[92:95]
	v_mfma_f32_16x16x32_bf16 v[80:83], v[160:163], v[200:203], v[80:83]
	v_mfma_f32_16x16x32_bf16 v[76:79], v[168:171], v[200:203], v[76:79]
	s_barrier
	s_add_i32 s8, s10, s84
	v_lshl_add_u64 v[234:235], v[234:235], 0, s[60:61]
	s_mov_b32 m0, s8
	ds_read_b128 v[172:175], v244 offset:49152
	ds_read_b128 v[176:179], v244 offset:50176
	ds_read_b128 v[180:183], v244 offset:51200
	ds_read_b128 v[184:187], v244 offset:52224
	ds_read_b128 v[188:191], v244 offset:53248
	ds_read_b128 v[192:195], v244 offset:54272
	ds_read_b128 v[196:199], v244 offset:55296
	ds_read_b128 v[200:203], v244 offset:56320
	global_load_lds_dwordx4 v[234:235], off
	s_add_i32 m0, s8, 0x2000
	s_add_u32 s8, s36, 0x40080
	v_lshl_add_u64 v[232:233], v[232:233], 0, s[60:61]
	s_addc_u32 s9, s37, 0
	s_add_i32 s10, s11, s84
	global_load_lds_dwordx4 v[232:233], off
	v_lshl_add_u64 v[232:233], s[8:9], 0, v[210:211]
	s_mov_b32 m0, s10
	v_lshl_add_u64 v[228:229], v[228:229], 0, s[60:61]
	global_load_lds_dwordx4 v[232:233], off
	v_lshl_add_u64 v[232:233], s[8:9], 0, v[214:215]
	s_add_i32 m0, s10, 0x2000
	s_nop 0
	global_load_lds_dwordx4 v[232:233], off
	s_mov_b32 m0, s96
	s_nop 0
	global_load_lds_dwordx4 v[228:229], off
	v_lshl_add_u64 v[228:229], v[230:231], 0, s[60:61]
	s_mov_b32 m0, s97
	s_nop 0
	global_load_lds_dwordx4 v[228:229], off
	s_waitcnt vmcnt(8)
	s_waitcnt lgkmcnt(0)
	s_barrier
	v_mfma_f32_16x16x32_bf16 v[72:75], v[140:143], v[172:175], v[72:75]
	v_mfma_f32_16x16x32_bf16 v[68:71], v[148:151], v[172:175], v[68:71]
	v_mfma_f32_16x16x32_bf16 v[54:57], v[140:143], v[180:183], v[54:57]
	v_mfma_f32_16x16x32_bf16 v[50:53], v[148:151], v[180:183], v[50:53]
	v_mfma_f32_16x16x32_bf16 v[38:41], v[140:143], v[188:191], v[38:41]
	v_mfma_f32_16x16x32_bf16 v[34:37], v[148:151], v[188:191], v[34:37]
	v_mfma_f32_16x16x32_bf16 v[22:25], v[140:143], v[196:199], v[22:25]
	v_mfma_f32_16x16x32_bf16 v[18:21], v[148:151], v[196:199], v[18:21]
	v_mfma_f32_16x16x32_bf16 v[72:75], v[144:147], v[176:179], v[72:75]
	v_mfma_f32_16x16x32_bf16 v[68:71], v[152:155], v[176:179], v[68:71]
	v_mfma_f32_16x16x32_bf16 v[54:57], v[144:147], v[184:187], v[54:57]
	v_mfma_f32_16x16x32_bf16 v[50:53], v[152:155], v[184:187], v[50:53]
	v_mfma_f32_16x16x32_bf16 v[38:41], v[144:147], v[192:195], v[38:41]
	v_mfma_f32_16x16x32_bf16 v[34:37], v[152:155], v[192:195], v[34:37]
	v_mfma_f32_16x16x32_bf16 v[22:25], v[144:147], v[200:203], v[22:25]
	v_mfma_f32_16x16x32_bf16 v[18:21], v[152:155], v[200:203], v[18:21]
	v_mfma_f32_16x16x32_bf16 v[62:65], v[156:159], v[172:175], v[62:65]
	v_mfma_f32_16x16x32_bf16 v[58:61], v[164:167], v[172:175], v[58:61]
	v_mfma_f32_16x16x32_bf16 v[46:49], v[156:159], v[180:183], v[46:49]
	v_mfma_f32_16x16x32_bf16 v[42:45], v[164:167], v[180:183], v[42:45]
	v_mfma_f32_16x16x32_bf16 v[30:33], v[156:159], v[188:191], v[30:33]
	v_mfma_f32_16x16x32_bf16 v[26:29], v[164:167], v[188:191], v[26:29]
	v_mfma_f32_16x16x32_bf16 v[14:17], v[156:159], v[196:199], v[14:17]
	v_mfma_f32_16x16x32_bf16 v[10:13], v[164:167], v[196:199], v[10:13]
	v_mfma_f32_16x16x32_bf16 v[62:65], v[160:163], v[176:179], v[62:65]
	v_mfma_f32_16x16x32_bf16 v[58:61], v[168:171], v[176:179], v[58:61]
	v_mfma_f32_16x16x32_bf16 v[46:49], v[160:163], v[184:187], v[46:49]
	v_mfma_f32_16x16x32_bf16 v[42:45], v[168:171], v[184:187], v[42:45]
	v_mfma_f32_16x16x32_bf16 v[30:33], v[160:163], v[192:195], v[30:33]
	v_mfma_f32_16x16x32_bf16 v[26:29], v[168:171], v[192:195], v[26:29]
	v_mfma_f32_16x16x32_bf16 v[14:17], v[160:163], v[200:203], v[14:17]
	v_mfma_f32_16x16x32_bf16 v[10:13], v[168:171], v[200:203], v[10:13]
	s_barrier
	s_add_i32 s69, s69, 2
	s_add_u32 s38, s38, 0x100
	s_addc_u32 s39, s39, 0
	s_cmp_gt_u32 s69, 13
	s_cbranch_scc1 .LBB0_209

.LBB0_205:
	s_add_u32 s8, s34, s38
	s_addc_u32 s9, s35, s39
	s_add_u32 s8, s8, 0x100
	s_addc_u32 s9, s9, 0
	s_add_u32 s10, s67, s38
	s_addc_u32 s11, s68, s39
	s_waitcnt lgkmcnt(0)
	s_cmpk_eq_i32 s38, 0x700
	s_cselect_b32 s59, s55, s9
	s_cselect_b32 s58, s54, s8
	s_cselect_b32 s37, s57, s11
	s_cselect_b32 s36, s56, s10
	s_barrier
	v_mfma_f32_16x16x32_bf16 v[136:139], v[156:159], v[196:199], v[136:139]
	v_mfma_f32_16x16x32_bf16 v[132:135], v[164:167], v[196:199], v[132:135]
	v_mfma_f32_16x16x32_bf16 v[120:123], v[156:159], v[188:191], v[120:123]
	v_mfma_f32_16x16x32_bf16 v[116:119], v[164:167], v[188:191], v[116:119]
	v_mfma_f32_16x16x32_bf16 v[104:107], v[156:159], v[180:183], v[104:107]
	v_mfma_f32_16x16x32_bf16 v[100:103], v[164:167], v[180:183], v[100:103]
	v_mfma_f32_16x16x32_bf16 v[88:91], v[156:159], v[172:175], v[88:91]
	v_mfma_f32_16x16x32_bf16 v[84:87], v[164:167], v[172:175], v[84:87]
	v_mfma_f32_16x16x32_bf16 v[136:139], v[160:163], v[200:203], v[136:139]
	v_mfma_f32_16x16x32_bf16 v[132:135], v[168:171], v[200:203], v[132:135]
	v_mfma_f32_16x16x32_bf16 v[120:123], v[160:163], v[192:195], v[120:123]
	v_mfma_f32_16x16x32_bf16 v[116:119], v[168:171], v[192:195], v[116:119]
	v_mfma_f32_16x16x32_bf16 v[104:107], v[160:163], v[184:187], v[104:107]
	v_mfma_f32_16x16x32_bf16 v[100:103], v[168:171], v[184:187], v[100:103]
	v_mfma_f32_16x16x32_bf16 v[88:91], v[160:163], v[176:179], v[88:91]
	v_mfma_f32_16x16x32_bf16 v[84:87], v[168:171], v[176:179], v[84:87]
	v_mfma_f32_16x16x32_bf16 v[128:131], v[140:143], v[196:199], v[128:131]
	v_mfma_f32_16x16x32_bf16 v[124:127], v[148:151], v[196:199], v[124:127]
	v_mfma_f32_16x16x32_bf16 v[112:115], v[140:143], v[188:191], v[112:115]
	v_mfma_f32_16x16x32_bf16 v[108:111], v[148:151], v[188:191], v[108:111]
	v_mfma_f32_16x16x32_bf16 v[96:99], v[140:143], v[180:183], v[96:99]
	v_mfma_f32_16x16x32_bf16 v[92:95], v[148:151], v[180:183], v[92:95]
	v_mfma_f32_16x16x32_bf16 v[80:83], v[140:143], v[172:175], v[80:83]
	v_mfma_f32_16x16x32_bf16 v[76:79], v[148:151], v[172:175], v[76:79]
	v_mfma_f32_16x16x32_bf16 v[128:131], v[144:147], v[200:203], v[128:131]
	v_mfma_f32_16x16x32_bf16 v[124:127], v[152:155], v[200:203], v[124:127]
	v_mfma_f32_16x16x32_bf16 v[112:115], v[144:147], v[192:195], v[112:115]
	v_mfma_f32_16x16x32_bf16 v[108:111], v[152:155], v[192:195], v[108:111]
	v_mfma_f32_16x16x32_bf16 v[96:99], v[144:147], v[184:187], v[96:99]
	v_mfma_f32_16x16x32_bf16 v[92:95], v[152:155], v[184:187], v[92:95]
	v_mfma_f32_16x16x32_bf16 v[80:83], v[144:147], v[176:179], v[80:83]
	v_mfma_f32_16x16x32_bf16 v[76:79], v[152:155], v[176:179], v[76:79]
	s_barrier
	s_mov_b32 m0, s86
	v_lshl_add_u64 v[234:235], s[36:37], 0, v[210:211]
	s_add_u32 s8, s36, 0x40000
	ds_read_b128 v[196:199], v244 offset:16384
	ds_read_b128 v[200:203], v244 offset:17408
	ds_read_b128 v[188:191], v244 offset:18432
	ds_read_b128 v[192:195], v244 offset:19456
	ds_read_b128 v[180:183], v244 offset:20480
	ds_read_b128 v[184:187], v244 offset:21504
	ds_read_b128 v[172:175], v244 offset:22528
	ds_read_b128 v[176:179], v244 offset:23552
	global_load_lds_dwordx4 v[234:235], off
	v_lshl_add_u64 v[232:233], s[36:37], 0, v[214:215]
	s_mov_b32 m0, s87
	s_addc_u32 s9, s37, 0
	global_load_lds_dwordx4 v[232:233], off
	v_lshl_add_u64 v[228:229], s[8:9], 0, v[210:211]
	s_mov_b32 m0, s88
	v_lshl_add_u64 v[230:231], s[58:59], 0, v[212:213]
	global_load_lds_dwordx4 v[228:229], off
	v_lshl_add_u64 v[228:229], s[8:9], 0, v[214:215]
	s_mov_b32 m0, s89
	s_mov_b64 s[26:27], -1
	global_load_lds_dwordx4 v[228:229], off
	v_lshl_add_u64 v[228:229], s[58:59], 0, v[208:209]
	s_mov_b32 m0, s85
	s_and_b64 vcc, exec, s[64:65]
	global_load_lds_dwordx4 v[228:229], off
	s_mov_b32 m0, s90
	s_nop 0
	global_load_lds_dwordx4 v[230:231], off
	s_cbranch_vccz .LBB0_207
	s_waitcnt vmcnt(8)
	s_mov_b64 s[26:27], 0

.LBB0_483:
	s_waitcnt lgkmcnt(0)
	s_xor_b64 s[84:85], s[36:37], -1
	s_barrier
	v_mfma_f32_16x16x32_bf16 v[62:65], v[148:151], v[188:191], v[62:65]
	v_mfma_f32_16x16x32_bf16 v[58:61], v[156:159], v[188:191], v[58:61]
	v_mfma_f32_16x16x32_bf16 v[46:49], v[148:151], v[180:183], v[46:49]
	v_mfma_f32_16x16x32_bf16 v[42:45], v[156:159], v[180:183], v[42:45]
	v_mfma_f32_16x16x32_bf16 v[30:33], v[148:151], v[172:175], v[30:33]
	v_mfma_f32_16x16x32_bf16 v[26:29], v[156:159], v[172:175], v[26:29]
	v_mfma_f32_16x16x32_bf16 v[14:17], v[148:151], v[164:167], v[14:17]
	v_mfma_f32_16x16x32_bf16 v[10:13], v[156:159], v[164:167], v[10:13]
	v_mfma_f32_16x16x32_bf16 v[62:65], v[152:155], v[192:195], v[62:65]
	v_mfma_f32_16x16x32_bf16 v[58:61], v[160:163], v[192:195], v[58:61]
	v_mfma_f32_16x16x32_bf16 v[46:49], v[152:155], v[184:187], v[46:49]
	v_mfma_f32_16x16x32_bf16 v[42:45], v[160:163], v[184:187], v[42:45]
	v_mfma_f32_16x16x32_bf16 v[30:33], v[152:155], v[176:179], v[30:33]
	v_mfma_f32_16x16x32_bf16 v[26:29], v[160:163], v[176:179], v[26:29]
	v_mfma_f32_16x16x32_bf16 v[14:17], v[152:155], v[168:171], v[14:17]
	v_mfma_f32_16x16x32_bf16 v[10:13], v[160:163], v[168:171], v[10:13]
	v_mfma_f32_16x16x32_bf16 v[54:57], v[132:135], v[188:191], v[54:57]
	v_mfma_f32_16x16x32_bf16 v[50:53], v[140:143], v[188:191], v[50:53]
	v_mfma_f32_16x16x32_bf16 v[38:41], v[132:135], v[180:183], v[38:41]
	v_mfma_f32_16x16x32_bf16 v[34:37], v[140:143], v[180:183], v[34:37]
	v_mfma_f32_16x16x32_bf16 v[22:25], v[132:135], v[172:175], v[22:25]
	v_mfma_f32_16x16x32_bf16 v[18:21], v[140:143], v[172:175], v[18:21]
	v_mfma_f32_16x16x32_bf16 v[6:9], v[132:135], v[164:167], v[6:9]
	v_mfma_f32_16x16x32_bf16 v[2:5], v[140:143], v[164:167], v[2:5]
	v_mfma_f32_16x16x32_bf16 v[54:57], v[136:139], v[192:195], v[54:57]
	v_mfma_f32_16x16x32_bf16 v[50:53], v[144:147], v[192:195], v[50:53]
	v_mfma_f32_16x16x32_bf16 v[38:41], v[136:139], v[184:187], v[38:41]
	v_mfma_f32_16x16x32_bf16 v[34:37], v[144:147], v[184:187], v[34:37]
	v_mfma_f32_16x16x32_bf16 v[22:25], v[136:139], v[176:179], v[22:25]
	v_mfma_f32_16x16x32_bf16 v[18:21], v[144:147], v[176:179], v[18:21]
	v_mfma_f32_16x16x32_bf16 v[6:9], v[136:139], v[168:171], v[6:9]
	v_mfma_f32_16x16x32_bf16 v[2:5], v[144:147], v[168:171], v[2:5]
	s_barrier
	s_add_i32 s10, 0, 0x18000
	v_add_u32_e32 v66, s10, v211
	s_add_i32 s11, 0, 0x1c000
	ds_read_b128 v[132:135], v66
	ds_read_b128 v[136:139], v66 offset:1024
	ds_read_b128 v[140:143], v66 offset:2048
	ds_read_b128 v[144:147], v66 offset:3072
	v_add_u32_e32 v66, s11, v211
	ds_read_b128 v[148:151], v66
	ds_read_b128 v[152:155], v66 offset:1024
	ds_read_b128 v[156:159], v66 offset:2048
	ds_read_b128 v[160:163], v66 offset:3072
	s_add_u32 s8, s86, 0x40000
	s_addc_u32 s9, s87, 0
	s_mov_b32 m0, s97
	v_lshl_add_u64 v[230:231], s[8:9], 0, v[198:199]
	ds_read_b128 v[164:167], v228 offset:32768
	ds_read_b128 v[168:171], v228 offset:33792
	ds_read_b128 v[172:175], v228 offset:34816
	ds_read_b128 v[176:179], v228 offset:35840
	ds_read_b128 v[180:183], v228 offset:36864
	ds_read_b128 v[184:187], v228 offset:37888
	ds_read_b128 v[188:191], v228 offset:38912
	ds_read_b128 v[192:195], v228 offset:39936
	global_load_lds_dwordx4 v[230:231], off
	v_lshl_add_u64 v[230:231], s[8:9], 0, v[202:203]
	s_mov_b32 m0, s64
	s_nop 0
	global_load_lds_dwordx4 v[230:231], off
	s_waitcnt vmcnt(8)
	s_waitcnt lgkmcnt(0)
	s_barrier
	v_mfma_f32_16x16x32_bf16 v[128:131], v[132:135], v[164:167], v[128:131]
	v_mfma_f32_16x16x32_bf16 v[124:127], v[140:143], v[164:167], v[124:127]
	v_mfma_f32_16x16x32_bf16 v[112:115], v[132:135], v[172:175], v[112:115]
	v_mfma_f32_16x16x32_bf16 v[108:111], v[140:143], v[172:175], v[108:111]
	v_mfma_f32_16x16x32_bf16 v[96:99], v[132:135], v[180:183], v[96:99]
	v_mfma_f32_16x16x32_bf16 v[92:95], v[140:143], v[180:183], v[92:95]
	v_mfma_f32_16x16x32_bf16 v[80:83], v[132:135], v[188:191], v[80:83]
	v_mfma_f32_16x16x32_bf16 v[76:79], v[140:143], v[188:191], v[76:79]
	v_mfma_f32_16x16x32_bf16 v[128:131], v[136:139], v[168:171], v[128:131]
	v_mfma_f32_16x16x32_bf16 v[124:127], v[144:147], v[168:171], v[124:127]
	v_mfma_f32_16x16x32_bf16 v[112:115], v[136:139], v[176:179], v[112:115]
	v_mfma_f32_16x16x32_bf16 v[108:111], v[144:147], v[176:179], v[108:111]
	v_mfma_f32_16x16x32_bf16 v[96:99], v[136:139], v[184:187], v[96:99]
	v_mfma_f32_16x16x32_bf16 v[92:95], v[144:147], v[184:187], v[92:95]
	v_mfma_f32_16x16x32_bf16 v[80:83], v[136:139], v[192:195], v[80:83]
	v_mfma_f32_16x16x32_bf16 v[76:79], v[144:147], v[192:195], v[76:79]
	v_mfma_f32_16x16x32_bf16 v[120:123], v[148:151], v[164:167], v[120:123]
	v_mfma_f32_16x16x32_bf16 v[116:119], v[156:159], v[164:167], v[116:119]
	v_mfma_f32_16x16x32_bf16 v[104:107], v[148:151], v[172:175], v[104:107]
	v_mfma_f32_16x16x32_bf16 v[100:103], v[156:159], v[172:175], v[100:103]
	v_mfma_f32_16x16x32_bf16 v[88:91], v[148:151], v[180:183], v[88:91]
	v_mfma_f32_16x16x32_bf16 v[84:87], v[156:159], v[180:183], v[84:87]
	v_mfma_f32_16x16x32_bf16 v[72:75], v[148:151], v[188:191], v[72:75]
	v_mfma_f32_16x16x32_bf16 v[68:71], v[156:159], v[188:191], v[68:71]
	v_mfma_f32_16x16x32_bf16 v[120:123], v[152:155], v[168:171], v[120:123]
	v_mfma_f32_16x16x32_bf16 v[116:119], v[160:163], v[168:171], v[116:119]
	v_mfma_f32_16x16x32_bf16 v[104:107], v[152:155], v[176:179], v[104:107]
	v_mfma_f32_16x16x32_bf16 v[100:103], v[160:163], v[176:179], v[100:103]
	v_mfma_f32_16x16x32_bf16 v[88:91], v[152:155], v[184:187], v[88:91]
	v_mfma_f32_16x16x32_bf16 v[84:87], v[160:163], v[184:187], v[84:87]
	v_mfma_f32_16x16x32_bf16 v[72:75], v[152:155], v[192:195], v[72:75]
	v_mfma_f32_16x16x32_bf16 v[68:71], v[160:163], v[192:195], v[68:71]
	s_barrier
	s_add_i32 s8, s10, s90
	v_lshl_add_u64 v[218:219], v[218:219], 0, s[60:61]
	s_mov_b32 m0, s8
	ds_read_b128 v[164:167], v228 offset:49152
	ds_read_b128 v[168:171], v228 offset:50176
	ds_read_b128 v[172:175], v228 offset:51200
	ds_read_b128 v[176:179], v228 offset:52224
	ds_read_b128 v[180:183], v228 offset:53248
	ds_read_b128 v[184:187], v228 offset:54272
	ds_read_b128 v[188:191], v228 offset:55296
	ds_read_b128 v[192:195], v228 offset:56320
	global_load_lds_dwordx4 v[218:219], off
	s_add_i32 m0, s8, 0x2000
	s_add_u32 s8, s58, 0x40080
	v_lshl_add_u64 v[216:217], v[216:217], 0, s[60:61]
	s_addc_u32 s9, s59, 0
	s_add_i32 s10, s11, s90
	global_load_lds_dwordx4 v[216:217], off
	v_lshl_add_u64 v[216:217], s[8:9], 0, v[200:201]
	s_mov_b32 m0, s10
	v_lshl_add_u64 v[212:213], v[212:213], 0, s[60:61]
	global_load_lds_dwordx4 v[216:217], off
	v_lshl_add_u64 v[216:217], s[8:9], 0, v[208:209]
	s_add_i32 m0, s10, 0x2000
	s_nop 0
	global_load_lds_dwordx4 v[216:217], off
	s_mov_b32 m0, s65
	s_nop 0
	global_load_lds_dwordx4 v[212:213], off
	v_lshl_add_u64 v[212:213], v[214:215], 0, s[60:61]
	s_mov_b32 m0, s68
	s_nop 0
	global_load_lds_dwordx4 v[212:213], off
	s_waitcnt vmcnt(8)
	s_waitcnt lgkmcnt(0)
	s_barrier
	v_mfma_f32_16x16x32_bf16 v[62:65], v[132:135], v[164:167], v[62:65]
	v_mfma_f32_16x16x32_bf16 v[58:61], v[140:143], v[164:167], v[58:61]
	v_mfma_f32_16x16x32_bf16 v[46:49], v[132:135], v[172:175], v[46:49]
	v_mfma_f32_16x16x32_bf16 v[42:45], v[140:143], v[172:175], v[42:45]
	v_mfma_f32_16x16x32_bf16 v[30:33], v[132:135], v[180:183], v[30:33]
	v_mfma_f32_16x16x32_bf16 v[26:29], v[140:143], v[180:183], v[26:29]
	v_mfma_f32_16x16x32_bf16 v[14:17], v[132:135], v[188:191], v[14:17]
	v_mfma_f32_16x16x32_bf16 v[10:13], v[140:143], v[188:191], v[10:13]
	v_mfma_f32_16x16x32_bf16 v[62:65], v[136:139], v[168:171], v[62:65]
	v_mfma_f32_16x16x32_bf16 v[58:61], v[144:147], v[168:171], v[58:61]
	v_mfma_f32_16x16x32_bf16 v[46:49], v[136:139], v[176:179], v[46:49]
	v_mfma_f32_16x16x32_bf16 v[42:45], v[144:147], v[176:179], v[42:45]
	v_mfma_f32_16x16x32_bf16 v[30:33], v[136:139], v[184:187], v[30:33]
	v_mfma_f32_16x16x32_bf16 v[26:29], v[144:147], v[184:187], v[26:29]
	v_mfma_f32_16x16x32_bf16 v[14:17], v[136:139], v[192:195], v[14:17]
	v_mfma_f32_16x16x32_bf16 v[10:13], v[144:147], v[192:195], v[10:13]
	v_mfma_f32_16x16x32_bf16 v[54:57], v[148:151], v[164:167], v[54:57]
	v_mfma_f32_16x16x32_bf16 v[50:53], v[156:159], v[164:167], v[50:53]
	v_mfma_f32_16x16x32_bf16 v[38:41], v[148:151], v[172:175], v[38:41]
	v_mfma_f32_16x16x32_bf16 v[34:37], v[156:159], v[172:175], v[34:37]
	v_mfma_f32_16x16x32_bf16 v[22:25], v[148:151], v[180:183], v[22:25]
	v_mfma_f32_16x16x32_bf16 v[18:21], v[156:159], v[180:183], v[18:21]
	v_mfma_f32_16x16x32_bf16 v[6:9], v[148:151], v[188:191], v[6:9]
	v_mfma_f32_16x16x32_bf16 v[2:5], v[156:159], v[188:191], v[2:5]
	v_mfma_f32_16x16x32_bf16 v[54:57], v[152:155], v[168:171], v[54:57]
	v_mfma_f32_16x16x32_bf16 v[50:53], v[160:163], v[168:171], v[50:53]
	v_mfma_f32_16x16x32_bf16 v[38:41], v[152:155], v[176:179], v[38:41]
	v_mfma_f32_16x16x32_bf16 v[34:37], v[160:163], v[176:179], v[34:37]
	v_mfma_f32_16x16x32_bf16 v[22:25], v[152:155], v[184:187], v[22:25]
	v_mfma_f32_16x16x32_bf16 v[18:21], v[160:163], v[184:187], v[18:21]
	v_mfma_f32_16x16x32_bf16 v[6:9], v[152:155], v[192:195], v[6:9]
	v_mfma_f32_16x16x32_bf16 v[2:5], v[160:163], v[192:195], v[2:5]
	s_barrier
	s_movk_i32 s8, 0x100
	s_mov_b64 s[36:37], 0
	s_mov_b64 s[58:59], -1
	s_and_b64 vcc, exec, s[84:85]
	s_cbranch_vccnz .LBB0_492

.LBB0_488:
	s_add_u32 s9, s9, 0x100
	s_addc_u32 s12, s10, 0
	s_and_b64 s[10:11], s[58:59], exec
	s_cselect_b32 s87, s47, s12
	s_cselect_b32 s86, s46, s9
	s_add_u32 s8, s52, s8
	s_addc_u32 s9, s53, 0
	s_add_u32 s10, s8, 0x100
	s_addc_u32 s11, s9, 0
	s_waitcnt lgkmcnt(0)
	s_and_b64 s[8:9], s[58:59], exec
	s_cselect_b32 s59, s49, s11
	s_cselect_b32 s58, s48, s10
	s_barrier
	v_mfma_f32_16x16x32_bf16 v[128:131], v[148:151], v[188:191], v[128:131]
	v_mfma_f32_16x16x32_bf16 v[124:127], v[156:159], v[188:191], v[124:127]
	v_mfma_f32_16x16x32_bf16 v[112:115], v[148:151], v[180:183], v[112:115]
	v_mfma_f32_16x16x32_bf16 v[108:111], v[156:159], v[180:183], v[108:111]
	v_mfma_f32_16x16x32_bf16 v[96:99], v[148:151], v[172:175], v[96:99]
	v_mfma_f32_16x16x32_bf16 v[92:95], v[156:159], v[172:175], v[92:95]
	v_mfma_f32_16x16x32_bf16 v[80:83], v[148:151], v[164:167], v[80:83]
	v_mfma_f32_16x16x32_bf16 v[76:79], v[156:159], v[164:167], v[76:79]
	v_mfma_f32_16x16x32_bf16 v[128:131], v[152:155], v[192:195], v[128:131]
	v_mfma_f32_16x16x32_bf16 v[124:127], v[160:163], v[192:195], v[124:127]
	v_mfma_f32_16x16x32_bf16 v[112:115], v[152:155], v[184:187], v[112:115]
	v_mfma_f32_16x16x32_bf16 v[108:111], v[160:163], v[184:187], v[108:111]
	v_mfma_f32_16x16x32_bf16 v[96:99], v[152:155], v[176:179], v[96:99]
	v_mfma_f32_16x16x32_bf16 v[92:95], v[160:163], v[176:179], v[92:95]
	v_mfma_f32_16x16x32_bf16 v[80:83], v[152:155], v[168:171], v[80:83]
	v_mfma_f32_16x16x32_bf16 v[76:79], v[160:163], v[168:171], v[76:79]
	v_mfma_f32_16x16x32_bf16 v[120:123], v[132:135], v[188:191], v[120:123]
	v_mfma_f32_16x16x32_bf16 v[116:119], v[140:143], v[188:191], v[116:119]
	v_mfma_f32_16x16x32_bf16 v[104:107], v[132:135], v[180:183], v[104:107]
	v_mfma_f32_16x16x32_bf16 v[100:103], v[140:143], v[180:183], v[100:103]
	v_mfma_f32_16x16x32_bf16 v[88:91], v[132:135], v[172:175], v[88:91]
	v_mfma_f32_16x16x32_bf16 v[84:87], v[140:143], v[172:175], v[84:87]
	v_mfma_f32_16x16x32_bf16 v[72:75], v[132:135], v[164:167], v[72:75]
	v_mfma_f32_16x16x32_bf16 v[68:71], v[140:143], v[164:167], v[68:71]
	v_mfma_f32_16x16x32_bf16 v[120:123], v[136:139], v[192:195], v[120:123]
	v_mfma_f32_16x16x32_bf16 v[116:119], v[144:147], v[192:195], v[116:119]
	v_mfma_f32_16x16x32_bf16 v[104:107], v[136:139], v[184:187], v[104:107]
	v_mfma_f32_16x16x32_bf16 v[100:103], v[144:147], v[184:187], v[100:103]
	v_mfma_f32_16x16x32_bf16 v[88:91], v[136:139], v[176:179], v[88:91]
	v_mfma_f32_16x16x32_bf16 v[84:87], v[144:147], v[176:179], v[84:87]
	v_mfma_f32_16x16x32_bf16 v[72:75], v[136:139], v[168:171], v[72:75]
	v_mfma_f32_16x16x32_bf16 v[68:71], v[144:147], v[168:171], v[68:71]
	s_barrier
	s_mov_b32 m0, s92
	v_lshl_add_u64 v[218:219], s[58:59], 0, v[200:201]
	s_add_u32 s8, s58, 0x40000
	ds_read_b128 v[188:191], v228 offset:16384
	ds_read_b128 v[192:195], v228 offset:17408
	ds_read_b128 v[180:183], v228 offset:18432
	ds_read_b128 v[184:187], v228 offset:19456
	ds_read_b128 v[172:175], v228 offset:20480
	ds_read_b128 v[176:179], v228 offset:21504
	ds_read_b128 v[164:167], v228 offset:22528
	ds_read_b128 v[168:171], v228 offset:23552
	global_load_lds_dwordx4 v[218:219], off
	v_lshl_add_u64 v[216:217], s[58:59], 0, v[208:209]
	s_mov_b32 m0, s93
	s_addc_u32 s9, s59, 0
	global_load_lds_dwordx4 v[216:217], off
	v_lshl_add_u64 v[212:213], s[8:9], 0, v[200:201]
	s_mov_b32 m0, s94
	v_lshl_add_u64 v[214:215], s[86:87], 0, v[202:203]
	global_load_lds_dwordx4 v[212:213], off
	v_lshl_add_u64 v[212:213], s[8:9], 0, v[208:209]
	s_mov_b32 m0, s95
	s_mov_b64 s[26:27], -1
	global_load_lds_dwordx4 v[212:213], off
	v_lshl_add_u64 v[212:213], s[86:87], 0, v[198:199]
	s_mov_b32 m0, s91
	s_and_b64 vcc, exec, s[84:85]
	global_load_lds_dwordx4 v[212:213], off
	s_mov_b32 m0, s96
	s_nop 0
	global_load_lds_dwordx4 v[214:215], off
	s_cbranch_vccz .LBB0_490
	s_waitcnt vmcnt(8)
	s_mov_b64 s[26:27], 0

.LBB0_507:
	s_waitcnt lgkmcnt(0)
	s_barrier
	v_mfma_f32_16x16x32_bf16 v[62:65], v[148:151], v[188:191], v[62:65]
	v_mfma_f32_16x16x32_bf16 v[58:61], v[156:159], v[188:191], v[58:61]
	v_mfma_f32_16x16x32_bf16 v[54:57], v[148:151], v[180:183], v[54:57]
	v_mfma_f32_16x16x32_bf16 v[46:49], v[156:159], v[180:183], v[46:49]
	v_mfma_f32_16x16x32_bf16 v[38:41], v[148:151], v[172:175], v[38:41]
	v_mfma_f32_16x16x32_bf16 v[30:33], v[156:159], v[172:175], v[30:33]
	v_mfma_f32_16x16x32_bf16 v[22:25], v[148:151], v[164:167], v[22:25]
	v_mfma_f32_16x16x32_bf16 v[14:17], v[156:159], v[164:167], v[14:17]
	v_mfma_f32_16x16x32_bf16 v[62:65], v[152:155], v[192:195], v[62:65]
	v_mfma_f32_16x16x32_bf16 v[58:61], v[160:163], v[192:195], v[58:61]
	v_mfma_f32_16x16x32_bf16 v[54:57], v[152:155], v[184:187], v[54:57]
	v_mfma_f32_16x16x32_bf16 v[46:49], v[160:163], v[184:187], v[46:49]
	v_mfma_f32_16x16x32_bf16 v[38:41], v[152:155], v[176:179], v[38:41]
	v_mfma_f32_16x16x32_bf16 v[30:33], v[160:163], v[176:179], v[30:33]
	v_mfma_f32_16x16x32_bf16 v[22:25], v[152:155], v[168:171], v[22:25]
	v_mfma_f32_16x16x32_bf16 v[14:17], v[160:163], v[168:171], v[14:17]
	v_mfma_f32_16x16x32_bf16 v[50:53], v[132:135], v[188:191], v[50:53]
	v_mfma_f32_16x16x32_bf16 v[42:45], v[140:143], v[188:191], v[42:45]
	v_mfma_f32_16x16x32_bf16 v[34:37], v[132:135], v[180:183], v[34:37]
	v_mfma_f32_16x16x32_bf16 v[26:29], v[140:143], v[180:183], v[26:29]
	v_mfma_f32_16x16x32_bf16 v[18:21], v[132:135], v[172:175], v[18:21]
	v_mfma_f32_16x16x32_bf16 v[10:13], v[140:143], v[172:175], v[10:13]
	v_mfma_f32_16x16x32_bf16 v[6:9], v[132:135], v[164:167], v[6:9]
	v_mfma_f32_16x16x32_bf16 v[2:5], v[140:143], v[164:167], v[2:5]
	v_mfma_f32_16x16x32_bf16 v[50:53], v[136:139], v[192:195], v[50:53]
	v_mfma_f32_16x16x32_bf16 v[42:45], v[144:147], v[192:195], v[42:45]
	v_mfma_f32_16x16x32_bf16 v[34:37], v[136:139], v[184:187], v[34:37]
	v_mfma_f32_16x16x32_bf16 v[26:29], v[144:147], v[184:187], v[26:29]
	v_mfma_f32_16x16x32_bf16 v[18:21], v[136:139], v[176:179], v[18:21]
	v_mfma_f32_16x16x32_bf16 v[10:13], v[144:147], v[176:179], v[10:13]
	v_mfma_f32_16x16x32_bf16 v[6:9], v[136:139], v[168:171], v[6:9]
	v_mfma_f32_16x16x32_bf16 v[2:5], v[144:147], v[168:171], v[2:5]
	s_barrier
	s_add_i32 s10, 0, 0x18000
	s_add_i32 s11, 0, 0x1c000
	v_add_u32_e32 v144, s10, v205
	v_add_u32_e32 v160, s11, v205
	ds_read_b128 v[132:135], v144
	ds_read_b128 v[136:139], v144 offset:1024
	ds_read_b128 v[140:143], v144 offset:2048
	ds_read_b128 v[144:147], v144 offset:3072
	ds_read_b128 v[148:151], v160
	ds_read_b128 v[152:155], v160 offset:1024
	ds_read_b128 v[156:159], v160 offset:2048
	ds_read_b128 v[160:163], v160 offset:3072
	s_add_u32 s8, s52, 0x40000
	s_addc_u32 s9, s53, 0
	s_mov_b32 m0, s70
	v_lshl_add_u64 v[228:229], s[8:9], 0, v[66:67]
	ds_read_b128 v[164:167], v226 offset:32768
	ds_read_b128 v[168:171], v226 offset:33792
	ds_read_b128 v[172:175], v226 offset:34816
	ds_read_b128 v[176:179], v226 offset:35840
	ds_read_b128 v[180:183], v226 offset:36864
	ds_read_b128 v[184:187], v226 offset:37888
	ds_read_b128 v[188:191], v226 offset:38912
	ds_read_b128 v[192:195], v226 offset:39936
	global_load_lds_dwordx4 v[228:229], off
	v_lshl_add_u64 v[228:229], s[8:9], 0, v[200:201]
	s_mov_b32 m0, s71
	s_nop 0
	global_load_lds_dwordx4 v[228:229], off
	s_waitcnt vmcnt(8)
	s_waitcnt lgkmcnt(0)
	s_barrier
	v_mfma_f32_16x16x32_bf16 v[128:131], v[132:135], v[164:167], v[128:131]
	v_mfma_f32_16x16x32_bf16 v[124:127], v[140:143], v[164:167], v[124:127]
	v_mfma_f32_16x16x32_bf16 v[120:123], v[132:135], v[172:175], v[120:123]
	v_mfma_f32_16x16x32_bf16 v[112:115], v[140:143], v[172:175], v[112:115]
	v_mfma_f32_16x16x32_bf16 v[104:107], v[132:135], v[180:183], v[104:107]
	v_mfma_f32_16x16x32_bf16 v[96:99], v[140:143], v[180:183], v[96:99]
	v_mfma_f32_16x16x32_bf16 v[88:91], v[132:135], v[188:191], v[88:91]
	v_mfma_f32_16x16x32_bf16 v[80:83], v[140:143], v[188:191], v[80:83]
	v_mfma_f32_16x16x32_bf16 v[128:131], v[136:139], v[168:171], v[128:131]
	v_mfma_f32_16x16x32_bf16 v[124:127], v[144:147], v[168:171], v[124:127]
	v_mfma_f32_16x16x32_bf16 v[120:123], v[136:139], v[176:179], v[120:123]
	v_mfma_f32_16x16x32_bf16 v[112:115], v[144:147], v[176:179], v[112:115]
	v_mfma_f32_16x16x32_bf16 v[104:107], v[136:139], v[184:187], v[104:107]
	v_mfma_f32_16x16x32_bf16 v[96:99], v[144:147], v[184:187], v[96:99]
	v_mfma_f32_16x16x32_bf16 v[88:91], v[136:139], v[192:195], v[88:91]
	v_mfma_f32_16x16x32_bf16 v[80:83], v[144:147], v[192:195], v[80:83]
	v_mfma_f32_16x16x32_bf16 v[116:119], v[148:151], v[164:167], v[116:119]
	v_mfma_f32_16x16x32_bf16 v[108:111], v[156:159], v[164:167], v[108:111]
	v_mfma_f32_16x16x32_bf16 v[100:103], v[148:151], v[172:175], v[100:103]
	v_mfma_f32_16x16x32_bf16 v[92:95], v[156:159], v[172:175], v[92:95]
	v_mfma_f32_16x16x32_bf16 v[84:87], v[148:151], v[180:183], v[84:87]
	v_mfma_f32_16x16x32_bf16 v[76:79], v[156:159], v[180:183], v[76:79]
	v_mfma_f32_16x16x32_bf16 v[72:75], v[148:151], v[188:191], v[72:75]
	v_mfma_f32_16x16x32_bf16 v[68:71], v[156:159], v[188:191], v[68:71]
	v_mfma_f32_16x16x32_bf16 v[116:119], v[152:155], v[168:171], v[116:119]
	v_mfma_f32_16x16x32_bf16 v[108:111], v[160:163], v[168:171], v[108:111]
	v_mfma_f32_16x16x32_bf16 v[100:103], v[152:155], v[176:179], v[100:103]
	v_mfma_f32_16x16x32_bf16 v[92:95], v[160:163], v[176:179], v[92:95]
	v_mfma_f32_16x16x32_bf16 v[84:87], v[152:155], v[184:187], v[84:87]
	v_mfma_f32_16x16x32_bf16 v[76:79], v[160:163], v[184:187], v[76:79]
	v_mfma_f32_16x16x32_bf16 v[72:75], v[152:155], v[192:195], v[72:75]
	v_mfma_f32_16x16x32_bf16 v[68:71], v[160:163], v[192:195], v[68:71]
	s_barrier
	s_add_i32 s8, s10, s57
	v_lshl_add_u64 v[222:223], v[222:223], 0, s[60:61]
	s_mov_b32 m0, s8
	ds_read_b128 v[164:167], v226 offset:49152
	ds_read_b128 v[168:171], v226 offset:50176
	ds_read_b128 v[172:175], v226 offset:51200
	ds_read_b128 v[176:179], v226 offset:52224
	ds_read_b128 v[180:183], v226 offset:53248
	ds_read_b128 v[184:187], v226 offset:54272
	ds_read_b128 v[188:191], v226 offset:55296
	ds_read_b128 v[192:195], v226 offset:56320
	global_load_lds_dwordx4 v[222:223], off
	s_add_i32 m0, s8, 0x2000
	s_add_u32 s8, s36, 0x40080
	v_lshl_add_u64 v[220:221], v[220:221], 0, s[60:61]
	s_addc_u32 s9, s37, 0
	s_add_i32 s10, s11, s57
	global_load_lds_dwordx4 v[220:221], off
	v_lshl_add_u64 v[220:221], s[8:9], 0, v[198:199]
	s_mov_b32 m0, s10
	v_lshl_add_u64 v[216:217], v[216:217], 0, s[60:61]
	global_load_lds_dwordx4 v[220:221], off
	v_lshl_add_u64 v[220:221], s[8:9], 0, v[202:203]
	s_add_i32 m0, s10, 0x2000
	s_nop 0
	global_load_lds_dwordx4 v[220:221], off
	s_mov_b32 m0, s72
	s_nop 0
	global_load_lds_dwordx4 v[216:217], off
	v_lshl_add_u64 v[216:217], v[218:219], 0, s[60:61]
	s_mov_b32 m0, s84
	s_nop 0
	global_load_lds_dwordx4 v[216:217], off
	s_waitcnt vmcnt(8)
	s_waitcnt lgkmcnt(0)
	s_barrier
	v_mfma_f32_16x16x32_bf16 v[62:65], v[132:135], v[164:167], v[62:65]
	v_mfma_f32_16x16x32_bf16 v[58:61], v[140:143], v[164:167], v[58:61]
	v_mfma_f32_16x16x32_bf16 v[54:57], v[132:135], v[172:175], v[54:57]
	v_mfma_f32_16x16x32_bf16 v[46:49], v[140:143], v[172:175], v[46:49]
	v_mfma_f32_16x16x32_bf16 v[38:41], v[132:135], v[180:183], v[38:41]
	v_mfma_f32_16x16x32_bf16 v[30:33], v[140:143], v[180:183], v[30:33]
	v_mfma_f32_16x16x32_bf16 v[22:25], v[132:135], v[188:191], v[22:25]
	v_mfma_f32_16x16x32_bf16 v[14:17], v[140:143], v[188:191], v[14:17]
	v_mfma_f32_16x16x32_bf16 v[62:65], v[136:139], v[168:171], v[62:65]
	v_mfma_f32_16x16x32_bf16 v[58:61], v[144:147], v[168:171], v[58:61]
	v_mfma_f32_16x16x32_bf16 v[54:57], v[136:139], v[176:179], v[54:57]
	v_mfma_f32_16x16x32_bf16 v[46:49], v[144:147], v[176:179], v[46:49]
	v_mfma_f32_16x16x32_bf16 v[38:41], v[136:139], v[184:187], v[38:41]
	v_mfma_f32_16x16x32_bf16 v[30:33], v[144:147], v[184:187], v[30:33]
	v_mfma_f32_16x16x32_bf16 v[22:25], v[136:139], v[192:195], v[22:25]
	v_mfma_f32_16x16x32_bf16 v[14:17], v[144:147], v[192:195], v[14:17]
	v_mfma_f32_16x16x32_bf16 v[50:53], v[148:151], v[164:167], v[50:53]
	v_mfma_f32_16x16x32_bf16 v[42:45], v[156:159], v[164:167], v[42:45]
	v_mfma_f32_16x16x32_bf16 v[34:37], v[148:151], v[172:175], v[34:37]
	v_mfma_f32_16x16x32_bf16 v[26:29], v[156:159], v[172:175], v[26:29]
	v_mfma_f32_16x16x32_bf16 v[18:21], v[148:151], v[180:183], v[18:21]
	v_mfma_f32_16x16x32_bf16 v[10:13], v[156:159], v[180:183], v[10:13]
	v_mfma_f32_16x16x32_bf16 v[6:9], v[148:151], v[188:191], v[6:9]
	v_mfma_f32_16x16x32_bf16 v[2:5], v[156:159], v[188:191], v[2:5]
	v_mfma_f32_16x16x32_bf16 v[50:53], v[152:155], v[168:171], v[50:53]
	v_mfma_f32_16x16x32_bf16 v[42:45], v[160:163], v[168:171], v[42:45]
	v_mfma_f32_16x16x32_bf16 v[34:37], v[152:155], v[176:179], v[34:37]
	v_mfma_f32_16x16x32_bf16 v[26:29], v[160:163], v[176:179], v[26:29]
	v_mfma_f32_16x16x32_bf16 v[18:21], v[152:155], v[184:187], v[18:21]
	v_mfma_f32_16x16x32_bf16 v[10:13], v[160:163], v[184:187], v[10:13]
	v_mfma_f32_16x16x32_bf16 v[6:9], v[152:155], v[192:195], v[6:9]
	v_mfma_f32_16x16x32_bf16 v[2:5], v[160:163], v[192:195], v[2:5]
	s_barrier
	s_add_i32 s91, s91, 2
	s_add_u32 s48, s48, 0x100
	s_addc_u32 s49, s49, 0
	s_cmp_gt_u32 s91, 13
	s_cbranch_scc1 .LBB0_516

.LBB0_512:
	s_add_u32 s8, s46, s48
	s_addc_u32 s9, s47, s49
	s_add_u32 s8, s8, 0x100
	s_addc_u32 s9, s9, 0
	s_add_u32 s10, s89, s48
	s_addc_u32 s11, s90, s49
	s_waitcnt lgkmcnt(0)
	s_cmpk_eq_i32 s48, 0x700
	s_cselect_b32 s53, s41, s9
	s_cselect_b32 s52, s40, s8
	s_cselect_b32 s37, s43, s11
	s_cselect_b32 s36, s42, s10
	s_barrier
	v_mfma_f32_16x16x32_bf16 v[128:131], v[148:151], v[188:191], v[128:131]
	v_mfma_f32_16x16x32_bf16 v[124:127], v[156:159], v[188:191], v[124:127]
	v_mfma_f32_16x16x32_bf16 v[120:123], v[148:151], v[180:183], v[120:123]
	v_mfma_f32_16x16x32_bf16 v[112:115], v[156:159], v[180:183], v[112:115]
	v_mfma_f32_16x16x32_bf16 v[104:107], v[148:151], v[172:175], v[104:107]
	v_mfma_f32_16x16x32_bf16 v[96:99], v[156:159], v[172:175], v[96:99]
	v_mfma_f32_16x16x32_bf16 v[88:91], v[148:151], v[164:167], v[88:91]
	v_mfma_f32_16x16x32_bf16 v[80:83], v[156:159], v[164:167], v[80:83]
	v_mfma_f32_16x16x32_bf16 v[128:131], v[152:155], v[192:195], v[128:131]
	v_mfma_f32_16x16x32_bf16 v[124:127], v[160:163], v[192:195], v[124:127]
	v_mfma_f32_16x16x32_bf16 v[120:123], v[152:155], v[184:187], v[120:123]
	v_mfma_f32_16x16x32_bf16 v[112:115], v[160:163], v[184:187], v[112:115]
	v_mfma_f32_16x16x32_bf16 v[104:107], v[152:155], v[176:179], v[104:107]
	v_mfma_f32_16x16x32_bf16 v[96:99], v[160:163], v[176:179], v[96:99]
	v_mfma_f32_16x16x32_bf16 v[88:91], v[152:155], v[168:171], v[88:91]
	v_mfma_f32_16x16x32_bf16 v[80:83], v[160:163], v[168:171], v[80:83]
	v_mfma_f32_16x16x32_bf16 v[116:119], v[132:135], v[188:191], v[116:119]
	v_mfma_f32_16x16x32_bf16 v[108:111], v[140:143], v[188:191], v[108:111]
	v_mfma_f32_16x16x32_bf16 v[100:103], v[132:135], v[180:183], v[100:103]
	v_mfma_f32_16x16x32_bf16 v[92:95], v[140:143], v[180:183], v[92:95]
	v_mfma_f32_16x16x32_bf16 v[84:87], v[132:135], v[172:175], v[84:87]
	v_mfma_f32_16x16x32_bf16 v[76:79], v[140:143], v[172:175], v[76:79]
	v_mfma_f32_16x16x32_bf16 v[72:75], v[132:135], v[164:167], v[72:75]
	v_mfma_f32_16x16x32_bf16 v[68:71], v[140:143], v[164:167], v[68:71]
	v_mfma_f32_16x16x32_bf16 v[116:119], v[136:139], v[192:195], v[116:119]
	v_mfma_f32_16x16x32_bf16 v[108:111], v[144:147], v[192:195], v[108:111]
	v_mfma_f32_16x16x32_bf16 v[100:103], v[136:139], v[184:187], v[100:103]
	v_mfma_f32_16x16x32_bf16 v[92:95], v[144:147], v[184:187], v[92:95]
	v_mfma_f32_16x16x32_bf16 v[84:87], v[136:139], v[176:179], v[84:87]
	v_mfma_f32_16x16x32_bf16 v[76:79], v[144:147], v[176:179], v[76:79]
	v_mfma_f32_16x16x32_bf16 v[72:75], v[136:139], v[168:171], v[72:75]
	v_mfma_f32_16x16x32_bf16 v[68:71], v[144:147], v[168:171], v[68:71]
	s_barrier
	s_mov_b32 m0, s59
	v_lshl_add_u64 v[222:223], s[36:37], 0, v[198:199]
	s_add_u32 s8, s36, 0x40000
	ds_read_b128 v[188:191], v226 offset:16384
	ds_read_b128 v[192:195], v226 offset:17408
	ds_read_b128 v[180:183], v226 offset:18432
	ds_read_b128 v[184:187], v226 offset:19456
	ds_read_b128 v[172:175], v226 offset:20480
	ds_read_b128 v[176:179], v226 offset:21504
	ds_read_b128 v[164:167], v226 offset:22528
	ds_read_b128 v[168:171], v226 offset:23552
	global_load_lds_dwordx4 v[222:223], off
	v_lshl_add_u64 v[220:221], s[36:37], 0, v[202:203]
	s_mov_b32 m0, s64
	s_addc_u32 s9, s37, 0
	global_load_lds_dwordx4 v[220:221], off
	v_lshl_add_u64 v[216:217], s[8:9], 0, v[198:199]
	s_mov_b32 m0, s65
	v_lshl_add_u64 v[218:219], s[52:53], 0, v[200:201]
	global_load_lds_dwordx4 v[216:217], off
	v_lshl_add_u64 v[216:217], s[8:9], 0, v[202:203]
	s_mov_b32 m0, s68
	s_mov_b64 s[26:27], -1
	global_load_lds_dwordx4 v[216:217], off
	v_lshl_add_u64 v[216:217], s[52:53], 0, v[66:67]
	s_mov_b32 m0, s58
	s_and_b64 vcc, exec, s[54:55]
	global_load_lds_dwordx4 v[216:217], off
	s_mov_b32 m0, s69
	s_nop 0
	global_load_lds_dwordx4 v[218:219], off
	s_cbranch_vccz .LBB0_514
	s_waitcnt vmcnt(8)
	s_mov_b64 s[26:27], 0

.LBB0_678:
	s_waitcnt lgkmcnt(0)
	s_barrier
	v_mfma_f32_16x16x32_bf16 v[62:65], v[148:151], v[188:191], v[62:65]
	v_mfma_f32_16x16x32_bf16 v[58:61], v[156:159], v[188:191], v[58:61]
	v_mfma_f32_16x16x32_bf16 v[54:57], v[148:151], v[180:183], v[54:57]
	v_mfma_f32_16x16x32_bf16 v[46:49], v[156:159], v[180:183], v[46:49]
	v_mfma_f32_16x16x32_bf16 v[38:41], v[148:151], v[172:175], v[38:41]
	v_mfma_f32_16x16x32_bf16 v[30:33], v[156:159], v[172:175], v[30:33]
	v_mfma_f32_16x16x32_bf16 v[22:25], v[148:151], v[164:167], v[22:25]
	v_mfma_f32_16x16x32_bf16 v[14:17], v[156:159], v[164:167], v[14:17]
	v_mfma_f32_16x16x32_bf16 v[62:65], v[152:155], v[192:195], v[62:65]
	v_mfma_f32_16x16x32_bf16 v[58:61], v[160:163], v[192:195], v[58:61]
	v_mfma_f32_16x16x32_bf16 v[54:57], v[152:155], v[184:187], v[54:57]
	v_mfma_f32_16x16x32_bf16 v[46:49], v[160:163], v[184:187], v[46:49]
	v_mfma_f32_16x16x32_bf16 v[38:41], v[152:155], v[176:179], v[38:41]
	v_mfma_f32_16x16x32_bf16 v[30:33], v[160:163], v[176:179], v[30:33]
	v_mfma_f32_16x16x32_bf16 v[22:25], v[152:155], v[168:171], v[22:25]
	v_mfma_f32_16x16x32_bf16 v[14:17], v[160:163], v[168:171], v[14:17]
	v_mfma_f32_16x16x32_bf16 v[50:53], v[132:135], v[188:191], v[50:53]
	v_mfma_f32_16x16x32_bf16 v[42:45], v[140:143], v[188:191], v[42:45]
	v_mfma_f32_16x16x32_bf16 v[34:37], v[132:135], v[180:183], v[34:37]
	v_mfma_f32_16x16x32_bf16 v[26:29], v[140:143], v[180:183], v[26:29]
	v_mfma_f32_16x16x32_bf16 v[18:21], v[132:135], v[172:175], v[18:21]
	v_mfma_f32_16x16x32_bf16 v[10:13], v[140:143], v[172:175], v[10:13]
	v_mfma_f32_16x16x32_bf16 v[6:9], v[132:135], v[164:167], v[6:9]
	v_mfma_f32_16x16x32_bf16 v[2:5], v[140:143], v[164:167], v[2:5]
	v_mfma_f32_16x16x32_bf16 v[50:53], v[136:139], v[192:195], v[50:53]
	v_mfma_f32_16x16x32_bf16 v[42:45], v[144:147], v[192:195], v[42:45]
	v_mfma_f32_16x16x32_bf16 v[34:37], v[136:139], v[184:187], v[34:37]
	v_mfma_f32_16x16x32_bf16 v[26:29], v[144:147], v[184:187], v[26:29]
	v_mfma_f32_16x16x32_bf16 v[18:21], v[136:139], v[176:179], v[18:21]
	v_mfma_f32_16x16x32_bf16 v[10:13], v[144:147], v[176:179], v[10:13]
	v_mfma_f32_16x16x32_bf16 v[6:9], v[136:139], v[168:171], v[6:9]
	v_mfma_f32_16x16x32_bf16 v[2:5], v[144:147], v[168:171], v[2:5]
	s_barrier
	s_add_i32 s10, 0, 0x18000
	s_add_i32 s11, 0, 0x1c000
	v_add_u32_e32 v144, s10, v222
	v_add_u32_e32 v160, s11, v222
	ds_read_b128 v[132:135], v144
	ds_read_b128 v[136:139], v144 offset:1024
	ds_read_b128 v[140:143], v144 offset:2048
	ds_read_b128 v[144:147], v144 offset:3072
	ds_read_b128 v[148:151], v160
	ds_read_b128 v[152:155], v160 offset:1024
	ds_read_b128 v[156:159], v160 offset:2048
	ds_read_b128 v[160:163], v160 offset:3072
	s_add_u32 s8, s52, 0x40000
	s_addc_u32 s9, s53, 0
	s_mov_b32 m0, s70
	v_lshl_add_u64 v[226:227], s[8:9], 0, v[66:67]
	ds_read_b128 v[164:167], v224 offset:32768
	ds_read_b128 v[168:171], v224 offset:33792
	ds_read_b128 v[172:175], v224 offset:34816
	ds_read_b128 v[176:179], v224 offset:35840
	ds_read_b128 v[180:183], v224 offset:36864
	ds_read_b128 v[184:187], v224 offset:37888
	ds_read_b128 v[188:191], v224 offset:38912
	ds_read_b128 v[192:195], v224 offset:39936
	global_load_lds_dwordx4 v[226:227], off
	v_lshl_add_u64 v[226:227], s[8:9], 0, v[198:199]
	s_mov_b32 m0, s71
	s_nop 0
	global_load_lds_dwordx4 v[226:227], off
	s_waitcnt vmcnt(8)
	s_waitcnt lgkmcnt(0)
	s_barrier
	v_mfma_f32_16x16x32_bf16 v[128:131], v[132:135], v[164:167], v[128:131]
	v_mfma_f32_16x16x32_bf16 v[124:127], v[140:143], v[164:167], v[124:127]
	v_mfma_f32_16x16x32_bf16 v[120:123], v[132:135], v[172:175], v[120:123]
	v_mfma_f32_16x16x32_bf16 v[112:115], v[140:143], v[172:175], v[112:115]
	v_mfma_f32_16x16x32_bf16 v[104:107], v[132:135], v[180:183], v[104:107]
	v_mfma_f32_16x16x32_bf16 v[96:99], v[140:143], v[180:183], v[96:99]
	v_mfma_f32_16x16x32_bf16 v[88:91], v[132:135], v[188:191], v[88:91]
	v_mfma_f32_16x16x32_bf16 v[80:83], v[140:143], v[188:191], v[80:83]
	v_mfma_f32_16x16x32_bf16 v[128:131], v[136:139], v[168:171], v[128:131]
	v_mfma_f32_16x16x32_bf16 v[124:127], v[144:147], v[168:171], v[124:127]
	v_mfma_f32_16x16x32_bf16 v[120:123], v[136:139], v[176:179], v[120:123]
	v_mfma_f32_16x16x32_bf16 v[112:115], v[144:147], v[176:179], v[112:115]
	v_mfma_f32_16x16x32_bf16 v[104:107], v[136:139], v[184:187], v[104:107]
	v_mfma_f32_16x16x32_bf16 v[96:99], v[144:147], v[184:187], v[96:99]
	v_mfma_f32_16x16x32_bf16 v[88:91], v[136:139], v[192:195], v[88:91]
	v_mfma_f32_16x16x32_bf16 v[80:83], v[144:147], v[192:195], v[80:83]
	v_mfma_f32_16x16x32_bf16 v[116:119], v[148:151], v[164:167], v[116:119]
	v_mfma_f32_16x16x32_bf16 v[108:111], v[156:159], v[164:167], v[108:111]
	v_mfma_f32_16x16x32_bf16 v[100:103], v[148:151], v[172:175], v[100:103]
	v_mfma_f32_16x16x32_bf16 v[92:95], v[156:159], v[172:175], v[92:95]
	v_mfma_f32_16x16x32_bf16 v[84:87], v[148:151], v[180:183], v[84:87]
	v_mfma_f32_16x16x32_bf16 v[76:79], v[156:159], v[180:183], v[76:79]
	v_mfma_f32_16x16x32_bf16 v[72:75], v[148:151], v[188:191], v[72:75]
	v_mfma_f32_16x16x32_bf16 v[68:71], v[156:159], v[188:191], v[68:71]
	v_mfma_f32_16x16x32_bf16 v[116:119], v[152:155], v[168:171], v[116:119]
	v_mfma_f32_16x16x32_bf16 v[108:111], v[160:163], v[168:171], v[108:111]
	v_mfma_f32_16x16x32_bf16 v[100:103], v[152:155], v[176:179], v[100:103]
	v_mfma_f32_16x16x32_bf16 v[92:95], v[160:163], v[176:179], v[92:95]
	v_mfma_f32_16x16x32_bf16 v[84:87], v[152:155], v[184:187], v[84:87]
	v_mfma_f32_16x16x32_bf16 v[76:79], v[160:163], v[184:187], v[76:79]
	v_mfma_f32_16x16x32_bf16 v[72:75], v[152:155], v[192:195], v[72:75]
	v_mfma_f32_16x16x32_bf16 v[68:71], v[160:163], v[192:195], v[68:71]
	s_barrier
	s_add_i32 s8, s10, s57
	v_lshl_add_u64 v[220:221], v[220:221], 0, s[60:61]
	s_mov_b32 m0, s8
	ds_read_b128 v[164:167], v224 offset:49152
	ds_read_b128 v[168:171], v224 offset:50176
	ds_read_b128 v[172:175], v224 offset:51200
	ds_read_b128 v[176:179], v224 offset:52224
	ds_read_b128 v[180:183], v224 offset:53248
	ds_read_b128 v[184:187], v224 offset:54272
	ds_read_b128 v[188:191], v224 offset:55296
	ds_read_b128 v[192:195], v224 offset:56320
	global_load_lds_dwordx4 v[220:221], off
	s_add_i32 m0, s8, 0x2000
	s_add_u32 s8, s36, 0x40080
	v_lshl_add_u64 v[218:219], v[218:219], 0, s[60:61]
	s_addc_u32 s9, s37, 0
	s_add_i32 s10, s11, s57
	global_load_lds_dwordx4 v[218:219], off
	v_lshl_add_u64 v[218:219], s[8:9], 0, v[196:197]
	s_mov_b32 m0, s10
	v_lshl_add_u64 v[214:215], v[214:215], 0, s[60:61]
	global_load_lds_dwordx4 v[218:219], off
	v_lshl_add_u64 v[218:219], s[8:9], 0, v[200:201]
	s_add_i32 m0, s10, 0x2000
	s_nop 0
	global_load_lds_dwordx4 v[218:219], off
	s_mov_b32 m0, s72
	s_nop 0
	global_load_lds_dwordx4 v[214:215], off
	v_lshl_add_u64 v[214:215], v[216:217], 0, s[60:61]
	s_mov_b32 m0, s84
	s_nop 0
	global_load_lds_dwordx4 v[214:215], off
	s_waitcnt vmcnt(8)
	s_waitcnt lgkmcnt(0)
	s_barrier
	v_mfma_f32_16x16x32_bf16 v[62:65], v[132:135], v[164:167], v[62:65]
	v_mfma_f32_16x16x32_bf16 v[58:61], v[140:143], v[164:167], v[58:61]
	v_mfma_f32_16x16x32_bf16 v[54:57], v[132:135], v[172:175], v[54:57]
	v_mfma_f32_16x16x32_bf16 v[46:49], v[140:143], v[172:175], v[46:49]
	v_mfma_f32_16x16x32_bf16 v[38:41], v[132:135], v[180:183], v[38:41]
	v_mfma_f32_16x16x32_bf16 v[30:33], v[140:143], v[180:183], v[30:33]
	v_mfma_f32_16x16x32_bf16 v[22:25], v[132:135], v[188:191], v[22:25]
	v_mfma_f32_16x16x32_bf16 v[14:17], v[140:143], v[188:191], v[14:17]
	v_mfma_f32_16x16x32_bf16 v[62:65], v[136:139], v[168:171], v[62:65]
	v_mfma_f32_16x16x32_bf16 v[58:61], v[144:147], v[168:171], v[58:61]
	v_mfma_f32_16x16x32_bf16 v[54:57], v[136:139], v[176:179], v[54:57]
	v_mfma_f32_16x16x32_bf16 v[46:49], v[144:147], v[176:179], v[46:49]
	v_mfma_f32_16x16x32_bf16 v[38:41], v[136:139], v[184:187], v[38:41]
	v_mfma_f32_16x16x32_bf16 v[30:33], v[144:147], v[184:187], v[30:33]
	v_mfma_f32_16x16x32_bf16 v[22:25], v[136:139], v[192:195], v[22:25]
	v_mfma_f32_16x16x32_bf16 v[14:17], v[144:147], v[192:195], v[14:17]
	v_mfma_f32_16x16x32_bf16 v[50:53], v[148:151], v[164:167], v[50:53]
	v_mfma_f32_16x16x32_bf16 v[42:45], v[156:159], v[164:167], v[42:45]
	v_mfma_f32_16x16x32_bf16 v[34:37], v[148:151], v[172:175], v[34:37]
	v_mfma_f32_16x16x32_bf16 v[26:29], v[156:159], v[172:175], v[26:29]
	v_mfma_f32_16x16x32_bf16 v[18:21], v[148:151], v[180:183], v[18:21]
	v_mfma_f32_16x16x32_bf16 v[10:13], v[156:159], v[180:183], v[10:13]
	v_mfma_f32_16x16x32_bf16 v[6:9], v[148:151], v[188:191], v[6:9]
	v_mfma_f32_16x16x32_bf16 v[2:5], v[156:159], v[188:191], v[2:5]
	v_mfma_f32_16x16x32_bf16 v[50:53], v[152:155], v[168:171], v[50:53]
	v_mfma_f32_16x16x32_bf16 v[42:45], v[160:163], v[168:171], v[42:45]
	v_mfma_f32_16x16x32_bf16 v[34:37], v[152:155], v[176:179], v[34:37]
	v_mfma_f32_16x16x32_bf16 v[26:29], v[160:163], v[176:179], v[26:29]
	v_mfma_f32_16x16x32_bf16 v[18:21], v[152:155], v[184:187], v[18:21]
	v_mfma_f32_16x16x32_bf16 v[10:13], v[160:163], v[184:187], v[10:13]
	v_mfma_f32_16x16x32_bf16 v[6:9], v[152:155], v[192:195], v[6:9]
	v_mfma_f32_16x16x32_bf16 v[2:5], v[160:163], v[192:195], v[2:5]
	s_barrier
	s_add_i32 s91, s91, 2
	s_add_u32 s48, s48, 0x100
	s_addc_u32 s49, s49, 0
	s_cmp_gt_u32 s91, 13
	s_cbranch_scc1 .LBB0_687

.LBB0_683:
	s_add_u32 s8, s46, s48
	s_addc_u32 s9, s47, s49
	s_add_u32 s8, s8, 0x100
	s_addc_u32 s9, s9, 0
	s_add_u32 s10, s89, s48
	s_addc_u32 s11, s90, s49
	s_waitcnt lgkmcnt(0)
	s_cmpk_eq_i32 s48, 0x700
	s_cselect_b32 s53, s41, s9
	s_cselect_b32 s52, s40, s8
	s_cselect_b32 s37, s43, s11
	s_cselect_b32 s36, s42, s10
	s_barrier
	v_mfma_f32_16x16x32_bf16 v[128:131], v[148:151], v[188:191], v[128:131]
	v_mfma_f32_16x16x32_bf16 v[124:127], v[156:159], v[188:191], v[124:127]
	v_mfma_f32_16x16x32_bf16 v[120:123], v[148:151], v[180:183], v[120:123]
	v_mfma_f32_16x16x32_bf16 v[112:115], v[156:159], v[180:183], v[112:115]
	v_mfma_f32_16x16x32_bf16 v[104:107], v[148:151], v[172:175], v[104:107]
	v_mfma_f32_16x16x32_bf16 v[96:99], v[156:159], v[172:175], v[96:99]
	v_mfma_f32_16x16x32_bf16 v[88:91], v[148:151], v[164:167], v[88:91]
	v_mfma_f32_16x16x32_bf16 v[80:83], v[156:159], v[164:167], v[80:83]
	v_mfma_f32_16x16x32_bf16 v[128:131], v[152:155], v[192:195], v[128:131]
	v_mfma_f32_16x16x32_bf16 v[124:127], v[160:163], v[192:195], v[124:127]
	v_mfma_f32_16x16x32_bf16 v[120:123], v[152:155], v[184:187], v[120:123]
	v_mfma_f32_16x16x32_bf16 v[112:115], v[160:163], v[184:187], v[112:115]
	v_mfma_f32_16x16x32_bf16 v[104:107], v[152:155], v[176:179], v[104:107]
	v_mfma_f32_16x16x32_bf16 v[96:99], v[160:163], v[176:179], v[96:99]
	v_mfma_f32_16x16x32_bf16 v[88:91], v[152:155], v[168:171], v[88:91]
	v_mfma_f32_16x16x32_bf16 v[80:83], v[160:163], v[168:171], v[80:83]
	v_mfma_f32_16x16x32_bf16 v[116:119], v[132:135], v[188:191], v[116:119]
	v_mfma_f32_16x16x32_bf16 v[108:111], v[140:143], v[188:191], v[108:111]
	v_mfma_f32_16x16x32_bf16 v[100:103], v[132:135], v[180:183], v[100:103]
	v_mfma_f32_16x16x32_bf16 v[92:95], v[140:143], v[180:183], v[92:95]
	v_mfma_f32_16x16x32_bf16 v[84:87], v[132:135], v[172:175], v[84:87]
	v_mfma_f32_16x16x32_bf16 v[76:79], v[140:143], v[172:175], v[76:79]
	v_mfma_f32_16x16x32_bf16 v[72:75], v[132:135], v[164:167], v[72:75]
	v_mfma_f32_16x16x32_bf16 v[68:71], v[140:143], v[164:167], v[68:71]
	v_mfma_f32_16x16x32_bf16 v[116:119], v[136:139], v[192:195], v[116:119]
	v_mfma_f32_16x16x32_bf16 v[108:111], v[144:147], v[192:195], v[108:111]
	v_mfma_f32_16x16x32_bf16 v[100:103], v[136:139], v[184:187], v[100:103]
	v_mfma_f32_16x16x32_bf16 v[92:95], v[144:147], v[184:187], v[92:95]
	v_mfma_f32_16x16x32_bf16 v[84:87], v[136:139], v[176:179], v[84:87]
	v_mfma_f32_16x16x32_bf16 v[76:79], v[144:147], v[176:179], v[76:79]
	v_mfma_f32_16x16x32_bf16 v[72:75], v[136:139], v[168:171], v[72:75]
	v_mfma_f32_16x16x32_bf16 v[68:71], v[144:147], v[168:171], v[68:71]
	s_barrier
	s_mov_b32 m0, s59
	v_lshl_add_u64 v[220:221], s[36:37], 0, v[196:197]
	s_add_u32 s8, s36, 0x40000
	ds_read_b128 v[188:191], v224 offset:16384
	ds_read_b128 v[192:195], v224 offset:17408
	ds_read_b128 v[180:183], v224 offset:18432
	ds_read_b128 v[184:187], v224 offset:19456
	ds_read_b128 v[172:175], v224 offset:20480
	ds_read_b128 v[176:179], v224 offset:21504
	ds_read_b128 v[164:167], v224 offset:22528
	ds_read_b128 v[168:171], v224 offset:23552
	global_load_lds_dwordx4 v[220:221], off
	v_lshl_add_u64 v[218:219], s[36:37], 0, v[200:201]
	s_mov_b32 m0, s64
	s_addc_u32 s9, s37, 0
	global_load_lds_dwordx4 v[218:219], off
	v_lshl_add_u64 v[214:215], s[8:9], 0, v[196:197]
	s_mov_b32 m0, s65
	v_lshl_add_u64 v[216:217], s[52:53], 0, v[198:199]
	global_load_lds_dwordx4 v[214:215], off
	v_lshl_add_u64 v[214:215], s[8:9], 0, v[200:201]
	s_mov_b32 m0, s68
	s_mov_b64 s[26:27], -1
	global_load_lds_dwordx4 v[214:215], off
	v_lshl_add_u64 v[214:215], s[52:53], 0, v[66:67]
	s_mov_b32 m0, s58
	s_and_b64 vcc, exec, s[54:55]
	global_load_lds_dwordx4 v[214:215], off
	s_mov_b32 m0, s69
	s_nop 0
	global_load_lds_dwordx4 v[216:217], off
	s_cbranch_vccz .LBB0_685
	s_waitcnt vmcnt(8)
	s_mov_b64 s[26:27], 0

.LBB0_703:
	s_waitcnt lgkmcnt(0)
	s_barrier
	v_mfma_f32_16x16x32_bf16 v[62:65], v[150:153], v[190:193], v[62:65]
	v_mfma_f32_16x16x32_bf16 v[58:61], v[158:161], v[190:193], v[58:61]
	v_mfma_f32_16x16x32_bf16 v[54:57], v[150:153], v[182:185], v[54:57]
	v_mfma_f32_16x16x32_bf16 v[50:53], v[158:161], v[182:185], v[50:53]
	v_mfma_f32_16x16x32_bf16 v[46:49], v[150:153], v[174:177], v[46:49]
	v_mfma_f32_16x16x32_bf16 v[42:45], v[158:161], v[174:177], v[42:45]
	v_mfma_f32_16x16x32_bf16 v[38:41], v[150:153], v[166:169], v[38:41]
	v_mfma_f32_16x16x32_bf16 v[34:37], v[158:161], v[166:169], v[34:37]
	v_mfma_f32_16x16x32_bf16 v[62:65], v[154:157], v[194:197], v[62:65]
	v_mfma_f32_16x16x32_bf16 v[58:61], v[162:165], v[194:197], v[58:61]
	v_mfma_f32_16x16x32_bf16 v[54:57], v[154:157], v[186:189], v[54:57]
	v_mfma_f32_16x16x32_bf16 v[50:53], v[162:165], v[186:189], v[50:53]
	v_mfma_f32_16x16x32_bf16 v[46:49], v[154:157], v[178:181], v[46:49]
	v_mfma_f32_16x16x32_bf16 v[42:45], v[162:165], v[178:181], v[42:45]
	v_mfma_f32_16x16x32_bf16 v[38:41], v[154:157], v[170:173], v[38:41]
	v_mfma_f32_16x16x32_bf16 v[34:37], v[162:165], v[170:173], v[34:37]
	v_mfma_f32_16x16x32_bf16 v[30:33], v[134:137], v[190:193], v[30:33]
	v_mfma_f32_16x16x32_bf16 v[26:29], v[142:145], v[190:193], v[26:29]
	v_mfma_f32_16x16x32_bf16 v[22:25], v[134:137], v[182:185], v[22:25]
	v_mfma_f32_16x16x32_bf16 v[18:21], v[142:145], v[182:185], v[18:21]
	v_mfma_f32_16x16x32_bf16 v[14:17], v[134:137], v[174:177], v[14:17]
	v_mfma_f32_16x16x32_bf16 v[10:13], v[142:145], v[174:177], v[10:13]
	v_mfma_f32_16x16x32_bf16 v[6:9], v[134:137], v[166:169], v[6:9]
	v_mfma_f32_16x16x32_bf16 v[2:5], v[142:145], v[166:169], v[2:5]
	v_mfma_f32_16x16x32_bf16 v[30:33], v[138:141], v[194:197], v[30:33]
	v_mfma_f32_16x16x32_bf16 v[26:29], v[146:149], v[194:197], v[26:29]
	v_mfma_f32_16x16x32_bf16 v[22:25], v[138:141], v[186:189], v[22:25]
	v_mfma_f32_16x16x32_bf16 v[18:21], v[146:149], v[186:189], v[18:21]
	v_mfma_f32_16x16x32_bf16 v[14:17], v[138:141], v[178:181], v[14:17]
	v_mfma_f32_16x16x32_bf16 v[10:13], v[146:149], v[178:181], v[10:13]
	v_mfma_f32_16x16x32_bf16 v[6:9], v[138:141], v[170:173], v[6:9]
	v_mfma_f32_16x16x32_bf16 v[2:5], v[146:149], v[170:173], v[2:5]
	s_barrier
	s_add_i32 s11, 0, 0x18000
	v_add_u32_e32 v66, s11, v205
	s_add_i32 s14, 0, 0x1c000
	ds_read_b128 v[134:137], v66
	ds_read_b128 v[138:141], v66 offset:1024
	ds_read_b128 v[142:145], v66 offset:2048
	ds_read_b128 v[146:149], v66 offset:3072
	v_add_u32_e32 v66, s14, v205
	ds_read_b128 v[150:153], v66
	ds_read_b128 v[154:157], v66 offset:1024
	ds_read_b128 v[158:161], v66 offset:2048
	ds_read_b128 v[162:165], v66 offset:3072
	s_add_u32 s12, s64, 0x40000
	s_addc_u32 s13, s65, 0
	s_mov_b32 m0, s85
	v_lshl_add_u64 v[72:73], s[12:13], 0, v[198:199]
	ds_read_b128 v[166:169], v217 offset:32768
	ds_read_b128 v[170:173], v217 offset:33792
	ds_read_b128 v[174:177], v217 offset:34816
	ds_read_b128 v[178:181], v217 offset:35840
	ds_read_b128 v[182:185], v217 offset:36864
	ds_read_b128 v[186:189], v217 offset:37888
	ds_read_b128 v[190:193], v217 offset:38912
	ds_read_b128 v[194:197], v217 offset:39936
	global_load_lds_dwordx4 v[72:73], off
	v_lshl_add_u64 v[72:73], s[12:13], 0, v[202:203]
	s_mov_b32 m0, s86
	s_nop 0
	global_load_lds_dwordx4 v[72:73], off
	s_waitcnt vmcnt(8)
	s_waitcnt lgkmcnt(0)
	s_barrier
	v_mfma_f32_16x16x32_bf16 v[130:133], v[134:137], v[166:169], v[130:133]
	v_mfma_f32_16x16x32_bf16 v[126:129], v[142:145], v[166:169], v[126:129]
	v_mfma_f32_16x16x32_bf16 v[122:125], v[134:137], v[174:177], v[122:125]
	v_mfma_f32_16x16x32_bf16 v[118:121], v[142:145], v[174:177], v[118:121]
	v_mfma_f32_16x16x32_bf16 v[114:117], v[134:137], v[182:185], v[114:117]
	v_mfma_f32_16x16x32_bf16 v[110:113], v[142:145], v[182:185], v[110:113]
	v_mfma_f32_16x16x32_bf16 v[106:109], v[134:137], v[190:193], v[106:109]
	v_mfma_f32_16x16x32_bf16 v[102:105], v[142:145], v[190:193], v[102:105]
	v_mfma_f32_16x16x32_bf16 v[130:133], v[138:141], v[170:173], v[130:133]
	v_mfma_f32_16x16x32_bf16 v[126:129], v[146:149], v[170:173], v[126:129]
	v_mfma_f32_16x16x32_bf16 v[122:125], v[138:141], v[178:181], v[122:125]
	v_mfma_f32_16x16x32_bf16 v[118:121], v[146:149], v[178:181], v[118:121]
	v_mfma_f32_16x16x32_bf16 v[114:117], v[138:141], v[186:189], v[114:117]
	v_mfma_f32_16x16x32_bf16 v[110:113], v[146:149], v[186:189], v[110:113]
	v_mfma_f32_16x16x32_bf16 v[106:109], v[138:141], v[194:197], v[106:109]
	v_mfma_f32_16x16x32_bf16 v[102:105], v[146:149], v[194:197], v[102:105]
	v_mfma_f32_16x16x32_bf16 v[98:101], v[150:153], v[166:169], v[98:101]
	v_mfma_f32_16x16x32_bf16 v[94:97], v[158:161], v[166:169], v[94:97]
	v_mfma_f32_16x16x32_bf16 v[90:93], v[150:153], v[174:177], v[90:93]
	v_mfma_f32_16x16x32_bf16 v[86:89], v[158:161], v[174:177], v[86:89]
	v_mfma_f32_16x16x32_bf16 v[82:85], v[150:153], v[182:185], v[82:85]
	v_mfma_f32_16x16x32_bf16 v[78:81], v[158:161], v[182:185], v[78:81]
	v_mfma_f32_16x16x32_bf16 v[72:75], v[150:153], v[190:193], v[74:77]
	v_mfma_f32_16x16x32_bf16 v[68:71], v[158:161], v[190:193], v[68:71]
	v_mfma_f32_16x16x32_bf16 v[98:101], v[154:157], v[170:173], v[98:101]
	v_mfma_f32_16x16x32_bf16 v[94:97], v[162:165], v[170:173], v[94:97]
	v_mfma_f32_16x16x32_bf16 v[90:93], v[154:157], v[178:181], v[90:93]
	v_mfma_f32_16x16x32_bf16 v[86:89], v[162:165], v[178:181], v[86:89]
	v_mfma_f32_16x16x32_bf16 v[82:85], v[154:157], v[186:189], v[82:85]
	v_mfma_f32_16x16x32_bf16 v[78:81], v[162:165], v[186:189], v[78:81]
	v_mfma_f32_16x16x32_bf16 v[74:77], v[154:157], v[194:197], v[72:75]
	v_mfma_f32_16x16x32_bf16 v[70:73], v[162:165], v[194:197], v[68:71]
	s_barrier
	s_add_i32 s11, s11, s6
	v_lshl_add_u64 v[68:69], v[246:247], 0, s[82:83]
	s_mov_b32 m0, s11
	ds_read_b128 v[166:169], v217 offset:49152
	ds_read_b128 v[170:173], v217 offset:50176
	ds_read_b128 v[174:177], v217 offset:51200
	ds_read_b128 v[178:181], v217 offset:52224
	ds_read_b128 v[182:185], v217 offset:53248
	ds_read_b128 v[186:189], v217 offset:54272
	ds_read_b128 v[190:193], v217 offset:55296
	ds_read_b128 v[194:197], v217 offset:56320
	global_load_lds_dwordx4 v[68:69], off
	s_add_i32 m0, s11, 0x2000
	s_add_u32 s12, s58, 0x20800
	v_lshl_add_u64 v[68:69], v[244:245], 0, s[82:83]
	s_addc_u32 s13, s59, 0
	s_add_i32 s11, s14, s6
	global_load_lds_dwordx4 v[68:69], off
	v_lshl_add_u64 v[68:69], s[12:13], 0, v[200:201]
	s_mov_b32 m0, s11
	s_nop 0
	global_load_lds_dwordx4 v[68:69], off
	v_lshl_add_u64 v[68:69], s[12:13], 0, v[208:209]
	s_add_i32 m0, s11, 0x2000
	s_nop 0
	global_load_lds_dwordx4 v[68:69], off
	v_lshl_add_u64 v[68:69], v[240:241], 0, s[60:61]
	s_mov_b32 m0, s87
	s_nop 0
	global_load_lds_dwordx4 v[68:69], off
	v_lshl_add_u64 v[68:69], v[242:243], 0, s[60:61]
	s_mov_b32 m0, s88
	s_nop 0
	global_load_lds_dwordx4 v[68:69], off
	s_waitcnt vmcnt(8)
	s_waitcnt lgkmcnt(0)
	s_barrier
	v_mfma_f32_16x16x32_bf16 v[62:65], v[134:137], v[166:169], v[62:65]
	v_mfma_f32_16x16x32_bf16 v[58:61], v[142:145], v[166:169], v[58:61]
	v_mfma_f32_16x16x32_bf16 v[54:57], v[134:137], v[174:177], v[54:57]
	v_mfma_f32_16x16x32_bf16 v[50:53], v[142:145], v[174:177], v[50:53]
	v_mfma_f32_16x16x32_bf16 v[46:49], v[134:137], v[182:185], v[46:49]
	v_mfma_f32_16x16x32_bf16 v[42:45], v[142:145], v[182:185], v[42:45]
	v_mfma_f32_16x16x32_bf16 v[38:41], v[134:137], v[190:193], v[38:41]
	v_mfma_f32_16x16x32_bf16 v[34:37], v[142:145], v[190:193], v[34:37]
	v_mfma_f32_16x16x32_bf16 v[62:65], v[138:141], v[170:173], v[62:65]
	v_mfma_f32_16x16x32_bf16 v[58:61], v[146:149], v[170:173], v[58:61]
	v_mfma_f32_16x16x32_bf16 v[54:57], v[138:141], v[178:181], v[54:57]
	v_mfma_f32_16x16x32_bf16 v[50:53], v[146:149], v[178:181], v[50:53]
	v_mfma_f32_16x16x32_bf16 v[46:49], v[138:141], v[186:189], v[46:49]
	v_mfma_f32_16x16x32_bf16 v[42:45], v[146:149], v[186:189], v[42:45]
	v_mfma_f32_16x16x32_bf16 v[38:41], v[138:141], v[194:197], v[38:41]
	v_mfma_f32_16x16x32_bf16 v[34:37], v[146:149], v[194:197], v[34:37]
	v_mfma_f32_16x16x32_bf16 v[30:33], v[150:153], v[166:169], v[30:33]
	v_mfma_f32_16x16x32_bf16 v[26:29], v[158:161], v[166:169], v[26:29]
	v_mfma_f32_16x16x32_bf16 v[22:25], v[150:153], v[174:177], v[22:25]
	v_mfma_f32_16x16x32_bf16 v[18:21], v[158:161], v[174:177], v[18:21]
	v_mfma_f32_16x16x32_bf16 v[14:17], v[150:153], v[182:185], v[14:17]
	v_mfma_f32_16x16x32_bf16 v[10:13], v[158:161], v[182:185], v[10:13]
	v_mfma_f32_16x16x32_bf16 v[6:9], v[150:153], v[190:193], v[6:9]
	v_mfma_f32_16x16x32_bf16 v[2:5], v[158:161], v[190:193], v[2:5]
	v_mfma_f32_16x16x32_bf16 v[30:33], v[154:157], v[170:173], v[30:33]
	v_mfma_f32_16x16x32_bf16 v[26:29], v[162:165], v[170:173], v[26:29]
	v_mfma_f32_16x16x32_bf16 v[22:25], v[154:157], v[178:181], v[22:25]
	v_mfma_f32_16x16x32_bf16 v[18:21], v[162:165], v[178:181], v[18:21]
	v_mfma_f32_16x16x32_bf16 v[14:17], v[154:157], v[186:189], v[14:17]
	v_mfma_f32_16x16x32_bf16 v[10:13], v[162:165], v[186:189], v[10:13]
	v_mfma_f32_16x16x32_bf16 v[6:9], v[154:157], v[194:197], v[6:9]
	v_mfma_f32_16x16x32_bf16 v[2:5], v[162:165], v[194:197], v[2:5]
	s_barrier
	s_add_i32 s10, s10, 2
	s_add_u32 s54, s54, 0x100
	s_addc_u32 s55, s55, 0
	s_add_u32 s8, s8, 0x1000
	s_addc_u32 s9, s9, 0
	s_cmp_gt_u32 s10, 5
	s_cbranch_scc1 .LBB0_712

.LBB0_708:
	s_add_u32 s11, s38, s54
	s_addc_u32 s12, s39, s55
	s_add_u32 s11, s11, 0x100
	s_addc_u32 s12, s12, 0
	s_waitcnt lgkmcnt(0)
	s_cmpk_eq_i32 s54, 0x300
	s_cselect_b32 s65, s53, s12
	s_cselect_b32 s64, s52, s11
	s_cselect_b32 s59, s57, s9
	s_cselect_b32 s58, s56, s8
	s_barrier
	v_mfma_f32_16x16x32_bf16 v[130:133], v[150:153], v[190:193], v[130:133]
	v_mfma_f32_16x16x32_bf16 v[126:129], v[158:161], v[190:193], v[126:129]
	v_mfma_f32_16x16x32_bf16 v[122:125], v[150:153], v[182:185], v[122:125]
	v_mfma_f32_16x16x32_bf16 v[118:121], v[158:161], v[182:185], v[118:121]
	v_mfma_f32_16x16x32_bf16 v[114:117], v[150:153], v[174:177], v[114:117]
	v_mfma_f32_16x16x32_bf16 v[110:113], v[158:161], v[174:177], v[110:113]
	v_mfma_f32_16x16x32_bf16 v[106:109], v[150:153], v[166:169], v[106:109]
	v_mfma_f32_16x16x32_bf16 v[102:105], v[158:161], v[166:169], v[102:105]
	v_mfma_f32_16x16x32_bf16 v[130:133], v[154:157], v[194:197], v[130:133]
	v_mfma_f32_16x16x32_bf16 v[126:129], v[162:165], v[194:197], v[126:129]
	v_mfma_f32_16x16x32_bf16 v[122:125], v[154:157], v[186:189], v[122:125]
	v_mfma_f32_16x16x32_bf16 v[118:121], v[162:165], v[186:189], v[118:121]
	v_mfma_f32_16x16x32_bf16 v[114:117], v[154:157], v[178:181], v[114:117]
	v_mfma_f32_16x16x32_bf16 v[110:113], v[162:165], v[178:181], v[110:113]
	v_mfma_f32_16x16x32_bf16 v[106:109], v[154:157], v[170:173], v[106:109]
	v_mfma_f32_16x16x32_bf16 v[102:105], v[162:165], v[170:173], v[102:105]
	v_mfma_f32_16x16x32_bf16 v[98:101], v[134:137], v[190:193], v[98:101]
	v_mfma_f32_16x16x32_bf16 v[94:97], v[142:145], v[190:193], v[94:97]
	v_mfma_f32_16x16x32_bf16 v[90:93], v[134:137], v[182:185], v[90:93]
	v_mfma_f32_16x16x32_bf16 v[86:89], v[142:145], v[182:185], v[86:89]
	v_mfma_f32_16x16x32_bf16 v[82:85], v[134:137], v[174:177], v[82:85]
	v_mfma_f32_16x16x32_bf16 v[78:81], v[142:145], v[174:177], v[78:81]
	v_mfma_f32_16x16x32_bf16 v[74:77], v[134:137], v[166:169], v[74:77]
	v_mfma_f32_16x16x32_bf16 v[68:71], v[142:145], v[166:169], v[70:73]
	v_mfma_f32_16x16x32_bf16 v[98:101], v[138:141], v[194:197], v[98:101]
	v_mfma_f32_16x16x32_bf16 v[94:97], v[146:149], v[194:197], v[94:97]
	v_mfma_f32_16x16x32_bf16 v[90:93], v[138:141], v[186:189], v[90:93]
	v_mfma_f32_16x16x32_bf16 v[86:89], v[146:149], v[186:189], v[86:89]
	v_mfma_f32_16x16x32_bf16 v[82:85], v[138:141], v[178:181], v[82:85]
	v_mfma_f32_16x16x32_bf16 v[78:81], v[146:149], v[178:181], v[78:81]
	v_mfma_f32_16x16x32_bf16 v[74:77], v[138:141], v[170:173], v[74:77]
	v_mfma_f32_16x16x32_bf16 v[68:71], v[146:149], v[170:173], v[68:71]
	s_barrier
	s_mov_b32 m0, s68
	v_lshl_add_u64 v[246:247], s[58:59], 0, v[200:201]
	s_add_u32 s12, s58, 0x20000
	ds_read_b128 v[190:193], v217 offset:16384
	ds_read_b128 v[194:197], v217 offset:17408
	ds_read_b128 v[182:185], v217 offset:18432
	ds_read_b128 v[186:189], v217 offset:19456
	ds_read_b128 v[174:177], v217 offset:20480
	ds_read_b128 v[178:181], v217 offset:21504
	ds_read_b128 v[166:169], v217 offset:22528
	ds_read_b128 v[170:173], v217 offset:23552
	global_load_lds_dwordx4 v[246:247], off
	v_lshl_add_u64 v[244:245], s[58:59], 0, v[208:209]
	s_mov_b32 m0, s69
	s_addc_u32 s13, s59, 0
	global_load_lds_dwordx4 v[244:245], off
	v_lshl_add_u64 v[72:73], s[12:13], 0, v[200:201]
	s_mov_b32 m0, s70
	v_lshl_add_u64 v[240:241], s[64:65], 0, v[198:199]
	global_load_lds_dwordx4 v[72:73], off
	v_lshl_add_u64 v[72:73], s[12:13], 0, v[208:209]
	s_mov_b32 m0, s71
	v_lshl_add_u64 v[242:243], s[64:65], 0, v[202:203]
	global_load_lds_dwordx4 v[72:73], off
	s_mov_b32 m0, s7
	s_mov_b64 s[26:27], -1
	global_load_lds_dwordx4 v[240:241], off
	s_mov_b32 m0, s84
	s_and_b64 vcc, exec, s[66:67]
	global_load_lds_dwordx4 v[242:243], off
	s_cbranch_vccz .LBB0_710
	s_waitcnt vmcnt(8)
	s_mov_b64 s[26:27], 0

.LBB0_799:
	s_waitcnt lgkmcnt(0)
	s_barrier
	v_mfma_f32_16x16x32_bf16 v[62:65], v[148:151], v[188:191], v[62:65]
	v_mfma_f32_16x16x32_bf16 v[58:61], v[156:159], v[188:191], v[58:61]
	v_mfma_f32_16x16x32_bf16 v[46:49], v[148:151], v[180:183], v[46:49]
	v_mfma_f32_16x16x32_bf16 v[42:45], v[156:159], v[180:183], v[42:45]
	v_mfma_f32_16x16x32_bf16 v[30:33], v[148:151], v[172:175], v[30:33]
	v_mfma_f32_16x16x32_bf16 v[26:29], v[156:159], v[172:175], v[26:29]
	v_mfma_f32_16x16x32_bf16 v[14:17], v[148:151], v[164:167], v[14:17]
	v_mfma_f32_16x16x32_bf16 v[10:13], v[156:159], v[164:167], v[10:13]
	v_mfma_f32_16x16x32_bf16 v[62:65], v[152:155], v[192:195], v[62:65]
	v_mfma_f32_16x16x32_bf16 v[58:61], v[160:163], v[192:195], v[58:61]
	v_mfma_f32_16x16x32_bf16 v[46:49], v[152:155], v[184:187], v[46:49]
	v_mfma_f32_16x16x32_bf16 v[42:45], v[160:163], v[184:187], v[42:45]
	v_mfma_f32_16x16x32_bf16 v[30:33], v[152:155], v[176:179], v[30:33]
	v_mfma_f32_16x16x32_bf16 v[26:29], v[160:163], v[176:179], v[26:29]
	v_mfma_f32_16x16x32_bf16 v[14:17], v[152:155], v[168:171], v[14:17]
	v_mfma_f32_16x16x32_bf16 v[10:13], v[160:163], v[168:171], v[10:13]
	v_mfma_f32_16x16x32_bf16 v[54:57], v[132:135], v[188:191], v[54:57]
	v_mfma_f32_16x16x32_bf16 v[50:53], v[140:143], v[188:191], v[50:53]
	v_mfma_f32_16x16x32_bf16 v[38:41], v[132:135], v[180:183], v[38:41]
	v_mfma_f32_16x16x32_bf16 v[34:37], v[140:143], v[180:183], v[34:37]
	v_mfma_f32_16x16x32_bf16 v[22:25], v[132:135], v[172:175], v[22:25]
	v_mfma_f32_16x16x32_bf16 v[18:21], v[140:143], v[172:175], v[18:21]
	v_mfma_f32_16x16x32_bf16 v[6:9], v[132:135], v[164:167], v[6:9]
	v_mfma_f32_16x16x32_bf16 v[2:5], v[140:143], v[164:167], v[2:5]
	v_mfma_f32_16x16x32_bf16 v[54:57], v[136:139], v[192:195], v[54:57]
	v_mfma_f32_16x16x32_bf16 v[50:53], v[144:147], v[192:195], v[50:53]
	v_mfma_f32_16x16x32_bf16 v[38:41], v[136:139], v[184:187], v[38:41]
	v_mfma_f32_16x16x32_bf16 v[34:37], v[144:147], v[184:187], v[34:37]
	v_mfma_f32_16x16x32_bf16 v[22:25], v[136:139], v[176:179], v[22:25]
	v_mfma_f32_16x16x32_bf16 v[18:21], v[144:147], v[176:179], v[18:21]
	v_mfma_f32_16x16x32_bf16 v[6:9], v[136:139], v[168:171], v[6:9]
	v_mfma_f32_16x16x32_bf16 v[2:5], v[144:147], v[168:171], v[2:5]
	s_barrier
	s_add_i32 s9, 0, 0x18000
	s_add_i32 s12, 0, 0x1c000
	v_add_u32_e32 v144, s9, v225
	v_add_u32_e32 v160, s12, v225
	ds_read_b128 v[132:135], v144
	ds_read_b128 v[136:139], v144 offset:1024
	ds_read_b128 v[140:143], v144 offset:2048
	ds_read_b128 v[144:147], v144 offset:3072
	ds_read_b128 v[148:151], v160
	ds_read_b128 v[152:155], v160 offset:1024
	ds_read_b128 v[156:159], v160 offset:2048
	ds_read_b128 v[160:163], v160 offset:3072
	s_add_u32 s10, s66, 0x100000
	s_addc_u32 s11, s67, 0
	s_mov_b32 m0, s88
	v_lshl_add_u64 v[228:229], s[10:11], 0, v[196:197]
	ds_read_b128 v[164:167], v226 offset:32768
	ds_read_b128 v[168:171], v226 offset:33792
	ds_read_b128 v[172:175], v226 offset:34816
	ds_read_b128 v[176:179], v226 offset:35840
	ds_read_b128 v[180:183], v226 offset:36864
	ds_read_b128 v[184:187], v226 offset:37888
	ds_read_b128 v[188:191], v226 offset:38912
	ds_read_b128 v[192:195], v226 offset:39936
	global_load_lds_dwordx4 v[228:229], off
	v_lshl_add_u64 v[228:229], s[10:11], 0, v[200:201]
	s_mov_b32 m0, s89
	s_nop 0
	global_load_lds_dwordx4 v[228:229], off
	s_waitcnt vmcnt(8)
	s_waitcnt lgkmcnt(0)
	s_barrier
	v_mfma_f32_16x16x32_bf16 v[128:131], v[132:135], v[164:167], v[128:131]
	v_mfma_f32_16x16x32_bf16 v[124:127], v[140:143], v[164:167], v[124:127]
	v_mfma_f32_16x16x32_bf16 v[112:115], v[132:135], v[172:175], v[112:115]
	v_mfma_f32_16x16x32_bf16 v[108:111], v[140:143], v[172:175], v[108:111]
	v_mfma_f32_16x16x32_bf16 v[96:99], v[132:135], v[180:183], v[96:99]
	v_mfma_f32_16x16x32_bf16 v[92:95], v[140:143], v[180:183], v[92:95]
	v_mfma_f32_16x16x32_bf16 v[80:83], v[132:135], v[188:191], v[80:83]
	v_mfma_f32_16x16x32_bf16 v[76:79], v[140:143], v[188:191], v[76:79]
	v_mfma_f32_16x16x32_bf16 v[128:131], v[136:139], v[168:171], v[128:131]
	v_mfma_f32_16x16x32_bf16 v[124:127], v[144:147], v[168:171], v[124:127]
	v_mfma_f32_16x16x32_bf16 v[112:115], v[136:139], v[176:179], v[112:115]
	v_mfma_f32_16x16x32_bf16 v[108:111], v[144:147], v[176:179], v[108:111]
	v_mfma_f32_16x16x32_bf16 v[96:99], v[136:139], v[184:187], v[96:99]
	v_mfma_f32_16x16x32_bf16 v[92:95], v[144:147], v[184:187], v[92:95]
	v_mfma_f32_16x16x32_bf16 v[80:83], v[136:139], v[192:195], v[80:83]
	v_mfma_f32_16x16x32_bf16 v[76:79], v[144:147], v[192:195], v[76:79]
	v_mfma_f32_16x16x32_bf16 v[120:123], v[148:151], v[164:167], v[120:123]
	v_mfma_f32_16x16x32_bf16 v[116:119], v[156:159], v[164:167], v[116:119]
	v_mfma_f32_16x16x32_bf16 v[104:107], v[148:151], v[172:175], v[104:107]
	v_mfma_f32_16x16x32_bf16 v[100:103], v[156:159], v[172:175], v[100:103]
	v_mfma_f32_16x16x32_bf16 v[88:91], v[148:151], v[180:183], v[88:91]
	v_mfma_f32_16x16x32_bf16 v[84:87], v[156:159], v[180:183], v[84:87]
	v_mfma_f32_16x16x32_bf16 v[72:75], v[148:151], v[188:191], v[72:75]
	v_mfma_f32_16x16x32_bf16 v[68:71], v[156:159], v[188:191], v[68:71]
	v_mfma_f32_16x16x32_bf16 v[120:123], v[152:155], v[168:171], v[120:123]
	v_mfma_f32_16x16x32_bf16 v[116:119], v[160:163], v[168:171], v[116:119]
	v_mfma_f32_16x16x32_bf16 v[104:107], v[152:155], v[176:179], v[104:107]
	v_mfma_f32_16x16x32_bf16 v[100:103], v[160:163], v[176:179], v[100:103]
	v_mfma_f32_16x16x32_bf16 v[88:91], v[152:155], v[184:187], v[88:91]
	v_mfma_f32_16x16x32_bf16 v[84:87], v[160:163], v[184:187], v[84:87]
	v_mfma_f32_16x16x32_bf16 v[72:75], v[152:155], v[192:195], v[72:75]
	v_mfma_f32_16x16x32_bf16 v[68:71], v[160:163], v[192:195], v[68:71]
	s_barrier
	s_add_i32 s9, s9, s72
	v_lshl_add_u64 v[222:223], v[222:223], 0, s[60:61]
	s_mov_b32 m0, s9
	ds_read_b128 v[164:167], v226 offset:49152
	ds_read_b128 v[168:171], v226 offset:50176
	ds_read_b128 v[172:175], v226 offset:51200
	ds_read_b128 v[176:179], v226 offset:52224
	ds_read_b128 v[180:183], v226 offset:53248
	ds_read_b128 v[184:187], v226 offset:54272
	ds_read_b128 v[188:191], v226 offset:55296
	ds_read_b128 v[192:195], v226 offset:56320
	global_load_lds_dwordx4 v[222:223], off
	s_add_i32 m0, s9, 0x2000
	s_add_u32 s10, s36, 0x40080
	v_lshl_add_u64 v[220:221], v[220:221], 0, s[60:61]
	s_addc_u32 s11, s37, 0
	s_add_i32 s9, s12, s72
	global_load_lds_dwordx4 v[220:221], off
	v_lshl_add_u64 v[220:221], s[10:11], 0, v[198:199]
	s_mov_b32 m0, s9
	v_lshl_add_u64 v[216:217], v[216:217], 0, s[60:61]
	global_load_lds_dwordx4 v[220:221], off
	v_lshl_add_u64 v[220:221], s[10:11], 0, v[202:203]
	s_add_i32 m0, s9, 0x2000
	s_nop 0
	global_load_lds_dwordx4 v[220:221], off
	s_mov_b32 m0, s91
	s_nop 0
	global_load_lds_dwordx4 v[216:217], off
	v_lshl_add_u64 v[216:217], v[218:219], 0, s[60:61]
	s_mov_b32 m0, s92
	s_nop 0
	global_load_lds_dwordx4 v[216:217], off
	s_waitcnt vmcnt(8)
	s_waitcnt lgkmcnt(0)
	s_barrier
	v_mfma_f32_16x16x32_bf16 v[62:65], v[132:135], v[164:167], v[62:65]
	v_mfma_f32_16x16x32_bf16 v[58:61], v[140:143], v[164:167], v[58:61]
	v_mfma_f32_16x16x32_bf16 v[46:49], v[132:135], v[172:175], v[46:49]
	v_mfma_f32_16x16x32_bf16 v[42:45], v[140:143], v[172:175], v[42:45]
	v_mfma_f32_16x16x32_bf16 v[30:33], v[132:135], v[180:183], v[30:33]
	v_mfma_f32_16x16x32_bf16 v[26:29], v[140:143], v[180:183], v[26:29]
	v_mfma_f32_16x16x32_bf16 v[14:17], v[132:135], v[188:191], v[14:17]
	v_mfma_f32_16x16x32_bf16 v[10:13], v[140:143], v[188:191], v[10:13]
	v_mfma_f32_16x16x32_bf16 v[62:65], v[136:139], v[168:171], v[62:65]
	v_mfma_f32_16x16x32_bf16 v[58:61], v[144:147], v[168:171], v[58:61]
	v_mfma_f32_16x16x32_bf16 v[46:49], v[136:139], v[176:179], v[46:49]
	v_mfma_f32_16x16x32_bf16 v[42:45], v[144:147], v[176:179], v[42:45]
	v_mfma_f32_16x16x32_bf16 v[30:33], v[136:139], v[184:187], v[30:33]
	v_mfma_f32_16x16x32_bf16 v[26:29], v[144:147], v[184:187], v[26:29]
	v_mfma_f32_16x16x32_bf16 v[14:17], v[136:139], v[192:195], v[14:17]
	v_mfma_f32_16x16x32_bf16 v[10:13], v[144:147], v[192:195], v[10:13]
	v_mfma_f32_16x16x32_bf16 v[54:57], v[148:151], v[164:167], v[54:57]
	v_mfma_f32_16x16x32_bf16 v[50:53], v[156:159], v[164:167], v[50:53]
	v_mfma_f32_16x16x32_bf16 v[38:41], v[148:151], v[172:175], v[38:41]
	v_mfma_f32_16x16x32_bf16 v[34:37], v[156:159], v[172:175], v[34:37]
	v_mfma_f32_16x16x32_bf16 v[22:25], v[148:151], v[180:183], v[22:25]
	v_mfma_f32_16x16x32_bf16 v[18:21], v[156:159], v[180:183], v[18:21]
	v_mfma_f32_16x16x32_bf16 v[6:9], v[148:151], v[188:191], v[6:9]
	v_mfma_f32_16x16x32_bf16 v[2:5], v[156:159], v[188:191], v[2:5]
	v_mfma_f32_16x16x32_bf16 v[54:57], v[152:155], v[168:171], v[54:57]
	v_mfma_f32_16x16x32_bf16 v[50:53], v[160:163], v[168:171], v[50:53]
	v_mfma_f32_16x16x32_bf16 v[38:41], v[152:155], v[176:179], v[38:41]
	v_mfma_f32_16x16x32_bf16 v[34:37], v[160:163], v[176:179], v[34:37]
	v_mfma_f32_16x16x32_bf16 v[22:25], v[152:155], v[184:187], v[22:25]
	v_mfma_f32_16x16x32_bf16 v[18:21], v[160:163], v[184:187], v[18:21]
	v_mfma_f32_16x16x32_bf16 v[6:9], v[152:155], v[192:195], v[6:9]
	v_mfma_f32_16x16x32_bf16 v[2:5], v[160:163], v[192:195], v[2:5]
	s_barrier
	s_add_i32 s8, s8, 2
	s_add_u32 s58, s58, 0x100
	s_addc_u32 s59, s59, 0
	s_cmp_gt_u32 s8, 13
	s_cbranch_scc1 .LBB0_808

.LBB0_804:
	s_add_u32 s9, s40, s58
	s_addc_u32 s10, s41, s59
	s_add_u32 s9, s9, 0x100
	s_addc_u32 s10, s10, 0
	s_add_u32 s11, s70, s58
	s_addc_u32 s12, s71, s59
	s_waitcnt lgkmcnt(0)
	s_cmpk_eq_i32 s58, 0x700
	s_cselect_b32 s67, s53, s10
	s_cselect_b32 s66, s52, s9
	s_cselect_b32 s37, s55, s12
	s_cselect_b32 s36, s54, s11
	s_barrier
	v_mfma_f32_16x16x32_bf16 v[128:131], v[148:151], v[188:191], v[128:131]
	v_mfma_f32_16x16x32_bf16 v[124:127], v[156:159], v[188:191], v[124:127]
	v_mfma_f32_16x16x32_bf16 v[112:115], v[148:151], v[180:183], v[112:115]
	v_mfma_f32_16x16x32_bf16 v[108:111], v[156:159], v[180:183], v[108:111]
	v_mfma_f32_16x16x32_bf16 v[96:99], v[148:151], v[172:175], v[96:99]
	v_mfma_f32_16x16x32_bf16 v[92:95], v[156:159], v[172:175], v[92:95]
	v_mfma_f32_16x16x32_bf16 v[80:83], v[148:151], v[164:167], v[80:83]
	v_mfma_f32_16x16x32_bf16 v[76:79], v[156:159], v[164:167], v[76:79]
	v_mfma_f32_16x16x32_bf16 v[128:131], v[152:155], v[192:195], v[128:131]
	v_mfma_f32_16x16x32_bf16 v[124:127], v[160:163], v[192:195], v[124:127]
	v_mfma_f32_16x16x32_bf16 v[112:115], v[152:155], v[184:187], v[112:115]
	v_mfma_f32_16x16x32_bf16 v[108:111], v[160:163], v[184:187], v[108:111]
	v_mfma_f32_16x16x32_bf16 v[96:99], v[152:155], v[176:179], v[96:99]
	v_mfma_f32_16x16x32_bf16 v[92:95], v[160:163], v[176:179], v[92:95]
	v_mfma_f32_16x16x32_bf16 v[80:83], v[152:155], v[168:171], v[80:83]
	v_mfma_f32_16x16x32_bf16 v[76:79], v[160:163], v[168:171], v[76:79]
	v_mfma_f32_16x16x32_bf16 v[120:123], v[132:135], v[188:191], v[120:123]
	v_mfma_f32_16x16x32_bf16 v[116:119], v[140:143], v[188:191], v[116:119]
	v_mfma_f32_16x16x32_bf16 v[104:107], v[132:135], v[180:183], v[104:107]
	v_mfma_f32_16x16x32_bf16 v[100:103], v[140:143], v[180:183], v[100:103]
	v_mfma_f32_16x16x32_bf16 v[88:91], v[132:135], v[172:175], v[88:91]
	v_mfma_f32_16x16x32_bf16 v[84:87], v[140:143], v[172:175], v[84:87]
	v_mfma_f32_16x16x32_bf16 v[72:75], v[132:135], v[164:167], v[72:75]
	v_mfma_f32_16x16x32_bf16 v[68:71], v[140:143], v[164:167], v[68:71]
	v_mfma_f32_16x16x32_bf16 v[120:123], v[136:139], v[192:195], v[120:123]
	v_mfma_f32_16x16x32_bf16 v[116:119], v[144:147], v[192:195], v[116:119]
	v_mfma_f32_16x16x32_bf16 v[104:107], v[136:139], v[184:187], v[104:107]
	v_mfma_f32_16x16x32_bf16 v[100:103], v[144:147], v[184:187], v[100:103]
	v_mfma_f32_16x16x32_bf16 v[88:91], v[136:139], v[176:179], v[88:91]
	v_mfma_f32_16x16x32_bf16 v[84:87], v[144:147], v[176:179], v[84:87]
	v_mfma_f32_16x16x32_bf16 v[72:75], v[136:139], v[168:171], v[72:75]
	v_mfma_f32_16x16x32_bf16 v[68:71], v[144:147], v[168:171], v[68:71]
	s_barrier
	s_mov_b32 m0, s75
	v_lshl_add_u64 v[222:223], s[36:37], 0, v[198:199]
	s_add_u32 s10, s36, 0x40000
	ds_read_b128 v[188:191], v226 offset:16384
	ds_read_b128 v[192:195], v226 offset:17408
	ds_read_b128 v[180:183], v226 offset:18432
	ds_read_b128 v[184:187], v226 offset:19456
	ds_read_b128 v[172:175], v226 offset:20480
	ds_read_b128 v[176:179], v226 offset:21504
	ds_read_b128 v[164:167], v226 offset:22528
	ds_read_b128 v[168:171], v226 offset:23552
	global_load_lds_dwordx4 v[222:223], off
	v_lshl_add_u64 v[220:221], s[36:37], 0, v[202:203]
	s_mov_b32 m0, s84
	s_addc_u32 s11, s37, 0
	global_load_lds_dwordx4 v[220:221], off
	v_lshl_add_u64 v[216:217], s[10:11], 0, v[198:199]
	s_mov_b32 m0, s85
	v_lshl_add_u64 v[218:219], s[66:67], 0, v[200:201]
	global_load_lds_dwordx4 v[216:217], off
	v_lshl_add_u64 v[216:217], s[10:11], 0, v[202:203]
	s_mov_b32 m0, s86
	s_mov_b64 s[26:27], -1
	global_load_lds_dwordx4 v[216:217], off
	v_lshl_add_u64 v[216:217], s[66:67], 0, v[196:197]
	s_mov_b32 m0, s74
	s_and_b64 vcc, exec, s[68:69]
	global_load_lds_dwordx4 v[216:217], off
	s_mov_b32 m0, s87
	s_nop 0
	global_load_lds_dwordx4 v[218:219], off
	s_cbranch_vccz .LBB0_806
	s_waitcnt vmcnt(8)
	s_mov_b64 s[26:27], 0

.LBB0_911:
	s_add_u32 s10, s52, 0xfff80080
	s_addc_u32 s11, s53, -1
	s_add_i32 s12, 0, 0x10000
	s_cmp_eq_u32 s71, 28
	s_cselect_b32 s55, s47, s11
	s_cselect_b32 s54, s46, s10
	s_cselect_b32 s37, s49, s9
	s_cselect_b32 s36, s48, s8
	s_add_i32 s13, 0, 0x14000
	v_add_u32_e32 v158, s12, v147
	v_add_u32_e32 v174, s13, v147
	ds_read_b128 v[142:145], v158
	ds_read_b128 v[150:153], v158 offset:1024
	ds_read_b128 v[154:157], v158 offset:2048
	ds_read_b128 v[158:161], v158 offset:3072
	ds_read_b128 v[162:165], v174
	ds_read_b128 v[166:169], v174 offset:1024
	ds_read_b128 v[170:173], v174 offset:2048
	ds_read_b128 v[174:177], v174 offset:3072
	v_lshl_add_u64 v[202:203], s[52:53], 0, v[138:139]
	s_add_i32 m0, s59, 0xc000
	ds_read_b128 v[178:181], v149
	ds_read_b128 v[182:185], v149 offset:1024
	ds_read_b128 v[186:189], v149 offset:2048
	ds_read_b128 v[190:193], v149 offset:3072
	ds_read_b128 v[194:197], v149 offset:4096
	ds_read_b128 v[198:201], v149 offset:5120
	ds_read_b128 v[208:211], v149 offset:6144
	ds_read_b128 v[212:215], v149 offset:7168
	global_load_lds_dwordx4 v[202:203], off
	v_lshl_add_u64 v[202:203], s[52:53], 0, v[140:141]
	s_add_i32 m0, s59, 0xe000
	s_nop 0
	global_load_lds_dwordx4 v[202:203], off
	s_waitcnt vmcnt(8)
	s_waitcnt lgkmcnt(0)
	s_barrier
	v_mfma_f32_16x16x32_bf16 v[128:131], v[142:145], v[178:181], v[128:131]
	v_mfma_f32_16x16x32_bf16 v[124:127], v[154:157], v[178:181], v[124:127]
	v_mfma_f32_16x16x32_bf16 v[116:119], v[142:145], v[186:189], v[116:119]
	v_mfma_f32_16x16x32_bf16 v[108:111], v[154:157], v[186:189], v[108:111]
	v_mfma_f32_16x16x32_bf16 v[100:103], v[142:145], v[194:197], v[100:103]
	v_mfma_f32_16x16x32_bf16 v[92:95], v[154:157], v[194:197], v[92:95]
	v_mfma_f32_16x16x32_bf16 v[84:87], v[142:145], v[208:211], v[84:87]
	v_mfma_f32_16x16x32_bf16 v[76:79], v[154:157], v[208:211], v[76:79]
	v_mfma_f32_16x16x32_bf16 v[128:131], v[150:153], v[182:185], v[128:131]
	v_mfma_f32_16x16x32_bf16 v[124:127], v[158:161], v[182:185], v[124:127]
	v_mfma_f32_16x16x32_bf16 v[116:119], v[150:153], v[190:193], v[116:119]
	v_mfma_f32_16x16x32_bf16 v[108:111], v[158:161], v[190:193], v[108:111]
	v_mfma_f32_16x16x32_bf16 v[100:103], v[150:153], v[198:201], v[100:103]
	v_mfma_f32_16x16x32_bf16 v[92:95], v[158:161], v[198:201], v[92:95]
	v_mfma_f32_16x16x32_bf16 v[84:87], v[150:153], v[212:215], v[84:87]
	v_mfma_f32_16x16x32_bf16 v[76:79], v[158:161], v[212:215], v[76:79]
	v_mfma_f32_16x16x32_bf16 v[120:123], v[162:165], v[178:181], v[120:123]
	v_mfma_f32_16x16x32_bf16 v[112:115], v[170:173], v[178:181], v[112:115]
	v_mfma_f32_16x16x32_bf16 v[104:107], v[162:165], v[186:189], v[104:107]
	v_mfma_f32_16x16x32_bf16 v[96:99], v[170:173], v[186:189], v[96:99]
	v_mfma_f32_16x16x32_bf16 v[88:91], v[162:165], v[194:197], v[88:91]
	v_mfma_f32_16x16x32_bf16 v[80:83], v[170:173], v[194:197], v[80:83]
	v_mfma_f32_16x16x32_bf16 v[72:75], v[162:165], v[208:211], v[72:75]
	v_mfma_f32_16x16x32_bf16 v[68:71], v[170:173], v[208:211], v[68:71]
	v_mfma_f32_16x16x32_bf16 v[120:123], v[166:169], v[182:185], v[120:123]
	v_mfma_f32_16x16x32_bf16 v[112:115], v[174:177], v[182:185], v[112:115]
	v_mfma_f32_16x16x32_bf16 v[104:107], v[166:169], v[190:193], v[104:107]
	v_mfma_f32_16x16x32_bf16 v[96:99], v[174:177], v[190:193], v[96:99]
	v_mfma_f32_16x16x32_bf16 v[88:91], v[166:169], v[198:201], v[88:91]
	v_mfma_f32_16x16x32_bf16 v[80:83], v[174:177], v[198:201], v[80:83]
	v_mfma_f32_16x16x32_bf16 v[72:75], v[166:169], v[212:215], v[72:75]
	v_mfma_f32_16x16x32_bf16 v[68:71], v[174:177], v[212:215], v[68:71]
	s_barrier
	s_add_i32 s10, s12, s58
	v_lshl_add_u64 v[202:203], s[36:37], 0, v[66:67]
	s_mov_b32 m0, s10
	ds_read_b128 v[178:181], v149 offset:16384
	ds_read_b128 v[182:185], v149 offset:17408
	ds_read_b128 v[186:189], v149 offset:18432
	ds_read_b128 v[190:193], v149 offset:19456
	ds_read_b128 v[194:197], v149 offset:20480
	ds_read_b128 v[198:201], v149 offset:21504
	ds_read_b128 v[208:211], v149 offset:22528
	ds_read_b128 v[212:215], v149 offset:23552
	global_load_lds_dwordx4 v[202:203], off
	s_add_i32 m0, s10, 0x2000
	s_add_u32 s10, s36, 0x80000
	v_lshl_add_u64 v[216:217], s[36:37], 0, v[136:137]
	s_addc_u32 s11, s37, 0
	s_add_i32 s12, s13, s58
	global_load_lds_dwordx4 v[216:217], off
	v_lshl_add_u64 v[218:219], s[10:11], 0, v[66:67]
	s_mov_b32 m0, s12
	v_lshl_add_u64 v[220:221], s[54:55], 0, v[134:135]
	global_load_lds_dwordx4 v[218:219], off
	v_lshl_add_u64 v[218:219], s[10:11], 0, v[136:137]
	s_add_i32 m0, s12, 0x2000
	s_nop 0
	global_load_lds_dwordx4 v[218:219], off
	v_lshl_add_u64 v[218:219], s[54:55], 0, v[132:133]
	s_mov_b32 m0, s59
	s_nop 0
	global_load_lds_dwordx4 v[218:219], off
	s_mov_b32 m0, s64
	s_nop 0
	global_load_lds_dwordx4 v[220:221], off
	s_waitcnt vmcnt(8)
	s_waitcnt lgkmcnt(0)
	s_barrier
	v_mfma_f32_16x16x32_bf16 v[62:65], v[142:145], v[178:181], v[62:65]
	v_mfma_f32_16x16x32_bf16 v[58:61], v[154:157], v[178:181], v[58:61]
	v_mfma_f32_16x16x32_bf16 v[50:53], v[142:145], v[186:189], v[50:53]
	v_mfma_f32_16x16x32_bf16 v[42:45], v[154:157], v[186:189], v[42:45]
	v_mfma_f32_16x16x32_bf16 v[34:37], v[142:145], v[194:197], v[34:37]
	v_mfma_f32_16x16x32_bf16 v[26:29], v[154:157], v[194:197], v[26:29]
	v_mfma_f32_16x16x32_bf16 v[18:21], v[142:145], v[208:211], v[18:21]
	v_mfma_f32_16x16x32_bf16 v[10:13], v[154:157], v[208:211], v[10:13]
	v_mfma_f32_16x16x32_bf16 v[62:65], v[150:153], v[182:185], v[62:65]
	v_mfma_f32_16x16x32_bf16 v[58:61], v[158:161], v[182:185], v[58:61]
	v_mfma_f32_16x16x32_bf16 v[50:53], v[150:153], v[190:193], v[50:53]
	v_mfma_f32_16x16x32_bf16 v[42:45], v[158:161], v[190:193], v[42:45]
	v_mfma_f32_16x16x32_bf16 v[34:37], v[150:153], v[198:201], v[34:37]
	v_mfma_f32_16x16x32_bf16 v[26:29], v[158:161], v[198:201], v[26:29]
	v_mfma_f32_16x16x32_bf16 v[18:21], v[150:153], v[212:215], v[18:21]
	v_mfma_f32_16x16x32_bf16 v[10:13], v[158:161], v[212:215], v[10:13]
	v_mfma_f32_16x16x32_bf16 v[54:57], v[162:165], v[178:181], v[54:57]
	v_mfma_f32_16x16x32_bf16 v[46:49], v[170:173], v[178:181], v[46:49]
	v_mfma_f32_16x16x32_bf16 v[38:41], v[162:165], v[186:189], v[38:41]
	v_mfma_f32_16x16x32_bf16 v[30:33], v[170:173], v[186:189], v[30:33]
	v_mfma_f32_16x16x32_bf16 v[22:25], v[162:165], v[194:197], v[22:25]
	v_mfma_f32_16x16x32_bf16 v[14:17], v[170:173], v[194:197], v[14:17]
	v_mfma_f32_16x16x32_bf16 v[6:9], v[162:165], v[208:211], v[6:9]
	v_mfma_f32_16x16x32_bf16 v[2:5], v[170:173], v[208:211], v[2:5]
	v_mfma_f32_16x16x32_bf16 v[54:57], v[166:169], v[182:185], v[54:57]
	v_mfma_f32_16x16x32_bf16 v[46:49], v[174:177], v[182:185], v[46:49]
	v_mfma_f32_16x16x32_bf16 v[38:41], v[166:169], v[190:193], v[38:41]
	v_mfma_f32_16x16x32_bf16 v[30:33], v[174:177], v[190:193], v[30:33]
	v_mfma_f32_16x16x32_bf16 v[22:25], v[166:169], v[198:201], v[22:25]
	v_mfma_f32_16x16x32_bf16 v[14:17], v[174:177], v[198:201], v[14:17]
	v_mfma_f32_16x16x32_bf16 v[6:9], v[166:169], v[212:215], v[6:9]
	v_mfma_f32_16x16x32_bf16 v[2:5], v[174:177], v[212:215], v[2:5]
	s_barrier
	s_add_i32 s12, 0, 0x18000
	s_add_i32 s13, 0, 0x1c000
	v_add_u32_e32 v158, s12, v147
	v_add_u32_e32 v174, s13, v147
	ds_read_b128 v[142:145], v158
	ds_read_b128 v[150:153], v158 offset:1024
	ds_read_b128 v[154:157], v158 offset:2048
	ds_read_b128 v[158:161], v158 offset:3072
	ds_read_b128 v[162:165], v174
	ds_read_b128 v[166:169], v174 offset:1024
	ds_read_b128 v[170:173], v174 offset:2048
	ds_read_b128 v[174:177], v174 offset:3072
	s_add_u32 s10, s54, 0x80000
	s_addc_u32 s11, s55, 0
	s_mov_b32 m0, s65
	v_lshl_add_u64 v[222:223], s[10:11], 0, v[132:133]
	ds_read_b128 v[178:181], v149 offset:32768
	ds_read_b128 v[182:185], v149 offset:33792
	ds_read_b128 v[186:189], v149 offset:34816
	ds_read_b128 v[190:193], v149 offset:35840
	ds_read_b128 v[194:197], v149 offset:36864
	ds_read_b128 v[198:201], v149 offset:37888
	ds_read_b128 v[208:211], v149 offset:38912
	ds_read_b128 v[212:215], v149 offset:39936
	global_load_lds_dwordx4 v[222:223], off
	v_lshl_add_u64 v[222:223], s[10:11], 0, v[134:135]
	s_mov_b32 m0, s66
	s_nop 0
	global_load_lds_dwordx4 v[222:223], off
	s_waitcnt vmcnt(8)
	s_waitcnt lgkmcnt(0)
	s_barrier
	v_mfma_f32_16x16x32_bf16 v[128:131], v[142:145], v[178:181], v[128:131]
	v_mfma_f32_16x16x32_bf16 v[124:127], v[154:157], v[178:181], v[124:127]
	v_mfma_f32_16x16x32_bf16 v[116:119], v[142:145], v[186:189], v[116:119]
	v_mfma_f32_16x16x32_bf16 v[108:111], v[154:157], v[186:189], v[108:111]
	v_mfma_f32_16x16x32_bf16 v[100:103], v[142:145], v[194:197], v[100:103]
	v_mfma_f32_16x16x32_bf16 v[92:95], v[154:157], v[194:197], v[92:95]
	v_mfma_f32_16x16x32_bf16 v[84:87], v[142:145], v[208:211], v[84:87]
	v_mfma_f32_16x16x32_bf16 v[76:79], v[154:157], v[208:211], v[76:79]
	v_mfma_f32_16x16x32_bf16 v[128:131], v[150:153], v[182:185], v[128:131]
	v_mfma_f32_16x16x32_bf16 v[124:127], v[158:161], v[182:185], v[124:127]
	v_mfma_f32_16x16x32_bf16 v[116:119], v[150:153], v[190:193], v[116:119]
	v_mfma_f32_16x16x32_bf16 v[108:111], v[158:161], v[190:193], v[108:111]
	v_mfma_f32_16x16x32_bf16 v[100:103], v[150:153], v[198:201], v[100:103]
	v_mfma_f32_16x16x32_bf16 v[92:95], v[158:161], v[198:201], v[92:95]
	v_mfma_f32_16x16x32_bf16 v[84:87], v[150:153], v[212:215], v[84:87]
	v_mfma_f32_16x16x32_bf16 v[76:79], v[158:161], v[212:215], v[76:79]
	v_mfma_f32_16x16x32_bf16 v[120:123], v[162:165], v[178:181], v[120:123]
	v_mfma_f32_16x16x32_bf16 v[112:115], v[170:173], v[178:181], v[112:115]
	v_mfma_f32_16x16x32_bf16 v[104:107], v[162:165], v[186:189], v[104:107]
	v_mfma_f32_16x16x32_bf16 v[96:99], v[170:173], v[186:189], v[96:99]
	v_mfma_f32_16x16x32_bf16 v[88:91], v[162:165], v[194:197], v[88:91]
	v_mfma_f32_16x16x32_bf16 v[80:83], v[170:173], v[194:197], v[80:83]
	v_mfma_f32_16x16x32_bf16 v[72:75], v[162:165], v[208:211], v[72:75]
	v_mfma_f32_16x16x32_bf16 v[68:71], v[170:173], v[208:211], v[68:71]
	v_mfma_f32_16x16x32_bf16 v[120:123], v[166:169], v[182:185], v[120:123]
	v_mfma_f32_16x16x32_bf16 v[112:115], v[174:177], v[182:185], v[112:115]
	v_mfma_f32_16x16x32_bf16 v[104:107], v[166:169], v[190:193], v[104:107]
	v_mfma_f32_16x16x32_bf16 v[96:99], v[174:177], v[190:193], v[96:99]
	v_mfma_f32_16x16x32_bf16 v[88:91], v[166:169], v[198:201], v[88:91]
	v_mfma_f32_16x16x32_bf16 v[80:83], v[174:177], v[198:201], v[80:83]
	v_mfma_f32_16x16x32_bf16 v[72:75], v[166:169], v[212:215], v[72:75]
	v_mfma_f32_16x16x32_bf16 v[68:71], v[174:177], v[212:215], v[68:71]
	s_barrier
	s_add_i32 s10, s12, s58
	v_lshl_add_u64 v[202:203], v[202:203], 0, s[60:61]
	s_mov_b32 m0, s10
	ds_read_b128 v[178:181], v149 offset:49152
	ds_read_b128 v[182:185], v149 offset:50176
	ds_read_b128 v[186:189], v149 offset:51200
	ds_read_b128 v[190:193], v149 offset:52224
	ds_read_b128 v[194:197], v149 offset:53248
	ds_read_b128 v[198:201], v149 offset:54272
	ds_read_b128 v[208:211], v149 offset:55296
	ds_read_b128 v[212:215], v149 offset:56320
	global_load_lds_dwordx4 v[202:203], off
	s_add_i32 m0, s10, 0x2000
	s_add_u32 s10, s36, 0x80080
	v_lshl_add_u64 v[202:203], v[216:217], 0, s[60:61]
	s_addc_u32 s11, s37, 0
	s_add_i32 s12, s13, s58
	global_load_lds_dwordx4 v[202:203], off
	v_lshl_add_u64 v[202:203], s[10:11], 0, v[66:67]
	s_mov_b32 m0, s12
	s_nop 0
	global_load_lds_dwordx4 v[202:203], off
	v_lshl_add_u64 v[202:203], s[10:11], 0, v[136:137]
	s_add_i32 m0, s12, 0x2000
	s_nop 0
	global_load_lds_dwordx4 v[202:203], off
	v_lshl_add_u64 v[202:203], v[218:219], 0, s[60:61]
	s_mov_b32 m0, s67
	s_nop 0
	global_load_lds_dwordx4 v[202:203], off
	v_lshl_add_u64 v[202:203], v[220:221], 0, s[60:61]
	s_mov_b32 m0, s68
	s_nop 0
	global_load_lds_dwordx4 v[202:203], off
	s_waitcnt vmcnt(8)
	s_waitcnt lgkmcnt(0)
	s_barrier
	v_mfma_f32_16x16x32_bf16 v[62:65], v[142:145], v[178:181], v[62:65]
	v_mfma_f32_16x16x32_bf16 v[58:61], v[154:157], v[178:181], v[58:61]
	v_mfma_f32_16x16x32_bf16 v[50:53], v[142:145], v[186:189], v[50:53]
	v_mfma_f32_16x16x32_bf16 v[42:45], v[154:157], v[186:189], v[42:45]
	v_mfma_f32_16x16x32_bf16 v[34:37], v[142:145], v[194:197], v[34:37]
	v_mfma_f32_16x16x32_bf16 v[26:29], v[154:157], v[194:197], v[26:29]
	v_mfma_f32_16x16x32_bf16 v[18:21], v[142:145], v[208:211], v[18:21]
	v_mfma_f32_16x16x32_bf16 v[10:13], v[154:157], v[208:211], v[10:13]
	v_mfma_f32_16x16x32_bf16 v[62:65], v[150:153], v[182:185], v[62:65]
	v_mfma_f32_16x16x32_bf16 v[58:61], v[158:161], v[182:185], v[58:61]
	v_mfma_f32_16x16x32_bf16 v[50:53], v[150:153], v[190:193], v[50:53]
	v_mfma_f32_16x16x32_bf16 v[42:45], v[158:161], v[190:193], v[42:45]
	v_mfma_f32_16x16x32_bf16 v[34:37], v[150:153], v[198:201], v[34:37]
	v_mfma_f32_16x16x32_bf16 v[26:29], v[158:161], v[198:201], v[26:29]
	v_mfma_f32_16x16x32_bf16 v[18:21], v[150:153], v[212:215], v[18:21]
	v_mfma_f32_16x16x32_bf16 v[10:13], v[158:161], v[212:215], v[10:13]
	v_mfma_f32_16x16x32_bf16 v[54:57], v[162:165], v[178:181], v[54:57]
	v_mfma_f32_16x16x32_bf16 v[46:49], v[170:173], v[178:181], v[46:49]
	v_mfma_f32_16x16x32_bf16 v[38:41], v[162:165], v[186:189], v[38:41]
	v_mfma_f32_16x16x32_bf16 v[30:33], v[170:173], v[186:189], v[30:33]
	v_mfma_f32_16x16x32_bf16 v[22:25], v[162:165], v[194:197], v[22:25]
	v_mfma_f32_16x16x32_bf16 v[14:17], v[170:173], v[194:197], v[14:17]
	v_mfma_f32_16x16x32_bf16 v[6:9], v[162:165], v[208:211], v[6:9]
	v_mfma_f32_16x16x32_bf16 v[2:5], v[170:173], v[208:211], v[2:5]
	v_mfma_f32_16x16x32_bf16 v[54:57], v[166:169], v[182:185], v[54:57]
	v_mfma_f32_16x16x32_bf16 v[46:49], v[174:177], v[182:185], v[46:49]
	v_mfma_f32_16x16x32_bf16 v[38:41], v[166:169], v[190:193], v[38:41]
	v_mfma_f32_16x16x32_bf16 v[30:33], v[174:177], v[190:193], v[30:33]
	v_mfma_f32_16x16x32_bf16 v[22:25], v[166:169], v[198:201], v[22:25]
	v_mfma_f32_16x16x32_bf16 v[14:17], v[174:177], v[198:201], v[14:17]
	v_mfma_f32_16x16x32_bf16 v[6:9], v[166:169], v[212:215], v[6:9]
	v_mfma_f32_16x16x32_bf16 v[2:5], v[174:177], v[212:215], v[2:5]
	s_barrier
	s_add_i32 s71, s71, 2
	s_add_u32 s52, s52, 0x100
	s_addc_u32 s53, s53, 0
	s_add_u32 s8, s8, 0x100
	s_addc_u32 s9, s9, 0
	s_cmp_gt_u32 s71, 29
	s_cbranch_scc0 .LBB0_911
	s_and_b64 vcc, exec, s[44:45]
	s_cbranch_vccz .LBB0_914
	s_barrier

.LBB0_927:
	s_add_u32 s10, s50, 0xfffc0080
	s_addc_u32 s11, s51, -1
	s_add_i32 s12, 0, 0x10000
	s_cmp_eq_u32 s67, 12
	s_cselect_b32 s53, s45, s11
	s_cselect_b32 s52, s44, s10
	s_cselect_b32 s37, s47, s9
	s_cselect_b32 s36, s46, s8
	s_add_i32 s13, 0, 0x14000
	v_add_u32_e32 v144, s12, v171
	v_add_u32_e32 v174, s13, v171
	ds_read_b128 v[132:135], v144
	ds_read_b128 v[136:139], v144 offset:1024
	ds_read_b128 v[140:143], v144 offset:2048
	ds_read_b128 v[144:147], v144 offset:3072
	ds_read_b128 v[148:151], v174
	ds_read_b128 v[162:165], v174 offset:1024
	ds_read_b128 v[166:169], v174 offset:2048
	ds_read_b128 v[174:177], v174 offset:3072
	v_lshl_add_u64 v[202:203], s[50:51], 0, v[158:159]
	s_add_i32 m0, s55, 0xc000
	ds_read_b128 v[178:181], v173
	ds_read_b128 v[182:185], v173 offset:1024
	ds_read_b128 v[186:189], v173 offset:2048
	ds_read_b128 v[190:193], v173 offset:3072
	ds_read_b128 v[194:197], v173 offset:4096
	ds_read_b128 v[198:201], v173 offset:5120
	ds_read_b128 v[208:211], v173 offset:6144
	ds_read_b128 v[212:215], v173 offset:7168
	global_load_lds_dwordx4 v[202:203], off
	v_lshl_add_u64 v[202:203], s[50:51], 0, v[160:161]
	s_add_i32 m0, s55, 0xe000
	s_nop 0
	global_load_lds_dwordx4 v[202:203], off
	s_waitcnt vmcnt(8)
	s_waitcnt lgkmcnt(0)
	s_barrier
	v_mfma_f32_16x16x32_bf16 v[128:131], v[132:135], v[178:181], v[128:131]
	v_mfma_f32_16x16x32_bf16 v[124:127], v[140:143], v[178:181], v[124:127]
	v_mfma_f32_16x16x32_bf16 v[112:115], v[132:135], v[186:189], v[112:115]
	v_mfma_f32_16x16x32_bf16 v[108:111], v[140:143], v[186:189], v[108:111]
	v_mfma_f32_16x16x32_bf16 v[96:99], v[132:135], v[194:197], v[96:99]
	v_mfma_f32_16x16x32_bf16 v[92:95], v[140:143], v[194:197], v[92:95]
	v_mfma_f32_16x16x32_bf16 v[80:83], v[132:135], v[208:211], v[80:83]
	v_mfma_f32_16x16x32_bf16 v[76:79], v[140:143], v[208:211], v[76:79]
	v_mfma_f32_16x16x32_bf16 v[128:131], v[136:139], v[182:185], v[128:131]
	v_mfma_f32_16x16x32_bf16 v[124:127], v[144:147], v[182:185], v[124:127]
	v_mfma_f32_16x16x32_bf16 v[112:115], v[136:139], v[190:193], v[112:115]
	v_mfma_f32_16x16x32_bf16 v[108:111], v[144:147], v[190:193], v[108:111]
	v_mfma_f32_16x16x32_bf16 v[96:99], v[136:139], v[198:201], v[96:99]
	v_mfma_f32_16x16x32_bf16 v[92:95], v[144:147], v[198:201], v[92:95]
	v_mfma_f32_16x16x32_bf16 v[80:83], v[136:139], v[212:215], v[80:83]
	v_mfma_f32_16x16x32_bf16 v[76:79], v[144:147], v[212:215], v[76:79]
	v_mfma_f32_16x16x32_bf16 v[120:123], v[148:151], v[178:181], v[120:123]
	v_mfma_f32_16x16x32_bf16 v[116:119], v[166:169], v[178:181], v[116:119]
	v_mfma_f32_16x16x32_bf16 v[104:107], v[148:151], v[186:189], v[104:107]
	v_mfma_f32_16x16x32_bf16 v[100:103], v[166:169], v[186:189], v[100:103]
	v_mfma_f32_16x16x32_bf16 v[88:91], v[148:151], v[194:197], v[88:91]
	v_mfma_f32_16x16x32_bf16 v[84:87], v[166:169], v[194:197], v[84:87]
	v_mfma_f32_16x16x32_bf16 v[72:75], v[148:151], v[208:211], v[72:75]
	v_mfma_f32_16x16x32_bf16 v[68:71], v[166:169], v[208:211], v[68:71]
	v_mfma_f32_16x16x32_bf16 v[120:123], v[162:165], v[182:185], v[120:123]
	v_mfma_f32_16x16x32_bf16 v[116:119], v[174:177], v[182:185], v[116:119]
	v_mfma_f32_16x16x32_bf16 v[104:107], v[162:165], v[190:193], v[104:107]
	v_mfma_f32_16x16x32_bf16 v[100:103], v[174:177], v[190:193], v[100:103]
	v_mfma_f32_16x16x32_bf16 v[88:91], v[162:165], v[198:201], v[88:91]
	v_mfma_f32_16x16x32_bf16 v[84:87], v[174:177], v[198:201], v[84:87]
	v_mfma_f32_16x16x32_bf16 v[72:75], v[162:165], v[212:215], v[72:75]
	v_mfma_f32_16x16x32_bf16 v[68:71], v[174:177], v[212:215], v[68:71]
	s_barrier
	s_add_i32 s10, s12, s54
	v_lshl_add_u64 v[202:203], s[36:37], 0, v[66:67]
	s_mov_b32 m0, s10
	ds_read_b128 v[178:181], v173 offset:16384
	ds_read_b128 v[182:185], v173 offset:17408
	ds_read_b128 v[186:189], v173 offset:18432
	ds_read_b128 v[190:193], v173 offset:19456
	ds_read_b128 v[194:197], v173 offset:20480
	ds_read_b128 v[198:201], v173 offset:21504
	ds_read_b128 v[208:211], v173 offset:22528
	ds_read_b128 v[212:215], v173 offset:23552
	global_load_lds_dwordx4 v[202:203], off
	s_add_i32 m0, s10, 0x2000
	s_add_u32 s10, s36, 0x40000
	v_lshl_add_u64 v[216:217], s[36:37], 0, v[156:157]
	s_addc_u32 s11, s37, 0
	s_add_i32 s12, s13, s54
	global_load_lds_dwordx4 v[216:217], off
	v_lshl_add_u64 v[218:219], s[10:11], 0, v[66:67]
	s_mov_b32 m0, s12
	v_lshl_add_u64 v[220:221], s[52:53], 0, v[154:155]
	global_load_lds_dwordx4 v[218:219], off
	v_lshl_add_u64 v[218:219], s[10:11], 0, v[156:157]
	s_add_i32 m0, s12, 0x2000
	s_nop 0
	global_load_lds_dwordx4 v[218:219], off
	v_lshl_add_u64 v[218:219], s[52:53], 0, v[152:153]
	s_mov_b32 m0, s55
	s_nop 0
	global_load_lds_dwordx4 v[218:219], off
	s_mov_b32 m0, s56
	s_nop 0
	global_load_lds_dwordx4 v[220:221], off
	s_waitcnt vmcnt(8)
	s_waitcnt lgkmcnt(0)
	s_barrier
	v_mfma_f32_16x16x32_bf16 v[62:65], v[132:135], v[178:181], v[62:65]
	v_mfma_f32_16x16x32_bf16 v[58:61], v[140:143], v[178:181], v[58:61]
	v_mfma_f32_16x16x32_bf16 v[46:49], v[132:135], v[186:189], v[46:49]
	v_mfma_f32_16x16x32_bf16 v[42:45], v[140:143], v[186:189], v[42:45]
	v_mfma_f32_16x16x32_bf16 v[30:33], v[132:135], v[194:197], v[30:33]
	v_mfma_f32_16x16x32_bf16 v[26:29], v[140:143], v[194:197], v[26:29]
	v_mfma_f32_16x16x32_bf16 v[14:17], v[132:135], v[208:211], v[14:17]
	v_mfma_f32_16x16x32_bf16 v[10:13], v[140:143], v[208:211], v[10:13]
	v_mfma_f32_16x16x32_bf16 v[62:65], v[136:139], v[182:185], v[62:65]
	v_mfma_f32_16x16x32_bf16 v[58:61], v[144:147], v[182:185], v[58:61]
	v_mfma_f32_16x16x32_bf16 v[46:49], v[136:139], v[190:193], v[46:49]
	v_mfma_f32_16x16x32_bf16 v[42:45], v[144:147], v[190:193], v[42:45]
	v_mfma_f32_16x16x32_bf16 v[30:33], v[136:139], v[198:201], v[30:33]
	v_mfma_f32_16x16x32_bf16 v[26:29], v[144:147], v[198:201], v[26:29]
	v_mfma_f32_16x16x32_bf16 v[14:17], v[136:139], v[212:215], v[14:17]
	v_mfma_f32_16x16x32_bf16 v[10:13], v[144:147], v[212:215], v[10:13]
	v_mfma_f32_16x16x32_bf16 v[54:57], v[148:151], v[178:181], v[54:57]
	v_mfma_f32_16x16x32_bf16 v[50:53], v[166:169], v[178:181], v[50:53]
	v_mfma_f32_16x16x32_bf16 v[38:41], v[148:151], v[186:189], v[38:41]
	v_mfma_f32_16x16x32_bf16 v[34:37], v[166:169], v[186:189], v[34:37]
	v_mfma_f32_16x16x32_bf16 v[22:25], v[148:151], v[194:197], v[22:25]
	v_mfma_f32_16x16x32_bf16 v[18:21], v[166:169], v[194:197], v[18:21]
	v_mfma_f32_16x16x32_bf16 v[6:9], v[148:151], v[208:211], v[6:9]
	v_mfma_f32_16x16x32_bf16 v[2:5], v[166:169], v[208:211], v[2:5]
	v_mfma_f32_16x16x32_bf16 v[54:57], v[162:165], v[182:185], v[54:57]
	v_mfma_f32_16x16x32_bf16 v[50:53], v[174:177], v[182:185], v[50:53]
	v_mfma_f32_16x16x32_bf16 v[38:41], v[162:165], v[190:193], v[38:41]
	v_mfma_f32_16x16x32_bf16 v[34:37], v[174:177], v[190:193], v[34:37]
	v_mfma_f32_16x16x32_bf16 v[22:25], v[162:165], v[198:201], v[22:25]
	v_mfma_f32_16x16x32_bf16 v[18:21], v[174:177], v[198:201], v[18:21]
	v_mfma_f32_16x16x32_bf16 v[6:9], v[162:165], v[212:215], v[6:9]
	v_mfma_f32_16x16x32_bf16 v[2:5], v[174:177], v[212:215], v[2:5]
	s_barrier
	s_add_i32 s12, 0, 0x18000
	s_add_i32 s13, 0, 0x1c000
	v_add_u32_e32 v144, s12, v171
	v_add_u32_e32 v174, s13, v171
	ds_read_b128 v[132:135], v144
	ds_read_b128 v[136:139], v144 offset:1024
	ds_read_b128 v[140:143], v144 offset:2048
	ds_read_b128 v[144:147], v144 offset:3072
	ds_read_b128 v[148:151], v174
	ds_read_b128 v[162:165], v174 offset:1024
	ds_read_b128 v[166:169], v174 offset:2048
	ds_read_b128 v[174:177], v174 offset:3072
	s_add_u32 s10, s52, 0x40000
	s_addc_u32 s11, s53, 0
	s_mov_b32 m0, s57
	v_lshl_add_u64 v[222:223], s[10:11], 0, v[152:153]
	ds_read_b128 v[178:181], v173 offset:32768
	ds_read_b128 v[182:185], v173 offset:33792
	ds_read_b128 v[186:189], v173 offset:34816
	ds_read_b128 v[190:193], v173 offset:35840
	ds_read_b128 v[194:197], v173 offset:36864
	ds_read_b128 v[198:201], v173 offset:37888
	ds_read_b128 v[208:211], v173 offset:38912
	ds_read_b128 v[212:215], v173 offset:39936
	global_load_lds_dwordx4 v[222:223], off
	v_lshl_add_u64 v[222:223], s[10:11], 0, v[154:155]
	s_mov_b32 m0, s58
	s_nop 0
	global_load_lds_dwordx4 v[222:223], off
	s_waitcnt vmcnt(8)
	s_waitcnt lgkmcnt(0)
	s_barrier
	v_mfma_f32_16x16x32_bf16 v[128:131], v[132:135], v[178:181], v[128:131]
	v_mfma_f32_16x16x32_bf16 v[124:127], v[140:143], v[178:181], v[124:127]
	v_mfma_f32_16x16x32_bf16 v[112:115], v[132:135], v[186:189], v[112:115]
	v_mfma_f32_16x16x32_bf16 v[108:111], v[140:143], v[186:189], v[108:111]
	v_mfma_f32_16x16x32_bf16 v[96:99], v[132:135], v[194:197], v[96:99]
	v_mfma_f32_16x16x32_bf16 v[92:95], v[140:143], v[194:197], v[92:95]
	v_mfma_f32_16x16x32_bf16 v[80:83], v[132:135], v[208:211], v[80:83]
	v_mfma_f32_16x16x32_bf16 v[76:79], v[140:143], v[208:211], v[76:79]
	v_mfma_f32_16x16x32_bf16 v[128:131], v[136:139], v[182:185], v[128:131]
	v_mfma_f32_16x16x32_bf16 v[124:127], v[144:147], v[182:185], v[124:127]
	v_mfma_f32_16x16x32_bf16 v[112:115], v[136:139], v[190:193], v[112:115]
	v_mfma_f32_16x16x32_bf16 v[108:111], v[144:147], v[190:193], v[108:111]
	v_mfma_f32_16x16x32_bf16 v[96:99], v[136:139], v[198:201], v[96:99]
	v_mfma_f32_16x16x32_bf16 v[92:95], v[144:147], v[198:201], v[92:95]
	v_mfma_f32_16x16x32_bf16 v[80:83], v[136:139], v[212:215], v[80:83]
	v_mfma_f32_16x16x32_bf16 v[76:79], v[144:147], v[212:215], v[76:79]
	v_mfma_f32_16x16x32_bf16 v[120:123], v[148:151], v[178:181], v[120:123]
	v_mfma_f32_16x16x32_bf16 v[116:119], v[166:169], v[178:181], v[116:119]
	v_mfma_f32_16x16x32_bf16 v[104:107], v[148:151], v[186:189], v[104:107]
	v_mfma_f32_16x16x32_bf16 v[100:103], v[166:169], v[186:189], v[100:103]
	v_mfma_f32_16x16x32_bf16 v[88:91], v[148:151], v[194:197], v[88:91]
	v_mfma_f32_16x16x32_bf16 v[84:87], v[166:169], v[194:197], v[84:87]
	v_mfma_f32_16x16x32_bf16 v[72:75], v[148:151], v[208:211], v[72:75]
	v_mfma_f32_16x16x32_bf16 v[68:71], v[166:169], v[208:211], v[68:71]
	v_mfma_f32_16x16x32_bf16 v[120:123], v[162:165], v[182:185], v[120:123]
	v_mfma_f32_16x16x32_bf16 v[116:119], v[174:177], v[182:185], v[116:119]
	v_mfma_f32_16x16x32_bf16 v[104:107], v[162:165], v[190:193], v[104:107]
	v_mfma_f32_16x16x32_bf16 v[100:103], v[174:177], v[190:193], v[100:103]
	v_mfma_f32_16x16x32_bf16 v[88:91], v[162:165], v[198:201], v[88:91]
	v_mfma_f32_16x16x32_bf16 v[84:87], v[174:177], v[198:201], v[84:87]
	v_mfma_f32_16x16x32_bf16 v[72:75], v[162:165], v[212:215], v[72:75]
	v_mfma_f32_16x16x32_bf16 v[68:71], v[174:177], v[212:215], v[68:71]
	s_barrier
	s_add_i32 s10, s12, s54
	v_lshl_add_u64 v[202:203], v[202:203], 0, s[60:61]
	s_mov_b32 m0, s10
	ds_read_b128 v[178:181], v173 offset:49152
	ds_read_b128 v[182:185], v173 offset:50176
	ds_read_b128 v[186:189], v173 offset:51200
	ds_read_b128 v[190:193], v173 offset:52224
	ds_read_b128 v[194:197], v173 offset:53248
	ds_read_b128 v[198:201], v173 offset:54272
	ds_read_b128 v[208:211], v173 offset:55296
	ds_read_b128 v[212:215], v173 offset:56320
	global_load_lds_dwordx4 v[202:203], off
	s_add_i32 m0, s10, 0x2000
	s_add_u32 s10, s36, 0x40080
	v_lshl_add_u64 v[202:203], v[216:217], 0, s[60:61]
	s_addc_u32 s11, s37, 0
	s_add_i32 s12, s13, s54
	global_load_lds_dwordx4 v[202:203], off
	v_lshl_add_u64 v[202:203], s[10:11], 0, v[66:67]
	s_mov_b32 m0, s12
	s_nop 0
	global_load_lds_dwordx4 v[202:203], off
	v_lshl_add_u64 v[202:203], s[10:11], 0, v[156:157]
	s_add_i32 m0, s12, 0x2000
	s_nop 0
	global_load_lds_dwordx4 v[202:203], off
	v_lshl_add_u64 v[202:203], v[218:219], 0, s[60:61]
	s_mov_b32 m0, s59
	s_nop 0
	global_load_lds_dwordx4 v[202:203], off
	v_lshl_add_u64 v[202:203], v[220:221], 0, s[60:61]
	s_mov_b32 m0, s64
	s_nop 0
	global_load_lds_dwordx4 v[202:203], off
	s_waitcnt vmcnt(8)
	s_waitcnt lgkmcnt(0)
	s_barrier
	v_mfma_f32_16x16x32_bf16 v[62:65], v[132:135], v[178:181], v[62:65]
	v_mfma_f32_16x16x32_bf16 v[58:61], v[140:143], v[178:181], v[58:61]
	v_mfma_f32_16x16x32_bf16 v[46:49], v[132:135], v[186:189], v[46:49]
	v_mfma_f32_16x16x32_bf16 v[42:45], v[140:143], v[186:189], v[42:45]
	v_mfma_f32_16x16x32_bf16 v[30:33], v[132:135], v[194:197], v[30:33]
	v_mfma_f32_16x16x32_bf16 v[26:29], v[140:143], v[194:197], v[26:29]
	v_mfma_f32_16x16x32_bf16 v[14:17], v[132:135], v[208:211], v[14:17]
	v_mfma_f32_16x16x32_bf16 v[10:13], v[140:143], v[208:211], v[10:13]
	v_mfma_f32_16x16x32_bf16 v[62:65], v[136:139], v[182:185], v[62:65]
	v_mfma_f32_16x16x32_bf16 v[58:61], v[144:147], v[182:185], v[58:61]
	v_mfma_f32_16x16x32_bf16 v[46:49], v[136:139], v[190:193], v[46:49]
	v_mfma_f32_16x16x32_bf16 v[42:45], v[144:147], v[190:193], v[42:45]
	v_mfma_f32_16x16x32_bf16 v[30:33], v[136:139], v[198:201], v[30:33]
	v_mfma_f32_16x16x32_bf16 v[26:29], v[144:147], v[198:201], v[26:29]
	v_mfma_f32_16x16x32_bf16 v[14:17], v[136:139], v[212:215], v[14:17]
	v_mfma_f32_16x16x32_bf16 v[10:13], v[144:147], v[212:215], v[10:13]
	v_mfma_f32_16x16x32_bf16 v[54:57], v[148:151], v[178:181], v[54:57]
	v_mfma_f32_16x16x32_bf16 v[50:53], v[166:169], v[178:181], v[50:53]
	v_mfma_f32_16x16x32_bf16 v[38:41], v[148:151], v[186:189], v[38:41]
	v_mfma_f32_16x16x32_bf16 v[34:37], v[166:169], v[186:189], v[34:37]
	v_mfma_f32_16x16x32_bf16 v[22:25], v[148:151], v[194:197], v[22:25]
	v_mfma_f32_16x16x32_bf16 v[18:21], v[166:169], v[194:197], v[18:21]
	v_mfma_f32_16x16x32_bf16 v[6:9], v[148:151], v[208:211], v[6:9]
	v_mfma_f32_16x16x32_bf16 v[2:5], v[166:169], v[208:211], v[2:5]
	v_mfma_f32_16x16x32_bf16 v[54:57], v[162:165], v[182:185], v[54:57]
	v_mfma_f32_16x16x32_bf16 v[50:53], v[174:177], v[182:185], v[50:53]
	v_mfma_f32_16x16x32_bf16 v[38:41], v[162:165], v[190:193], v[38:41]
	v_mfma_f32_16x16x32_bf16 v[34:37], v[174:177], v[190:193], v[34:37]
	v_mfma_f32_16x16x32_bf16 v[22:25], v[162:165], v[198:201], v[22:25]
	v_mfma_f32_16x16x32_bf16 v[18:21], v[174:177], v[198:201], v[18:21]
	v_mfma_f32_16x16x32_bf16 v[6:9], v[162:165], v[212:215], v[6:9]
	v_mfma_f32_16x16x32_bf16 v[2:5], v[174:177], v[212:215], v[2:5]
	s_barrier
	s_add_i32 s67, s67, 2
	s_add_u32 s50, s50, 0x100
	s_addc_u32 s51, s51, 0
	s_add_u32 s8, s8, 0x100
	s_addc_u32 s9, s9, 0
	s_cmp_gt_u32 s67, 13
	s_cbranch_scc0 .LBB0_927
	s_and_b64 vcc, exec, s[42:43]
	s_cbranch_vccz .LBB0_930
	s_barrier

.LBB0_998:
	s_add_u32 s10, s34, 0xfffc0080
	s_addc_u32 s11, s35, -1
	s_add_i32 s42, 0, 0x10000
	s_cmp_eq_u32 s26, 12
	s_cselect_b32 s41, s55, s11
	s_cselect_b32 s40, s54, s10
	s_cselect_b32 s37, s57, s9
	s_cselect_b32 s36, s56, s8
	s_add_i32 s12, 0, 0x14000
	v_add_u32_e32 v72, s42, v218
	v_add_u32_e32 v96, s12, v218
	ds_read_b128 v[58:61], v72
	ds_read_b128 v[62:65], v72 offset:1024
	ds_read_b128 v[68:71], v72 offset:2048
	ds_read_b128 v[72:75], v72 offset:3072
	ds_read_b128 v[84:87], v96
	ds_read_b128 v[88:91], v96 offset:1024
	ds_read_b128 v[92:95], v96 offset:2048
	ds_read_b128 v[96:99], v96 offset:3072
	v_lshl_add_u64 v[202:203], s[34:35], 0, v[186:187]
	s_add_i32 m0, s85, 0xc000
	ds_read_b128 v[164:167], v219
	ds_read_b128 v[168:171], v219 offset:1024
	ds_read_b128 v[190:193], v219 offset:2048
	ds_read_b128 v[194:197], v219 offset:3072
	ds_read_b128 v[198:201], v219 offset:4096
	ds_read_b128 v[208:211], v219 offset:5120
	ds_read_b128 v[212:215], v219 offset:6144
	ds_read_b128 v[220:223], v219 offset:7168
	global_load_lds_dwordx4 v[202:203], off
	v_lshl_add_u64 v[202:203], s[34:35], 0, v[188:189]
	s_add_i32 m0, s85, 0xe000
	s_nop 0
	global_load_lds_dwordx4 v[202:203], off
	s_waitcnt vmcnt(8)
	s_waitcnt lgkmcnt(0)
	s_barrier
	v_mfma_f32_16x16x32_bf16 v[160:163], v[58:61], v[164:167], v[160:163]
	v_mfma_f32_16x16x32_bf16 v[156:159], v[68:71], v[164:167], v[156:159]
	v_mfma_f32_16x16x32_bf16 v[144:147], v[58:61], v[190:193], v[144:147]
	v_mfma_f32_16x16x32_bf16 v[140:143], v[68:71], v[190:193], v[140:143]
	v_mfma_f32_16x16x32_bf16 v[128:131], v[58:61], v[198:201], v[128:131]
	v_mfma_f32_16x16x32_bf16 v[124:127], v[68:71], v[198:201], v[124:127]
	v_mfma_f32_16x16x32_bf16 v[112:115], v[58:61], v[212:215], v[112:115]
	v_mfma_f32_16x16x32_bf16 v[108:111], v[68:71], v[212:215], v[108:111]
	v_mfma_f32_16x16x32_bf16 v[160:163], v[62:65], v[168:171], v[160:163]
	v_mfma_f32_16x16x32_bf16 v[156:159], v[72:75], v[168:171], v[156:159]
	v_mfma_f32_16x16x32_bf16 v[144:147], v[62:65], v[194:197], v[144:147]
	v_mfma_f32_16x16x32_bf16 v[140:143], v[72:75], v[194:197], v[140:143]
	v_mfma_f32_16x16x32_bf16 v[128:131], v[62:65], v[208:211], v[128:131]
	v_mfma_f32_16x16x32_bf16 v[124:127], v[72:75], v[208:211], v[124:127]
	v_mfma_f32_16x16x32_bf16 v[112:115], v[62:65], v[220:223], v[112:115]
	v_mfma_f32_16x16x32_bf16 v[108:111], v[72:75], v[220:223], v[108:111]
	v_mfma_f32_16x16x32_bf16 v[152:155], v[84:87], v[164:167], v[152:155]
	v_mfma_f32_16x16x32_bf16 v[148:151], v[92:95], v[164:167], v[148:151]
	v_mfma_f32_16x16x32_bf16 v[136:139], v[84:87], v[190:193], v[136:139]
	v_mfma_f32_16x16x32_bf16 v[132:135], v[92:95], v[190:193], v[132:135]
	v_mfma_f32_16x16x32_bf16 v[120:123], v[84:87], v[198:201], v[120:123]
	v_mfma_f32_16x16x32_bf16 v[116:119], v[92:95], v[198:201], v[116:119]
	v_mfma_f32_16x16x32_bf16 v[104:107], v[84:87], v[212:215], v[104:107]
	v_mfma_f32_16x16x32_bf16 v[100:103], v[92:95], v[212:215], v[100:103]
	v_mfma_f32_16x16x32_bf16 v[152:155], v[88:91], v[168:171], v[152:155]
	v_mfma_f32_16x16x32_bf16 v[148:151], v[96:99], v[168:171], v[148:151]
	v_mfma_f32_16x16x32_bf16 v[136:139], v[88:91], v[194:197], v[136:139]
	v_mfma_f32_16x16x32_bf16 v[132:135], v[96:99], v[194:197], v[132:135]
	v_mfma_f32_16x16x32_bf16 v[120:123], v[88:91], v[208:211], v[120:123]
	v_mfma_f32_16x16x32_bf16 v[116:119], v[96:99], v[208:211], v[116:119]
	v_mfma_f32_16x16x32_bf16 v[104:107], v[88:91], v[220:223], v[104:107]
	v_mfma_f32_16x16x32_bf16 v[100:103], v[96:99], v[220:223], v[100:103]
	s_barrier
	s_add_i32 s10, s42, s84
	v_lshl_add_u64 v[202:203], s[36:37], 0, v[174:175]
	s_mov_b32 m0, s10
	ds_read_b128 v[164:167], v219 offset:16384
	ds_read_b128 v[168:171], v219 offset:17408
	ds_read_b128 v[190:193], v219 offset:18432
	ds_read_b128 v[194:197], v219 offset:19456
	ds_read_b128 v[198:201], v219 offset:20480
	ds_read_b128 v[208:211], v219 offset:21504
	ds_read_b128 v[212:215], v219 offset:22528
	ds_read_b128 v[220:223], v219 offset:23552
	global_load_lds_dwordx4 v[202:203], off
	s_add_i32 m0, s10, 0x2000
	s_add_u32 s10, s36, 0x40000
	v_lshl_add_u64 v[224:225], s[36:37], 0, v[178:179]
	s_addc_u32 s11, s37, 0
	s_add_i32 s12, s12, s84
	global_load_lds_dwordx4 v[224:225], off
	v_lshl_add_u64 v[226:227], s[10:11], 0, v[174:175]
	s_mov_b32 m0, s12
	v_lshl_add_u64 v[228:229], s[40:41], 0, v[176:177]
	global_load_lds_dwordx4 v[226:227], off
	v_lshl_add_u64 v[226:227], s[10:11], 0, v[178:179]
	s_add_i32 m0, s12, 0x2000
	s_nop 0
	global_load_lds_dwordx4 v[226:227], off
	v_lshl_add_u64 v[226:227], s[40:41], 0, v[172:173]
	s_mov_b32 m0, s85
	s_nop 0
	global_load_lds_dwordx4 v[226:227], off
	s_mov_b32 m0, s86
	s_nop 0
	global_load_lds_dwordx4 v[228:229], off
	s_waitcnt vmcnt(8)
	s_waitcnt lgkmcnt(0)
	s_barrier
	v_mfma_f32_16x16x32_bf16 v[80:83], v[58:61], v[164:167], v[80:83]
	v_mfma_f32_16x16x32_bf16 v[76:79], v[68:71], v[164:167], v[76:79]
	v_mfma_f32_16x16x32_bf16 v[46:49], v[58:61], v[190:193], v[46:49]
	v_mfma_f32_16x16x32_bf16 v[42:45], v[68:71], v[190:193], v[42:45]
	v_mfma_f32_16x16x32_bf16 v[30:33], v[58:61], v[198:201], v[30:33]
	v_mfma_f32_16x16x32_bf16 v[26:29], v[68:71], v[198:201], v[26:29]
	v_mfma_f32_16x16x32_bf16 v[14:17], v[58:61], v[212:215], v[14:17]
	v_mfma_f32_16x16x32_bf16 v[10:13], v[68:71], v[212:215], v[10:13]
	v_mfma_f32_16x16x32_bf16 v[80:83], v[62:65], v[168:171], v[80:83]
	v_mfma_f32_16x16x32_bf16 v[76:79], v[72:75], v[168:171], v[76:79]
	v_mfma_f32_16x16x32_bf16 v[46:49], v[62:65], v[194:197], v[46:49]
	v_mfma_f32_16x16x32_bf16 v[42:45], v[72:75], v[194:197], v[42:45]
	v_mfma_f32_16x16x32_bf16 v[30:33], v[62:65], v[208:211], v[30:33]
	v_mfma_f32_16x16x32_bf16 v[26:29], v[72:75], v[208:211], v[26:29]
	v_mfma_f32_16x16x32_bf16 v[14:17], v[62:65], v[220:223], v[14:17]
	v_mfma_f32_16x16x32_bf16 v[10:13], v[72:75], v[220:223], v[10:13]
	v_mfma_f32_16x16x32_bf16 v[54:57], v[84:87], v[164:167], v[54:57]
	v_mfma_f32_16x16x32_bf16 v[50:53], v[92:95], v[164:167], v[50:53]
	v_mfma_f32_16x16x32_bf16 v[38:41], v[84:87], v[190:193], v[38:41]
	v_mfma_f32_16x16x32_bf16 v[34:37], v[92:95], v[190:193], v[34:37]
	v_mfma_f32_16x16x32_bf16 v[22:25], v[84:87], v[198:201], v[22:25]
	v_mfma_f32_16x16x32_bf16 v[18:21], v[92:95], v[198:201], v[18:21]
	v_mfma_f32_16x16x32_bf16 v[6:9], v[84:87], v[212:215], v[6:9]
	v_mfma_f32_16x16x32_bf16 v[2:5], v[92:95], v[212:215], v[2:5]
	v_mfma_f32_16x16x32_bf16 v[54:57], v[88:91], v[168:171], v[54:57]
	v_mfma_f32_16x16x32_bf16 v[50:53], v[96:99], v[168:171], v[50:53]
	v_mfma_f32_16x16x32_bf16 v[38:41], v[88:91], v[194:197], v[38:41]
	v_mfma_f32_16x16x32_bf16 v[34:37], v[96:99], v[194:197], v[34:37]
	v_mfma_f32_16x16x32_bf16 v[22:25], v[88:91], v[208:211], v[22:25]
	v_mfma_f32_16x16x32_bf16 v[18:21], v[96:99], v[208:211], v[18:21]
	v_mfma_f32_16x16x32_bf16 v[6:9], v[88:91], v[220:223], v[6:9]
	v_mfma_f32_16x16x32_bf16 v[2:5], v[96:99], v[220:223], v[2:5]
	s_barrier
	s_add_i32 s43, 0, 0x18000
	s_add_i32 s12, 0, 0x1c000
	v_add_u32_e32 v72, s43, v218
	v_add_u32_e32 v96, s12, v218
	ds_read_b128 v[58:61], v72
	ds_read_b128 v[62:65], v72 offset:1024
	ds_read_b128 v[68:71], v72 offset:2048
	ds_read_b128 v[72:75], v72 offset:3072
	ds_read_b128 v[84:87], v96
	ds_read_b128 v[88:91], v96 offset:1024
	ds_read_b128 v[92:95], v96 offset:2048
	ds_read_b128 v[96:99], v96 offset:3072
	s_add_u32 s10, s40, 0x40000
	s_addc_u32 s11, s41, 0
	s_mov_b32 m0, s87
	v_lshl_add_u64 v[230:231], s[10:11], 0, v[172:173]
	ds_read_b128 v[164:167], v219 offset:32768
	ds_read_b128 v[168:171], v219 offset:33792
	ds_read_b128 v[190:193], v219 offset:34816
	ds_read_b128 v[194:197], v219 offset:35840
	ds_read_b128 v[198:201], v219 offset:36864
	ds_read_b128 v[208:211], v219 offset:37888
	ds_read_b128 v[212:215], v219 offset:38912
	ds_read_b128 v[220:223], v219 offset:39936
	global_load_lds_dwordx4 v[230:231], off
	v_lshl_add_u64 v[230:231], s[10:11], 0, v[176:177]
	s_mov_b32 m0, s88
	s_nop 0
	global_load_lds_dwordx4 v[230:231], off
	s_waitcnt vmcnt(8)
	s_waitcnt lgkmcnt(0)
	s_barrier
	v_mfma_f32_16x16x32_bf16 v[160:163], v[58:61], v[164:167], v[160:163]
	v_mfma_f32_16x16x32_bf16 v[156:159], v[68:71], v[164:167], v[156:159]
	v_mfma_f32_16x16x32_bf16 v[144:147], v[58:61], v[190:193], v[144:147]
	v_mfma_f32_16x16x32_bf16 v[140:143], v[68:71], v[190:193], v[140:143]
	v_mfma_f32_16x16x32_bf16 v[128:131], v[58:61], v[198:201], v[128:131]
	v_mfma_f32_16x16x32_bf16 v[124:127], v[68:71], v[198:201], v[124:127]
	v_mfma_f32_16x16x32_bf16 v[112:115], v[58:61], v[212:215], v[112:115]
	v_mfma_f32_16x16x32_bf16 v[108:111], v[68:71], v[212:215], v[108:111]
	v_mfma_f32_16x16x32_bf16 v[160:163], v[62:65], v[168:171], v[160:163]
	v_mfma_f32_16x16x32_bf16 v[156:159], v[72:75], v[168:171], v[156:159]
	v_mfma_f32_16x16x32_bf16 v[144:147], v[62:65], v[194:197], v[144:147]
	v_mfma_f32_16x16x32_bf16 v[140:143], v[72:75], v[194:197], v[140:143]
	v_mfma_f32_16x16x32_bf16 v[128:131], v[62:65], v[208:211], v[128:131]
	v_mfma_f32_16x16x32_bf16 v[124:127], v[72:75], v[208:211], v[124:127]
	v_mfma_f32_16x16x32_bf16 v[112:115], v[62:65], v[220:223], v[112:115]
	v_mfma_f32_16x16x32_bf16 v[108:111], v[72:75], v[220:223], v[108:111]
	v_mfma_f32_16x16x32_bf16 v[152:155], v[84:87], v[164:167], v[152:155]
	v_mfma_f32_16x16x32_bf16 v[148:151], v[92:95], v[164:167], v[148:151]
	v_mfma_f32_16x16x32_bf16 v[136:139], v[84:87], v[190:193], v[136:139]
	v_mfma_f32_16x16x32_bf16 v[132:135], v[92:95], v[190:193], v[132:135]
	v_mfma_f32_16x16x32_bf16 v[120:123], v[84:87], v[198:201], v[120:123]
	v_mfma_f32_16x16x32_bf16 v[116:119], v[92:95], v[198:201], v[116:119]
	v_mfma_f32_16x16x32_bf16 v[104:107], v[84:87], v[212:215], v[104:107]
	v_mfma_f32_16x16x32_bf16 v[100:103], v[92:95], v[212:215], v[100:103]
	v_mfma_f32_16x16x32_bf16 v[152:155], v[88:91], v[168:171], v[152:155]
	v_mfma_f32_16x16x32_bf16 v[148:151], v[96:99], v[168:171], v[148:151]
	v_mfma_f32_16x16x32_bf16 v[136:139], v[88:91], v[194:197], v[136:139]
	v_mfma_f32_16x16x32_bf16 v[132:135], v[96:99], v[194:197], v[132:135]
	v_mfma_f32_16x16x32_bf16 v[120:123], v[88:91], v[208:211], v[120:123]
	v_mfma_f32_16x16x32_bf16 v[116:119], v[96:99], v[208:211], v[116:119]
	v_mfma_f32_16x16x32_bf16 v[104:107], v[88:91], v[220:223], v[104:107]
	v_mfma_f32_16x16x32_bf16 v[100:103], v[96:99], v[220:223], v[100:103]
	s_barrier
	s_add_i32 s10, s43, s84
	v_lshl_add_u64 v[202:203], v[202:203], 0, s[60:61]
	s_mov_b32 m0, s10
	ds_read_b128 v[164:167], v219 offset:49152
	ds_read_b128 v[168:171], v219 offset:50176
	ds_read_b128 v[190:193], v219 offset:51200
	ds_read_b128 v[194:197], v219 offset:52224
	ds_read_b128 v[198:201], v219 offset:53248
	ds_read_b128 v[208:211], v219 offset:54272
	ds_read_b128 v[212:215], v219 offset:55296
	ds_read_b128 v[220:223], v219 offset:56320
	global_load_lds_dwordx4 v[202:203], off
	s_add_i32 m0, s10, 0x2000
	s_add_u32 s10, s36, 0x40080
	v_lshl_add_u64 v[202:203], v[224:225], 0, s[60:61]
	s_addc_u32 s11, s37, 0
	s_add_i32 s12, s12, s84
	global_load_lds_dwordx4 v[202:203], off
	v_lshl_add_u64 v[202:203], s[10:11], 0, v[174:175]
	s_mov_b32 m0, s12
	s_nop 0
	global_load_lds_dwordx4 v[202:203], off
	v_lshl_add_u64 v[202:203], s[10:11], 0, v[178:179]
	s_add_i32 m0, s12, 0x2000
	s_nop 0
	global_load_lds_dwordx4 v[202:203], off
	v_lshl_add_u64 v[202:203], v[226:227], 0, s[60:61]
	s_mov_b32 m0, s72
	s_nop 0
	global_load_lds_dwordx4 v[202:203], off
	v_lshl_add_u64 v[202:203], v[228:229], 0, s[60:61]
	s_mov_b32 m0, s90
	s_nop 0
	global_load_lds_dwordx4 v[202:203], off
	s_waitcnt vmcnt(8)
	s_waitcnt lgkmcnt(0)
	s_barrier
	v_mfma_f32_16x16x32_bf16 v[80:83], v[58:61], v[164:167], v[80:83]
	v_mfma_f32_16x16x32_bf16 v[76:79], v[68:71], v[164:167], v[76:79]
	v_mfma_f32_16x16x32_bf16 v[46:49], v[58:61], v[190:193], v[46:49]
	v_mfma_f32_16x16x32_bf16 v[42:45], v[68:71], v[190:193], v[42:45]
	v_mfma_f32_16x16x32_bf16 v[30:33], v[58:61], v[198:201], v[30:33]
	v_mfma_f32_16x16x32_bf16 v[26:29], v[68:71], v[198:201], v[26:29]
	v_mfma_f32_16x16x32_bf16 v[14:17], v[58:61], v[212:215], v[14:17]
	v_mfma_f32_16x16x32_bf16 v[10:13], v[68:71], v[212:215], v[10:13]
	v_mfma_f32_16x16x32_bf16 v[80:83], v[62:65], v[168:171], v[80:83]
	v_mfma_f32_16x16x32_bf16 v[76:79], v[72:75], v[168:171], v[76:79]
	v_mfma_f32_16x16x32_bf16 v[46:49], v[62:65], v[194:197], v[46:49]
	v_mfma_f32_16x16x32_bf16 v[42:45], v[72:75], v[194:197], v[42:45]
	v_mfma_f32_16x16x32_bf16 v[30:33], v[62:65], v[208:211], v[30:33]
	v_mfma_f32_16x16x32_bf16 v[26:29], v[72:75], v[208:211], v[26:29]
	v_mfma_f32_16x16x32_bf16 v[14:17], v[62:65], v[220:223], v[14:17]
	v_mfma_f32_16x16x32_bf16 v[10:13], v[72:75], v[220:223], v[10:13]
	v_mfma_f32_16x16x32_bf16 v[54:57], v[84:87], v[164:167], v[54:57]
	v_mfma_f32_16x16x32_bf16 v[50:53], v[92:95], v[164:167], v[50:53]
	v_mfma_f32_16x16x32_bf16 v[38:41], v[84:87], v[190:193], v[38:41]
	v_mfma_f32_16x16x32_bf16 v[34:37], v[92:95], v[190:193], v[34:37]
	v_mfma_f32_16x16x32_bf16 v[22:25], v[84:87], v[198:201], v[22:25]
	v_mfma_f32_16x16x32_bf16 v[18:21], v[92:95], v[198:201], v[18:21]
	v_mfma_f32_16x16x32_bf16 v[6:9], v[84:87], v[212:215], v[6:9]
	v_mfma_f32_16x16x32_bf16 v[2:5], v[92:95], v[212:215], v[2:5]
	v_mfma_f32_16x16x32_bf16 v[54:57], v[88:91], v[168:171], v[54:57]
	v_mfma_f32_16x16x32_bf16 v[50:53], v[96:99], v[168:171], v[50:53]
	v_mfma_f32_16x16x32_bf16 v[38:41], v[88:91], v[194:197], v[38:41]
	v_mfma_f32_16x16x32_bf16 v[34:37], v[96:99], v[194:197], v[34:37]
	v_mfma_f32_16x16x32_bf16 v[22:25], v[88:91], v[208:211], v[22:25]
	v_mfma_f32_16x16x32_bf16 v[18:21], v[96:99], v[208:211], v[18:21]
	v_mfma_f32_16x16x32_bf16 v[6:9], v[88:91], v[220:223], v[6:9]
	v_mfma_f32_16x16x32_bf16 v[2:5], v[96:99], v[220:223], v[2:5]
	s_barrier
	s_add_i32 s26, s26, 2
	s_add_u32 s34, s34, 0x100
	s_addc_u32 s35, s35, 0
	s_add_u32 s8, s8, 0x100
	s_addc_u32 s9, s9, 0
	s_cmp_gt_u32 s26, 13
	s_cbranch_scc0 .LBB0_998
	s_and_b64 vcc, exec, s[52:53]
	s_cbranch_vccz .LBB0_1001
	s_barrier

.LBB0_1238:
	s_waitcnt lgkmcnt(0)
	v_mov_b32_e32 v229, v67
	v_lshl_add_u64 v[244:245], s[36:37], 0, v[66:67]
	v_lshl_add_u64 v[228:229], s[36:37], 0, v[228:229]
	s_barrier
	v_mfma_f32_16x16x32_bf16 v[62:65], v[148:151], v[188:191], v[62:65]
	v_mfma_f32_16x16x32_bf16 v[54:57], v[156:159], v[188:191], v[54:57]
	v_mfma_f32_16x16x32_bf16 v[38:41], v[148:151], v[180:183], v[38:41]
	v_mfma_f32_16x16x32_bf16 v[34:37], v[156:159], v[180:183], v[34:37]
	v_mfma_f32_16x16x32_bf16 v[22:25], v[148:151], v[172:175], v[22:25]
	v_mfma_f32_16x16x32_bf16 v[18:21], v[156:159], v[172:175], v[18:21]
	v_mfma_f32_16x16x32_bf16 v[6:9], v[148:151], v[164:167], v[6:9]
	v_mfma_f32_16x16x32_bf16 v[2:5], v[156:159], v[164:167], v[2:5]
	v_mfma_f32_16x16x32_bf16 v[62:65], v[152:155], v[192:195], v[62:65]
	v_mfma_f32_16x16x32_bf16 v[54:57], v[160:163], v[192:195], v[54:57]
	v_mfma_f32_16x16x32_bf16 v[38:41], v[152:155], v[184:187], v[38:41]
	v_mfma_f32_16x16x32_bf16 v[34:37], v[160:163], v[184:187], v[34:37]
	v_mfma_f32_16x16x32_bf16 v[22:25], v[152:155], v[176:179], v[22:25]
	v_mfma_f32_16x16x32_bf16 v[18:21], v[160:163], v[176:179], v[18:21]
	v_mfma_f32_16x16x32_bf16 v[6:9], v[152:155], v[168:171], v[6:9]
	v_mfma_f32_16x16x32_bf16 v[2:5], v[160:163], v[168:171], v[2:5]
	v_mfma_f32_16x16x32_bf16 v[58:61], v[132:135], v[188:191], v[58:61]
	v_mfma_f32_16x16x32_bf16 v[50:53], v[140:143], v[188:191], v[50:53]
	v_mfma_f32_16x16x32_bf16 v[46:49], v[132:135], v[180:183], v[46:49]
	v_mfma_f32_16x16x32_bf16 v[42:45], v[140:143], v[180:183], v[42:45]
	v_mfma_f32_16x16x32_bf16 v[30:33], v[132:135], v[172:175], v[30:33]
	v_mfma_f32_16x16x32_bf16 v[26:29], v[140:143], v[172:175], v[26:29]
	v_mfma_f32_16x16x32_bf16 v[14:17], v[132:135], v[164:167], v[14:17]
	v_mfma_f32_16x16x32_bf16 v[10:13], v[140:143], v[164:167], v[10:13]
	v_mfma_f32_16x16x32_bf16 v[58:61], v[136:139], v[192:195], v[58:61]
	v_mfma_f32_16x16x32_bf16 v[50:53], v[144:147], v[192:195], v[50:53]
	v_mfma_f32_16x16x32_bf16 v[46:49], v[136:139], v[184:187], v[46:49]
	v_mfma_f32_16x16x32_bf16 v[42:45], v[144:147], v[184:187], v[42:45]
	v_mfma_f32_16x16x32_bf16 v[30:33], v[136:139], v[176:179], v[30:33]
	v_mfma_f32_16x16x32_bf16 v[26:29], v[144:147], v[176:179], v[26:29]
	v_mfma_f32_16x16x32_bf16 v[14:17], v[136:139], v[168:171], v[14:17]
	v_mfma_f32_16x16x32_bf16 v[10:13], v[144:147], v[168:171], v[10:13]
	s_barrier
	s_add_i32 s8, 0, 0x18000
	v_add_u32_e32 v66, s8, v236
	s_add_i32 s9, 0, 0x1c000
	ds_read_b128 v[132:135], v66
	ds_read_b128 v[136:139], v66 offset:1024
	ds_read_b128 v[140:143], v66 offset:2048
	ds_read_b128 v[144:147], v66 offset:3072
	v_add_u32_e32 v66, s9, v236
	ds_read_b128 v[148:151], v66
	ds_read_b128 v[152:155], v66 offset:1024
	ds_read_b128 v[156:159], v66 offset:2048
	ds_read_b128 v[160:163], v66 offset:3072
	s_mov_b32 m0, s96
	v_cndmask_b32_e64 v66, v208, v239, s[42:43]
	ds_read_b128 v[164:167], v211 offset:32768
	ds_read_b128 v[168:171], v211 offset:33792
	ds_read_b128 v[172:175], v211 offset:34816
	ds_read_b128 v[176:179], v211 offset:35840
	ds_read_b128 v[180:183], v211 offset:36864
	ds_read_b128 v[184:187], v211 offset:37888
	ds_read_b128 v[188:191], v211 offset:38912
	ds_read_b128 v[192:195], v211 offset:39936
	v_cndmask_b32_e64 v209, v212, v241, s[42:43]
	global_load_lds_dwordx4 v66, s[36:37]
	s_mov_b32 m0, s97
	s_nop 0
	global_load_lds_dwordx4 v209, s[36:37]
	s_waitcnt vmcnt(8)
	s_waitcnt lgkmcnt(0)
	s_barrier
	v_mfma_f32_16x16x32_bf16 v[128:131], v[132:135], v[164:167], v[128:131]
	v_mfma_f32_16x16x32_bf16 v[120:123], v[140:143], v[164:167], v[120:123]
	v_mfma_f32_16x16x32_bf16 v[112:115], v[132:135], v[172:175], v[112:115]
	v_mfma_f32_16x16x32_bf16 v[104:107], v[140:143], v[172:175], v[104:107]
	v_mfma_f32_16x16x32_bf16 v[96:99], v[132:135], v[180:183], v[96:99]
	v_mfma_f32_16x16x32_bf16 v[88:91], v[140:143], v[180:183], v[88:91]
	v_mfma_f32_16x16x32_bf16 v[80:83], v[132:135], v[188:191], v[80:83]
	v_mfma_f32_16x16x32_bf16 v[72:75], v[140:143], v[188:191], v[72:75]
	v_mfma_f32_16x16x32_bf16 v[128:131], v[136:139], v[168:171], v[128:131]
	v_mfma_f32_16x16x32_bf16 v[120:123], v[144:147], v[168:171], v[120:123]
	v_mfma_f32_16x16x32_bf16 v[112:115], v[136:139], v[176:179], v[112:115]
	v_mfma_f32_16x16x32_bf16 v[104:107], v[144:147], v[176:179], v[104:107]
	v_mfma_f32_16x16x32_bf16 v[96:99], v[136:139], v[184:187], v[96:99]
	v_mfma_f32_16x16x32_bf16 v[88:91], v[144:147], v[184:187], v[88:91]
	v_mfma_f32_16x16x32_bf16 v[80:83], v[136:139], v[192:195], v[80:83]
	v_mfma_f32_16x16x32_bf16 v[72:75], v[144:147], v[192:195], v[72:75]
	v_mfma_f32_16x16x32_bf16 v[124:127], v[148:151], v[164:167], v[124:127]
	v_mfma_f32_16x16x32_bf16 v[116:119], v[156:159], v[164:167], v[116:119]
	v_mfma_f32_16x16x32_bf16 v[108:111], v[148:151], v[172:175], v[108:111]
	v_mfma_f32_16x16x32_bf16 v[100:103], v[156:159], v[172:175], v[100:103]
	v_mfma_f32_16x16x32_bf16 v[92:95], v[148:151], v[180:183], v[92:95]
	v_mfma_f32_16x16x32_bf16 v[84:87], v[156:159], v[180:183], v[84:87]
	v_mfma_f32_16x16x32_bf16 v[76:79], v[148:151], v[188:191], v[76:79]
	v_mfma_f32_16x16x32_bf16 v[68:71], v[156:159], v[188:191], v[68:71]
	v_mfma_f32_16x16x32_bf16 v[124:127], v[152:155], v[168:171], v[124:127]
	v_mfma_f32_16x16x32_bf16 v[116:119], v[160:163], v[168:171], v[116:119]
	v_mfma_f32_16x16x32_bf16 v[108:111], v[152:155], v[176:179], v[108:111]
	v_mfma_f32_16x16x32_bf16 v[100:103], v[160:163], v[176:179], v[100:103]
	v_mfma_f32_16x16x32_bf16 v[92:95], v[152:155], v[184:187], v[92:95]
	v_mfma_f32_16x16x32_bf16 v[84:87], v[160:163], v[184:187], v[84:87]
	v_mfma_f32_16x16x32_bf16 v[76:79], v[152:155], v[192:195], v[76:79]
	v_mfma_f32_16x16x32_bf16 v[68:71], v[160:163], v[192:195], v[68:71]
	s_barrier
	s_add_i32 s8, s8, s89
	v_lshl_add_u64 v[226:227], v[226:227], 0, s[60:61]
	s_mov_b32 m0, s8
	ds_read_b128 v[164:167], v211 offset:49152
	ds_read_b128 v[168:171], v211 offset:50176
	ds_read_b128 v[172:175], v211 offset:51200
	ds_read_b128 v[176:179], v211 offset:52224
	ds_read_b128 v[180:183], v211 offset:53248
	ds_read_b128 v[184:187], v211 offset:54272
	ds_read_b128 v[188:191], v211 offset:55296
	ds_read_b128 v[192:195], v211 offset:56320
	global_load_lds_dwordx4 v[226:227], off
	v_lshl_add_u64 v[224:225], v[224:225], 0, s[60:61]
	s_add_i32 m0, s8, 0x2000
	v_lshl_add_u64 v[222:223], v[222:223], 0, s[30:31]
	s_add_i32 s8, s9, s89
	global_load_lds_dwordx4 v[224:225], off
	v_lshl_add_u64 v[224:225], v[222:223], 0, v[196:197]
	s_mov_b32 m0, s8
	v_lshl_add_u64 v[222:223], v[222:223], 0, v[198:199]
	global_load_lds_dwordx4 v[224:225], off
	s_add_i32 m0, s8, 0x2000
	s_nop 0
	global_load_lds_dwordx4 v[222:223], off
	v_lshl_add_u64 v[222:223], v[244:245], 0, s[60:61]
	s_mov_b32 m0, s56
	s_nop 0
	global_load_lds_dwordx4 v[222:223], off
	v_lshl_add_u64 v[222:223], v[228:229], 0, s[60:61]
	s_mov_b32 m0, s57
	s_nop 0
	global_load_lds_dwordx4 v[222:223], off
	s_waitcnt vmcnt(8)
	s_waitcnt lgkmcnt(0)
	s_barrier
	v_mfma_f32_16x16x32_bf16 v[62:65], v[132:135], v[164:167], v[62:65]
	v_mfma_f32_16x16x32_bf16 v[54:57], v[140:143], v[164:167], v[54:57]
	v_mfma_f32_16x16x32_bf16 v[38:41], v[132:135], v[172:175], v[38:41]
	v_mfma_f32_16x16x32_bf16 v[34:37], v[140:143], v[172:175], v[34:37]
	v_mfma_f32_16x16x32_bf16 v[22:25], v[132:135], v[180:183], v[22:25]
	v_mfma_f32_16x16x32_bf16 v[18:21], v[140:143], v[180:183], v[18:21]
	v_mfma_f32_16x16x32_bf16 v[6:9], v[132:135], v[188:191], v[6:9]
	v_mfma_f32_16x16x32_bf16 v[2:5], v[140:143], v[188:191], v[2:5]
	v_mfma_f32_16x16x32_bf16 v[62:65], v[136:139], v[168:171], v[62:65]
	v_mfma_f32_16x16x32_bf16 v[54:57], v[144:147], v[168:171], v[54:57]
	v_mfma_f32_16x16x32_bf16 v[38:41], v[136:139], v[176:179], v[38:41]
	v_mfma_f32_16x16x32_bf16 v[34:37], v[144:147], v[176:179], v[34:37]
	v_mfma_f32_16x16x32_bf16 v[22:25], v[136:139], v[184:187], v[22:25]
	v_mfma_f32_16x16x32_bf16 v[18:21], v[144:147], v[184:187], v[18:21]
	v_mfma_f32_16x16x32_bf16 v[6:9], v[136:139], v[192:195], v[6:9]
	v_mfma_f32_16x16x32_bf16 v[2:5], v[144:147], v[192:195], v[2:5]
	v_mfma_f32_16x16x32_bf16 v[58:61], v[148:151], v[164:167], v[58:61]
	v_mfma_f32_16x16x32_bf16 v[50:53], v[156:159], v[164:167], v[50:53]
	v_mfma_f32_16x16x32_bf16 v[46:49], v[148:151], v[172:175], v[46:49]
	v_mfma_f32_16x16x32_bf16 v[42:45], v[156:159], v[172:175], v[42:45]
	v_mfma_f32_16x16x32_bf16 v[30:33], v[148:151], v[180:183], v[30:33]
	v_mfma_f32_16x16x32_bf16 v[26:29], v[156:159], v[180:183], v[26:29]
	v_mfma_f32_16x16x32_bf16 v[14:17], v[148:151], v[188:191], v[14:17]
	v_mfma_f32_16x16x32_bf16 v[10:13], v[156:159], v[188:191], v[10:13]
	v_mfma_f32_16x16x32_bf16 v[58:61], v[152:155], v[168:171], v[58:61]
	v_mfma_f32_16x16x32_bf16 v[50:53], v[160:163], v[168:171], v[50:53]
	v_mfma_f32_16x16x32_bf16 v[46:49], v[152:155], v[176:179], v[46:49]
	v_mfma_f32_16x16x32_bf16 v[42:45], v[160:163], v[176:179], v[42:45]
	v_mfma_f32_16x16x32_bf16 v[30:33], v[152:155], v[184:187], v[30:33]
	v_mfma_f32_16x16x32_bf16 v[26:29], v[160:163], v[184:187], v[26:29]
	v_mfma_f32_16x16x32_bf16 v[14:17], v[152:155], v[192:195], v[14:17]
	v_mfma_f32_16x16x32_bf16 v[10:13], v[160:163], v[192:195], v[10:13]
	s_barrier
	s_add_i32 s45, s45, 2
	s_cmp_gt_u32 s45, 13
	s_mov_b64 s[36:37], s[84:85]
	s_cbranch_scc1 .LBB0_1247

.LBB0_1243:
	s_add_u32 s84, s36, 0x100
	s_addc_u32 s85, s37, 0
	s_cmpk_eq_i32 s36, 0x700
	s_cselect_b64 s[42:43], -1, 0
	s_and_b64 s[8:9], s[42:43], exec
	s_cselect_b32 s9, 0, s84
	s_waitcnt lgkmcnt(0)
	v_lshl_add_u64 v[222:223], v[220:221], 0, s[36:37]
	s_cselect_b32 s8, 0, s85
	s_add_u32 s36, s66, s9
	v_cndmask_b32_e64 v223, v223, v203, s[42:43]
	s_addc_u32 s37, s67, s8
	v_cndmask_b32_e64 v222, v222, v202, s[42:43]
	s_barrier
	v_mfma_f32_16x16x32_bf16 v[128:131], v[148:151], v[188:191], v[128:131]
	v_mfma_f32_16x16x32_bf16 v[120:123], v[156:159], v[188:191], v[120:123]
	v_mfma_f32_16x16x32_bf16 v[112:115], v[148:151], v[180:183], v[112:115]
	v_mfma_f32_16x16x32_bf16 v[104:107], v[156:159], v[180:183], v[104:107]
	v_mfma_f32_16x16x32_bf16 v[96:99], v[148:151], v[172:175], v[96:99]
	v_mfma_f32_16x16x32_bf16 v[88:91], v[156:159], v[172:175], v[88:91]
	v_mfma_f32_16x16x32_bf16 v[80:83], v[148:151], v[164:167], v[80:83]
	v_mfma_f32_16x16x32_bf16 v[72:75], v[156:159], v[164:167], v[72:75]
	v_mfma_f32_16x16x32_bf16 v[128:131], v[152:155], v[192:195], v[128:131]
	v_mfma_f32_16x16x32_bf16 v[120:123], v[160:163], v[192:195], v[120:123]
	v_mfma_f32_16x16x32_bf16 v[112:115], v[152:155], v[184:187], v[112:115]
	v_mfma_f32_16x16x32_bf16 v[104:107], v[160:163], v[184:187], v[104:107]
	v_mfma_f32_16x16x32_bf16 v[96:99], v[152:155], v[176:179], v[96:99]
	v_mfma_f32_16x16x32_bf16 v[88:91], v[160:163], v[176:179], v[88:91]
	v_mfma_f32_16x16x32_bf16 v[80:83], v[152:155], v[168:171], v[80:83]
	v_mfma_f32_16x16x32_bf16 v[72:75], v[160:163], v[168:171], v[72:75]
	v_mfma_f32_16x16x32_bf16 v[124:127], v[132:135], v[188:191], v[124:127]
	v_mfma_f32_16x16x32_bf16 v[116:119], v[140:143], v[188:191], v[116:119]
	v_mfma_f32_16x16x32_bf16 v[108:111], v[132:135], v[180:183], v[108:111]
	v_mfma_f32_16x16x32_bf16 v[100:103], v[140:143], v[180:183], v[100:103]
	v_mfma_f32_16x16x32_bf16 v[92:95], v[132:135], v[172:175], v[92:95]
	v_mfma_f32_16x16x32_bf16 v[84:87], v[140:143], v[172:175], v[84:87]
	v_mfma_f32_16x16x32_bf16 v[76:79], v[132:135], v[164:167], v[76:79]
	v_mfma_f32_16x16x32_bf16 v[68:71], v[140:143], v[164:167], v[68:71]
	v_mfma_f32_16x16x32_bf16 v[124:127], v[136:139], v[192:195], v[124:127]
	v_mfma_f32_16x16x32_bf16 v[116:119], v[144:147], v[192:195], v[116:119]
	v_mfma_f32_16x16x32_bf16 v[108:111], v[136:139], v[184:187], v[108:111]
	v_mfma_f32_16x16x32_bf16 v[100:103], v[144:147], v[184:187], v[100:103]
	v_mfma_f32_16x16x32_bf16 v[92:95], v[136:139], v[176:179], v[92:95]
	v_mfma_f32_16x16x32_bf16 v[84:87], v[144:147], v[176:179], v[84:87]
	v_mfma_f32_16x16x32_bf16 v[76:79], v[136:139], v[168:171], v[76:79]
	v_mfma_f32_16x16x32_bf16 v[68:71], v[144:147], v[168:171], v[68:71]
	s_barrier
	s_mov_b32 m0, s91
	v_lshl_add_u64 v[226:227], v[222:223], 0, v[196:197]
	ds_read_b128 v[188:191], v211 offset:16384
	ds_read_b128 v[192:195], v211 offset:17408
	ds_read_b128 v[180:183], v211 offset:18432
	ds_read_b128 v[184:187], v211 offset:19456
	ds_read_b128 v[172:175], v211 offset:20480
	ds_read_b128 v[176:179], v211 offset:21504
	ds_read_b128 v[164:167], v211 offset:22528
	ds_read_b128 v[168:171], v211 offset:23552
	global_load_lds_dwordx4 v[226:227], off
	v_lshl_add_u64 v[224:225], v[222:223], 0, v[198:199]
	s_mov_b32 m0, s92
	v_lshl_add_u64 v[228:229], v[222:223], 0, s[78:79]
	global_load_lds_dwordx4 v[224:225], off
	v_lshl_add_u64 v[244:245], v[228:229], 0, v[196:197]
	s_mov_b32 m0, s93
	v_lshl_add_u64 v[228:229], v[228:229], 0, v[198:199]
	global_load_lds_dwordx4 v[244:245], off
	s_mov_b32 m0, s94
	v_cndmask_b32_e64 v66, v210, v238, s[42:43]
	global_load_lds_dwordx4 v[228:229], off
	s_mov_b32 m0, s90
	v_cndmask_b32_e64 v228, v214, v240, s[42:43]
	global_load_lds_dwordx4 v66, s[36:37]
	s_mov_b32 m0, s95
	s_mov_b64 s[26:27], -1
	global_load_lds_dwordx4 v228, s[36:37]
	s_and_b64 vcc, exec, s[86:87]
	s_cbranch_vccz .LBB0_1245
	s_waitcnt vmcnt(8)
	s_mov_b64 s[26:27], 0

.LBB0_1479:
	s_waitcnt lgkmcnt(0)
	s_barrier
	v_mfma_f32_16x16x32_bf16 v[62:65], v[148:151], v[188:191], v[62:65]
	v_mfma_f32_16x16x32_bf16 v[58:61], v[156:159], v[188:191], v[58:61]
	v_mfma_f32_16x16x32_bf16 v[50:53], v[148:151], v[180:183], v[50:53]
	v_mfma_f32_16x16x32_bf16 v[42:45], v[156:159], v[180:183], v[42:45]
	v_mfma_f32_16x16x32_bf16 v[34:37], v[148:151], v[172:175], v[34:37]
	v_mfma_f32_16x16x32_bf16 v[26:29], v[156:159], v[172:175], v[26:29]
	v_mfma_f32_16x16x32_bf16 v[18:21], v[148:151], v[164:167], v[18:21]
	v_mfma_f32_16x16x32_bf16 v[10:13], v[156:159], v[164:167], v[10:13]
	v_mfma_f32_16x16x32_bf16 v[62:65], v[152:155], v[192:195], v[62:65]
	v_mfma_f32_16x16x32_bf16 v[58:61], v[160:163], v[192:195], v[58:61]
	v_mfma_f32_16x16x32_bf16 v[50:53], v[152:155], v[184:187], v[50:53]
	v_mfma_f32_16x16x32_bf16 v[42:45], v[160:163], v[184:187], v[42:45]
	v_mfma_f32_16x16x32_bf16 v[34:37], v[152:155], v[176:179], v[34:37]
	v_mfma_f32_16x16x32_bf16 v[26:29], v[160:163], v[176:179], v[26:29]
	v_mfma_f32_16x16x32_bf16 v[18:21], v[152:155], v[168:171], v[18:21]
	v_mfma_f32_16x16x32_bf16 v[10:13], v[160:163], v[168:171], v[10:13]
	v_mfma_f32_16x16x32_bf16 v[54:57], v[132:135], v[188:191], v[54:57]
	v_mfma_f32_16x16x32_bf16 v[46:49], v[140:143], v[188:191], v[46:49]
	v_mfma_f32_16x16x32_bf16 v[38:41], v[132:135], v[180:183], v[38:41]
	v_mfma_f32_16x16x32_bf16 v[30:33], v[140:143], v[180:183], v[30:33]
	v_mfma_f32_16x16x32_bf16 v[22:25], v[132:135], v[172:175], v[22:25]
	v_mfma_f32_16x16x32_bf16 v[14:17], v[140:143], v[172:175], v[14:17]
	v_mfma_f32_16x16x32_bf16 v[6:9], v[132:135], v[164:167], v[6:9]
	v_mfma_f32_16x16x32_bf16 v[2:5], v[140:143], v[164:167], v[2:5]
	v_mfma_f32_16x16x32_bf16 v[54:57], v[136:139], v[192:195], v[54:57]
	v_mfma_f32_16x16x32_bf16 v[46:49], v[144:147], v[192:195], v[46:49]
	v_mfma_f32_16x16x32_bf16 v[38:41], v[136:139], v[184:187], v[38:41]
	v_mfma_f32_16x16x32_bf16 v[30:33], v[144:147], v[184:187], v[30:33]
	v_mfma_f32_16x16x32_bf16 v[22:25], v[136:139], v[176:179], v[22:25]
	v_mfma_f32_16x16x32_bf16 v[14:17], v[144:147], v[176:179], v[14:17]
	v_mfma_f32_16x16x32_bf16 v[6:9], v[136:139], v[168:171], v[6:9]
	v_mfma_f32_16x16x32_bf16 v[2:5], v[144:147], v[168:171], v[2:5]
	s_barrier
	s_add_i32 s9, 0, 0x18000
	s_add_i32 s12, 0, 0x1c000
	v_add_u32_e32 v144, s9, v231
	v_add_u32_e32 v160, s12, v231
	ds_read_b128 v[132:135], v144
	ds_read_b128 v[136:139], v144 offset:1024
	ds_read_b128 v[140:143], v144 offset:2048
	ds_read_b128 v[144:147], v144 offset:3072
	ds_read_b128 v[148:151], v160
	ds_read_b128 v[152:155], v160 offset:1024
	ds_read_b128 v[156:159], v160 offset:2048
	ds_read_b128 v[160:163], v160 offset:3072
	s_add_u32 s10, s36, 0x20000
	s_addc_u32 s11, s37, 0
	s_mov_b32 m0, s50
	v_lshl_add_u64 v[234:235], s[10:11], 0, v[196:197]
	ds_read_b128 v[164:167], v232 offset:32768
	ds_read_b128 v[168:171], v232 offset:33792
	ds_read_b128 v[172:175], v232 offset:34816
	ds_read_b128 v[176:179], v232 offset:35840
	ds_read_b128 v[180:183], v232 offset:36864
	ds_read_b128 v[184:187], v232 offset:37888
	ds_read_b128 v[188:191], v232 offset:38912
	ds_read_b128 v[192:195], v232 offset:39936
	global_load_lds_dwordx4 v[234:235], off
	v_lshl_add_u64 v[234:235], s[10:11], 0, v[200:201]
	s_mov_b32 m0, s51
	s_nop 0
	global_load_lds_dwordx4 v[234:235], off
	s_waitcnt vmcnt(8)
	s_waitcnt lgkmcnt(0)
	s_barrier
	v_mfma_f32_16x16x32_bf16 v[128:131], v[132:135], v[164:167], v[128:131]
	v_mfma_f32_16x16x32_bf16 v[124:127], v[140:143], v[164:167], v[124:127]
	v_mfma_f32_16x16x32_bf16 v[116:119], v[132:135], v[172:175], v[116:119]
	v_mfma_f32_16x16x32_bf16 v[108:111], v[140:143], v[172:175], v[108:111]
	v_mfma_f32_16x16x32_bf16 v[100:103], v[132:135], v[180:183], v[100:103]
	v_mfma_f32_16x16x32_bf16 v[92:95], v[140:143], v[180:183], v[92:95]
	v_mfma_f32_16x16x32_bf16 v[84:87], v[132:135], v[188:191], v[84:87]
	v_mfma_f32_16x16x32_bf16 v[76:79], v[140:143], v[188:191], v[76:79]
	v_mfma_f32_16x16x32_bf16 v[128:131], v[136:139], v[168:171], v[128:131]
	v_mfma_f32_16x16x32_bf16 v[124:127], v[144:147], v[168:171], v[124:127]
	v_mfma_f32_16x16x32_bf16 v[116:119], v[136:139], v[176:179], v[116:119]
	v_mfma_f32_16x16x32_bf16 v[108:111], v[144:147], v[176:179], v[108:111]
	v_mfma_f32_16x16x32_bf16 v[100:103], v[136:139], v[184:187], v[100:103]
	v_mfma_f32_16x16x32_bf16 v[92:95], v[144:147], v[184:187], v[92:95]
	v_mfma_f32_16x16x32_bf16 v[84:87], v[136:139], v[192:195], v[84:87]
	v_mfma_f32_16x16x32_bf16 v[76:79], v[144:147], v[192:195], v[76:79]
	v_mfma_f32_16x16x32_bf16 v[120:123], v[148:151], v[164:167], v[120:123]
	v_mfma_f32_16x16x32_bf16 v[112:115], v[156:159], v[164:167], v[112:115]
	v_mfma_f32_16x16x32_bf16 v[104:107], v[148:151], v[172:175], v[104:107]
	v_mfma_f32_16x16x32_bf16 v[96:99], v[156:159], v[172:175], v[96:99]
	v_mfma_f32_16x16x32_bf16 v[88:91], v[148:151], v[180:183], v[88:91]
	v_mfma_f32_16x16x32_bf16 v[80:83], v[156:159], v[180:183], v[80:83]
	v_mfma_f32_16x16x32_bf16 v[72:75], v[148:151], v[188:191], v[72:75]
	v_mfma_f32_16x16x32_bf16 v[68:71], v[156:159], v[188:191], v[68:71]
	v_mfma_f32_16x16x32_bf16 v[120:123], v[152:155], v[168:171], v[120:123]
	v_mfma_f32_16x16x32_bf16 v[112:115], v[160:163], v[168:171], v[112:115]
	v_mfma_f32_16x16x32_bf16 v[104:107], v[152:155], v[176:179], v[104:107]
	v_mfma_f32_16x16x32_bf16 v[96:99], v[160:163], v[176:179], v[96:99]
	v_mfma_f32_16x16x32_bf16 v[88:91], v[152:155], v[184:187], v[88:91]
	v_mfma_f32_16x16x32_bf16 v[80:83], v[160:163], v[184:187], v[80:83]
	v_mfma_f32_16x16x32_bf16 v[72:75], v[152:155], v[192:195], v[72:75]
	v_mfma_f32_16x16x32_bf16 v[68:71], v[160:163], v[192:195], v[68:71]
	s_barrier
	s_add_i32 s9, s9, s89
	v_lshl_add_u64 v[228:229], v[228:229], 0, s[60:61]
	s_mov_b32 m0, s9
	ds_read_b128 v[164:167], v232 offset:49152
	ds_read_b128 v[168:171], v232 offset:50176
	ds_read_b128 v[172:175], v232 offset:51200
	ds_read_b128 v[176:179], v232 offset:52224
	ds_read_b128 v[180:183], v232 offset:53248
	ds_read_b128 v[184:187], v232 offset:54272
	ds_read_b128 v[188:191], v232 offset:55296
	ds_read_b128 v[192:195], v232 offset:56320
	global_load_lds_dwordx4 v[228:229], off
	v_lshl_add_u64 v[226:227], v[226:227], 0, s[60:61]
	s_add_i32 m0, s9, 0x2000
	v_lshl_add_u64 v[220:221], v[220:221], 0, s[62:63]
	s_add_i32 s9, s12, s89
	global_load_lds_dwordx4 v[226:227], off
	v_lshl_add_u64 v[226:227], v[220:221], 0, v[198:199]
	s_mov_b32 m0, s9
	v_lshl_add_u64 v[220:221], v[220:221], 0, v[202:203]
	global_load_lds_dwordx4 v[226:227], off
	s_add_i32 m0, s9, 0x2000
	s_nop 0
	global_load_lds_dwordx4 v[220:221], off
	v_lshl_add_u64 v[220:221], v[222:223], 0, s[60:61]
	s_mov_b32 m0, s48
	s_nop 0
	global_load_lds_dwordx4 v[220:221], off
	v_lshl_add_u64 v[220:221], v[224:225], 0, s[60:61]
	s_mov_b32 m0, s49
	s_nop 0
	global_load_lds_dwordx4 v[220:221], off
	s_waitcnt vmcnt(8)
	s_waitcnt lgkmcnt(0)
	s_barrier
	v_mfma_f32_16x16x32_bf16 v[62:65], v[132:135], v[164:167], v[62:65]
	v_mfma_f32_16x16x32_bf16 v[58:61], v[140:143], v[164:167], v[58:61]
	v_mfma_f32_16x16x32_bf16 v[50:53], v[132:135], v[172:175], v[50:53]
	v_mfma_f32_16x16x32_bf16 v[42:45], v[140:143], v[172:175], v[42:45]
	v_mfma_f32_16x16x32_bf16 v[34:37], v[132:135], v[180:183], v[34:37]
	v_mfma_f32_16x16x32_bf16 v[26:29], v[140:143], v[180:183], v[26:29]
	v_mfma_f32_16x16x32_bf16 v[18:21], v[132:135], v[188:191], v[18:21]
	v_mfma_f32_16x16x32_bf16 v[10:13], v[140:143], v[188:191], v[10:13]
	v_mfma_f32_16x16x32_bf16 v[62:65], v[136:139], v[168:171], v[62:65]
	v_mfma_f32_16x16x32_bf16 v[58:61], v[144:147], v[168:171], v[58:61]
	v_mfma_f32_16x16x32_bf16 v[50:53], v[136:139], v[176:179], v[50:53]
	v_mfma_f32_16x16x32_bf16 v[42:45], v[144:147], v[176:179], v[42:45]
	v_mfma_f32_16x16x32_bf16 v[34:37], v[136:139], v[184:187], v[34:37]
	v_mfma_f32_16x16x32_bf16 v[26:29], v[144:147], v[184:187], v[26:29]
	v_mfma_f32_16x16x32_bf16 v[18:21], v[136:139], v[192:195], v[18:21]
	v_mfma_f32_16x16x32_bf16 v[10:13], v[144:147], v[192:195], v[10:13]
	v_mfma_f32_16x16x32_bf16 v[54:57], v[148:151], v[164:167], v[54:57]
	v_mfma_f32_16x16x32_bf16 v[46:49], v[156:159], v[164:167], v[46:49]
	v_mfma_f32_16x16x32_bf16 v[38:41], v[148:151], v[172:175], v[38:41]
	v_mfma_f32_16x16x32_bf16 v[30:33], v[156:159], v[172:175], v[30:33]
	v_mfma_f32_16x16x32_bf16 v[22:25], v[148:151], v[180:183], v[22:25]
	v_mfma_f32_16x16x32_bf16 v[14:17], v[156:159], v[180:183], v[14:17]
	v_mfma_f32_16x16x32_bf16 v[6:9], v[148:151], v[188:191], v[6:9]
	v_mfma_f32_16x16x32_bf16 v[2:5], v[156:159], v[188:191], v[2:5]
	v_mfma_f32_16x16x32_bf16 v[54:57], v[152:155], v[168:171], v[54:57]
	v_mfma_f32_16x16x32_bf16 v[46:49], v[160:163], v[168:171], v[46:49]
	v_mfma_f32_16x16x32_bf16 v[38:41], v[152:155], v[176:179], v[38:41]
	v_mfma_f32_16x16x32_bf16 v[30:33], v[160:163], v[176:179], v[30:33]
	v_mfma_f32_16x16x32_bf16 v[22:25], v[152:155], v[184:187], v[22:25]
	v_mfma_f32_16x16x32_bf16 v[14:17], v[160:163], v[184:187], v[14:17]
	v_mfma_f32_16x16x32_bf16 v[6:9], v[152:155], v[192:195], v[6:9]
	v_mfma_f32_16x16x32_bf16 v[2:5], v[160:163], v[192:195], v[2:5]
	s_barrier
	s_add_i32 s8, s8, 2
	s_add_u32 s84, s84, 0x100
	s_addc_u32 s85, s85, 0
	s_cmp_gt_u32 s8, 5
	s_cbranch_scc1 .LBB0_1488

.LBB0_1484:
	s_add_u32 s9, s74, s84
	s_addc_u32 s10, s75, s85
	s_add_u32 s9, s9, 0x100
	s_addc_u32 s10, s10, 0
	s_cmpk_eq_i32 s84, 0x300
	s_waitcnt lgkmcnt(0)
	v_lshl_add_u64 v[220:221], v[218:219], 0, s[84:85]
	s_cselect_b64 vcc, -1, 0
	s_cselect_b32 s37, s71, s10
	s_cselect_b32 s36, s70, s9
	v_cndmask_b32_e32 v221, v221, v213, vcc
	v_cndmask_b32_e32 v220, v220, v212, vcc
	s_barrier
	v_mfma_f32_16x16x32_bf16 v[128:131], v[148:151], v[188:191], v[128:131]
	v_mfma_f32_16x16x32_bf16 v[124:127], v[156:159], v[188:191], v[124:127]
	v_mfma_f32_16x16x32_bf16 v[116:119], v[148:151], v[180:183], v[116:119]
	v_mfma_f32_16x16x32_bf16 v[108:111], v[156:159], v[180:183], v[108:111]
	v_mfma_f32_16x16x32_bf16 v[100:103], v[148:151], v[172:175], v[100:103]
	v_mfma_f32_16x16x32_bf16 v[92:95], v[156:159], v[172:175], v[92:95]
	v_mfma_f32_16x16x32_bf16 v[84:87], v[148:151], v[164:167], v[84:87]
	v_mfma_f32_16x16x32_bf16 v[76:79], v[156:159], v[164:167], v[76:79]
	v_mfma_f32_16x16x32_bf16 v[128:131], v[152:155], v[192:195], v[128:131]
	v_mfma_f32_16x16x32_bf16 v[124:127], v[160:163], v[192:195], v[124:127]
	v_mfma_f32_16x16x32_bf16 v[116:119], v[152:155], v[184:187], v[116:119]
	v_mfma_f32_16x16x32_bf16 v[108:111], v[160:163], v[184:187], v[108:111]
	v_mfma_f32_16x16x32_bf16 v[100:103], v[152:155], v[176:179], v[100:103]
	v_mfma_f32_16x16x32_bf16 v[92:95], v[160:163], v[176:179], v[92:95]
	v_mfma_f32_16x16x32_bf16 v[84:87], v[152:155], v[168:171], v[84:87]
	v_mfma_f32_16x16x32_bf16 v[76:79], v[160:163], v[168:171], v[76:79]
	v_mfma_f32_16x16x32_bf16 v[120:123], v[132:135], v[188:191], v[120:123]
	v_mfma_f32_16x16x32_bf16 v[112:115], v[140:143], v[188:191], v[112:115]
	v_mfma_f32_16x16x32_bf16 v[104:107], v[132:135], v[180:183], v[104:107]
	v_mfma_f32_16x16x32_bf16 v[96:99], v[140:143], v[180:183], v[96:99]
	v_mfma_f32_16x16x32_bf16 v[88:91], v[132:135], v[172:175], v[88:91]
	v_mfma_f32_16x16x32_bf16 v[80:83], v[140:143], v[172:175], v[80:83]
	v_mfma_f32_16x16x32_bf16 v[72:75], v[132:135], v[164:167], v[72:75]
	v_mfma_f32_16x16x32_bf16 v[68:71], v[140:143], v[164:167], v[68:71]
	v_mfma_f32_16x16x32_bf16 v[120:123], v[136:139], v[192:195], v[120:123]
	v_mfma_f32_16x16x32_bf16 v[112:115], v[144:147], v[192:195], v[112:115]
	v_mfma_f32_16x16x32_bf16 v[104:107], v[136:139], v[184:187], v[104:107]
	v_mfma_f32_16x16x32_bf16 v[96:99], v[144:147], v[184:187], v[96:99]
	v_mfma_f32_16x16x32_bf16 v[88:91], v[136:139], v[176:179], v[88:91]
	v_mfma_f32_16x16x32_bf16 v[80:83], v[144:147], v[176:179], v[80:83]
	v_mfma_f32_16x16x32_bf16 v[72:75], v[136:139], v[168:171], v[72:75]
	v_mfma_f32_16x16x32_bf16 v[68:71], v[144:147], v[168:171], v[68:71]
	s_barrier
	s_mov_b32 m0, s93
	v_lshl_add_u64 v[228:229], v[220:221], 0, v[198:199]
	ds_read_b128 v[188:191], v232 offset:16384
	ds_read_b128 v[192:195], v232 offset:17408
	ds_read_b128 v[180:183], v232 offset:18432
	ds_read_b128 v[184:187], v232 offset:19456
	ds_read_b128 v[172:175], v232 offset:20480
	ds_read_b128 v[176:179], v232 offset:21504
	ds_read_b128 v[164:167], v232 offset:22528
	ds_read_b128 v[168:171], v232 offset:23552
	global_load_lds_dwordx4 v[228:229], off
	v_lshl_add_u64 v[226:227], v[220:221], 0, v[202:203]
	s_mov_b32 m0, s94
	v_lshl_add_u64 v[222:223], v[220:221], 0, s[80:81]
	global_load_lds_dwordx4 v[226:227], off
	v_lshl_add_u64 v[224:225], v[222:223], 0, v[198:199]
	s_mov_b32 m0, s95
	v_lshl_add_u64 v[222:223], v[222:223], 0, v[202:203]
	global_load_lds_dwordx4 v[224:225], off
	s_mov_b32 m0, s96
	v_lshl_add_u64 v[224:225], s[36:37], 0, v[200:201]
	global_load_lds_dwordx4 v[222:223], off
	v_lshl_add_u64 v[222:223], s[36:37], 0, v[196:197]
	s_mov_b32 m0, s92
	s_mov_b64 s[26:27], -1
	global_load_lds_dwordx4 v[222:223], off
	s_mov_b32 m0, s97
	s_and_b64 vcc, exec, s[40:41]
	global_load_lds_dwordx4 v[224:225], off
	s_cbranch_vccz .LBB0_1486
	s_waitcnt vmcnt(8)
	s_mov_b64 s[26:27], 0
